# expert indices of the sliced PEER passes come through scalar loads (16 at a time, one batch ahead) instead of a v_readlane per table row
# speedup vs baseline: 1.0255x; 1.0255x over previous
.Lgba_1444:
	s_or_b64 exec, exec, s[2:3]
	s_waitcnt lgkmcnt(0)
	s_barrier
	s_mov_b64 exec, -1
	v_and_b32_e32 v1, 63, v0
	v_readfirstlane_b32 s16, v0
	s_load_dwordx2 s[12:13], s[0:1], 0xc0
	s_lshr_b32 s16, s16, 6
	s_and_b32 s18, s33, 7
	s_lshr_b32 s19, s33, 3
	s_lshl_b32 s19, s19, 8
	s_lshl_b32 s16, s16, 5
	s_add_i32 s16, s16, s19
	s_add_i32 s17, s16, 32
	s_add_i32 s24, s17, -1
	s_lshl_b32 s19, s18, 9
	v_lshl_add_u32 v162, v1, 3, s19
	v_mov_b32_e32 v163, 0
	s_mov_b32 s31, 0
	v_and_b32_e32 v4, 8, v1
	v_cmp_eq_u32_e64 s[8:9], 0, v4
	v_and_b32_e32 v4, 4, v1
	v_cmp_eq_u32_e64 s[10:11], 0, v4
	v_and_b32_e32 v4, 2, v1
	v_cmp_eq_u32_e64 s[14:15], 0, v4
	s_mov_b32 s2, 0x55555555
	s_mov_b32 s3, 0x55555555
	s_load_dwordx2 s[4:5], s[0:1], 0x88
	s_waitcnt lgkmcnt(0)
	v_lshl_add_u64 v[160:161], v[162:163], 2, s[4:5]
	global_load_dwordx4 v[100:103], v[160:161], off
	global_load_dwordx4 v[104:107], v[160:161], off offset:16
	s_lshl_b32 s19, s18, 20
	s_add_u32 s22, s12, 0x25c00000
	s_addc_u32 s23, s13, 0
	s_add_u32 s22, s22, s19
	s_addc_u32 s23, s23, 0
	s_add_u32 s26, s12, 0xfc00000
	s_addc_u32 s27, s13, 0
	s_add_u32 s20, s12, 0x100000
	s_addc_u32 s21, s13, 0
	v_lshl_add_u64 v[172:173], v[162:163], 1, s[20:21]
	s_add_u32 s20, s12, 0x4da00000
	s_addc_u32 s21, s13, 0
	v_mov_b32_e32 v4, v1
	v_mov_b32_e32 v5, 0
	v_lshl_add_u64 v[174:175], v[4:5], 2, s[20:21]
	s_lshl_b32 s19, s18, 22
	s_add_u32 s20, s12, 0x23c00000
	s_addc_u32 s21, s13, 0
	s_add_u32 s20, s20, s19
	s_addc_u32 s21, s21, 0
	v_lshl_add_u64 v[176:177], v[4:5], 1, s[20:21]
	s_lshl_b32 s30, s16, 13
	v_lshl_add_u64 v[160:161], v[172:173], 0, s[30:31]
	global_load_dwordx4 v[116:119], v[160:161], off
	s_lshl_b32 s30, s16, 9
	v_lshl_add_u64 v[160:161], v[174:175], 0, s[30:31]
	global_load_dword v122, v[160:161], off
	global_load_dword v123, v[160:161], off offset:256
	s_waitcnt vmcnt(0)
	s_add_u32 s40, s12, 0x4da00000
	s_addc_u32 s41, s13, 0
	s_lshl_b32 s30, s16, 9
	s_add_u32 s36, s40, s30
	s_addc_u32 s37, s41, 0
	s_load_dwordx16 s[68:83], s[36:37], 0x0
	s_load_dwordx16 s[84:99], s[36:37], 0x40
	s_waitcnt lgkmcnt(0)
	s_lshl_b32 s30, s68, 12
	s_add_u32 s28, s26, s30
	s_addc_u32 s29, s27, 0
	global_load_dwordx2 v[24:25], v162, s[28:29]
	s_lshl_b32 s30, s69, 12
	s_add_u32 s28, s26, s30
	s_addc_u32 s29, s27, 0
	global_load_dwordx2 v[26:27], v162, s[28:29]
	s_lshl_b32 s30, s70, 12
	s_add_u32 s28, s26, s30
	s_addc_u32 s29, s27, 0
	global_load_dwordx2 v[28:29], v162, s[28:29]
	s_lshl_b32 s30, s71, 12
	s_add_u32 s28, s26, s30
	s_addc_u32 s29, s27, 0
	global_load_dwordx2 v[30:31], v162, s[28:29]
	s_lshl_b32 s30, s72, 12
	s_add_u32 s28, s26, s30
	s_addc_u32 s29, s27, 0
	global_load_dwordx2 v[32:33], v162, s[28:29]
	s_lshl_b32 s30, s73, 12
	s_add_u32 s28, s26, s30
	s_addc_u32 s29, s27, 0
	global_load_dwordx2 v[34:35], v162, s[28:29]
	s_lshl_b32 s30, s74, 12
	s_add_u32 s28, s26, s30
	s_addc_u32 s29, s27, 0
	global_load_dwordx2 v[36:37], v162, s[28:29]
	s_lshl_b32 s30, s75, 12
	s_add_u32 s28, s26, s30
	s_addc_u32 s29, s27, 0
	global_load_dwordx2 v[38:39], v162, s[28:29]
	s_lshl_b32 s30, s76, 12
	s_add_u32 s28, s26, s30
	s_addc_u32 s29, s27, 0
	global_load_dwordx2 v[40:41], v162, s[28:29]
	s_lshl_b32 s30, s77, 12
	s_add_u32 s28, s26, s30
	s_addc_u32 s29, s27, 0
	global_load_dwordx2 v[42:43], v162, s[28:29]
	s_lshl_b32 s30, s78, 12
	s_add_u32 s28, s26, s30
	s_addc_u32 s29, s27, 0
	global_load_dwordx2 v[44:45], v162, s[28:29]
	s_lshl_b32 s30, s79, 12
	s_add_u32 s28, s26, s30
	s_addc_u32 s29, s27, 0
	global_load_dwordx2 v[46:47], v162, s[28:29]
	s_lshl_b32 s30, s80, 12
	s_add_u32 s28, s26, s30
	s_addc_u32 s29, s27, 0
	global_load_dwordx2 v[48:49], v162, s[28:29]
	s_lshl_b32 s30, s81, 12
	s_add_u32 s28, s26, s30
	s_addc_u32 s29, s27, 0
	global_load_dwordx2 v[50:51], v162, s[28:29]
	s_lshl_b32 s30, s82, 12
	s_add_u32 s28, s26, s30
	s_addc_u32 s29, s27, 0
	global_load_dwordx2 v[52:53], v162, s[28:29]
	s_lshl_b32 s30, s83, 12
	s_add_u32 s28, s26, s30
	s_addc_u32 s29, s27, 0
	global_load_dwordx2 v[54:55], v162, s[28:29]
	s_lshl_b32 s30, s84, 12
	s_add_u32 s28, s26, s30
	s_addc_u32 s29, s27, 0
	global_load_dwordx2 v[56:57], v162, s[28:29]
	s_lshl_b32 s30, s85, 12
	s_add_u32 s28, s26, s30
	s_addc_u32 s29, s27, 0
	global_load_dwordx2 v[58:59], v162, s[28:29]
	s_lshl_b32 s30, s86, 12
	s_add_u32 s28, s26, s30
	s_addc_u32 s29, s27, 0
	global_load_dwordx2 v[60:61], v162, s[28:29]
	s_lshl_b32 s30, s87, 12
	s_add_u32 s28, s26, s30
	s_addc_u32 s29, s27, 0
	global_load_dwordx2 v[62:63], v162, s[28:29]
	s_lshl_b32 s30, s88, 12
	s_add_u32 s28, s26, s30
	s_addc_u32 s29, s27, 0
	global_load_dwordx2 v[64:65], v162, s[28:29]
	s_lshl_b32 s30, s89, 12
	s_add_u32 s28, s26, s30
	s_addc_u32 s29, s27, 0
	global_load_dwordx2 v[66:67], v162, s[28:29]
	s_lshl_b32 s30, s90, 12
	s_add_u32 s28, s26, s30
	s_addc_u32 s29, s27, 0
	global_load_dwordx2 v[68:69], v162, s[28:29]
	s_lshl_b32 s30, s91, 12
	s_add_u32 s28, s26, s30
	s_addc_u32 s29, s27, 0
	global_load_dwordx2 v[70:71], v162, s[28:29]
	s_lshl_b32 s30, s92, 12
	s_add_u32 s28, s26, s30
	s_addc_u32 s29, s27, 0
	global_load_dwordx2 v[72:73], v162, s[28:29]
	s_lshl_b32 s30, s93, 12
	s_add_u32 s28, s26, s30
	s_addc_u32 s29, s27, 0
	global_load_dwordx2 v[74:75], v162, s[28:29]
	s_lshl_b32 s30, s94, 12
	s_add_u32 s28, s26, s30
	s_addc_u32 s29, s27, 0
	global_load_dwordx2 v[76:77], v162, s[28:29]
	s_lshl_b32 s30, s95, 12
	s_add_u32 s28, s26, s30
	s_addc_u32 s29, s27, 0
	global_load_dwordx2 v[78:79], v162, s[28:29]
	s_lshl_b32 s30, s96, 12
	s_add_u32 s28, s26, s30
	s_addc_u32 s29, s27, 0
	global_load_dwordx2 v[80:81], v162, s[28:29]
	s_lshl_b32 s30, s97, 12
	s_add_u32 s28, s26, s30
	s_addc_u32 s29, s27, 0
	global_load_dwordx2 v[82:83], v162, s[28:29]
	s_lshl_b32 s30, s98, 12
	s_add_u32 s28, s26, s30
	s_addc_u32 s29, s27, 0
	global_load_dwordx2 v[84:85], v162, s[28:29]
	s_lshl_b32 s30, s99, 12
	s_add_u32 s28, s26, s30
	s_addc_u32 s29, s27, 0
	global_load_dwordx2 v[86:87], v162, s[28:29]
	s_load_dwordx16 s[68:83], s[36:37], 0x80
.Lpa_tok:
	v_lshlrev_b32_e32 v124, 16, v116
	v_and_b32_e32 v125, 0xffff0000, v116
	v_pk_mul_f32 v[108:109], v[124:125], v[100:101]
	v_lshlrev_b32_e32 v124, 16, v117
	v_and_b32_e32 v125, 0xffff0000, v117
	v_pk_mul_f32 v[110:111], v[124:125], v[102:103]
	v_lshlrev_b32_e32 v124, 16, v118
	v_and_b32_e32 v125, 0xffff0000, v118
	v_pk_mul_f32 v[112:113], v[124:125], v[104:105]
	v_lshlrev_b32_e32 v124, 16, v119
	v_and_b32_e32 v125, 0xffff0000, v119
	v_pk_mul_f32 v[114:115], v[124:125], v[106:107]
	v_add_f32_e32 v16, v108, v109
	v_add_f32_e32 v17, v110, v111
	v_add_f32_e32 v18, v112, v113
	v_add_f32_e32 v19, v114, v115
	v_add_f32_e32 v16, v16, v17
	v_add_f32_e32 v18, v18, v19
	v_add_f32_e32 v16, v16, v18
	s_nop 1
	v_add_f32_dpp v17, v16, v16 quad_perm:[1,0,3,2] row_mask:0xf bank_mask:0xf
	s_nop 1
	v_add_f32_dpp v16, v17, v17 quad_perm:[2,3,0,1] row_mask:0xf bank_mask:0xf
	s_nop 1
	v_add_f32_dpp v17, v16, v16 row_half_mirror row_mask:0xf bank_mask:0xf
	s_nop 1
	v_add_f32_dpp v16, v17, v17 row_ror:8 row_mask:0xf bank_mask:0xf
	v_mov_b32_e32 v17, v16
	s_nop 1
	v_permlane16_swap_b32_e32 v16, v17
	v_add_f32_e32 v16, v16, v17
	v_mov_b32_e32 v17, v16
	s_nop 1
	v_permlane32_swap_b32_e32 v16, v17
	v_add_f32_e32 v16, v16, v17
	s_lshl_b32 s30, s16, 7
	s_add_u32 s28, s22, s30
	s_addc_u32 s29, s23, 0
	v_lshlrev_b32_e32 v19, 1, v1
	s_mov_b64 exec, s[2:3]
	global_store_dword v19, v16, s[28:29]
	s_mov_b64 exec, -1
	v_mov_b32_e32 v120, v122
	v_mov_b32_e32 v121, v123
	s_lshl_b32 s30, s16, 9
	v_lshl_add_u64 v[22:23], v[176:177], 0, s[30:31]
	s_add_i32 s18, s16, 1
	s_min_i32 s18, s18, s24
	s_lshl_b32 s30, s16, 9
	s_add_u32 s36, s40, s30
	s_addc_u32 s37, s41, 0
	s_lshl_b32 s30, s18, 9
	s_add_u32 s38, s40, s30
	s_addc_u32 s39, s41, 0
	s_lshl_b32 s30, s18, 13
	v_lshl_add_u64 v[160:161], v[172:173], 0, s[30:31]
	global_load_dwordx4 v[116:119], v[160:161], off
	s_lshl_b32 s30, s18, 9
	v_lshl_add_u64 v[160:161], v[174:175], 0, s[30:31]
	global_load_dword v122, v[160:161], off
	global_load_dword v123, v[160:161], off offset:256
	s_waitcnt vmcnt(34)
	v_cvt_f32_ubyte0_e32 v124, v24
	v_cvt_f32_ubyte1_e32 v126, v24
	v_cvt_f32_ubyte2_e32 v128, v24
	v_cvt_f32_ubyte3_e32 v130, v24
	v_cvt_f32_ubyte0_e32 v132, v25
	v_cvt_f32_ubyte1_e32 v134, v25
	v_cvt_f32_ubyte2_e32 v136, v25
	v_cvt_f32_ubyte3_e32 v138, v25
	s_waitcnt lgkmcnt(0)
	s_load_dwordx16 s[84:99], s[36:37], 0xc0
	s_lshl_b32 s30, s68, 12
	s_add_u32 s28, s26, s30
	s_addc_u32 s29, s27, 0
	global_load_dwordx2 v[24:25], v162, s[28:29]
	s_waitcnt vmcnt(34)
	v_cvt_f32_ubyte0_e32 v125, v26
	v_cvt_f32_ubyte1_e32 v127, v26
	v_cvt_f32_ubyte2_e32 v129, v26
	v_cvt_f32_ubyte3_e32 v131, v26
	v_cvt_f32_ubyte0_e32 v133, v27
	v_cvt_f32_ubyte1_e32 v135, v27
	v_cvt_f32_ubyte2_e32 v137, v27
	v_cvt_f32_ubyte3_e32 v139, v27
	s_lshl_b32 s30, s69, 12
	s_add_u32 s28, s26, s30
	s_addc_u32 s29, s27, 0
	global_load_dwordx2 v[26:27], v162, s[28:29]
	s_waitcnt vmcnt(34)
	v_cvt_f32_ubyte0_e32 v140, v28
	v_cvt_f32_ubyte1_e32 v142, v28
	v_cvt_f32_ubyte2_e32 v144, v28
	v_cvt_f32_ubyte3_e32 v146, v28
	v_cvt_f32_ubyte0_e32 v148, v29
	v_cvt_f32_ubyte1_e32 v150, v29
	v_cvt_f32_ubyte2_e32 v152, v29
	v_cvt_f32_ubyte3_e32 v154, v29
	s_lshl_b32 s30, s70, 12
	s_add_u32 s28, s26, s30
	s_addc_u32 s29, s27, 0
	global_load_dwordx2 v[28:29], v162, s[28:29]
	s_waitcnt vmcnt(34)
	v_cvt_f32_ubyte0_e32 v141, v30
	v_cvt_f32_ubyte1_e32 v143, v30
	v_cvt_f32_ubyte2_e32 v145, v30
	v_cvt_f32_ubyte3_e32 v147, v30
	v_cvt_f32_ubyte0_e32 v149, v31
	v_cvt_f32_ubyte1_e32 v151, v31
	v_cvt_f32_ubyte2_e32 v153, v31
	v_cvt_f32_ubyte3_e32 v155, v31
	s_lshl_b32 s30, s71, 12
	s_add_u32 s28, s26, s30
	s_addc_u32 s29, s27, 0
	global_load_dwordx2 v[30:31], v162, s[28:29]
	v_mul_f32_e32 v178, v124, v108
	v_mul_f32_e32 v179, v125, v108
	v_mul_f32_e32 v180, v140, v108
	v_mul_f32_e32 v181, v141, v108
	v_fmac_f32_e32 v178, v126, v109
	v_fmac_f32_e32 v179, v127, v109
	v_fmac_f32_e32 v180, v142, v109
	v_fmac_f32_e32 v181, v143, v109
	v_fmac_f32_e32 v178, v128, v110
	v_fmac_f32_e32 v179, v129, v110
	v_fmac_f32_e32 v180, v144, v110
	v_fmac_f32_e32 v181, v145, v110
	v_fmac_f32_e32 v178, v130, v111
	v_fmac_f32_e32 v179, v131, v111
	v_fmac_f32_e32 v180, v146, v111
	v_fmac_f32_e32 v181, v147, v111
	v_fmac_f32_e32 v178, v132, v112
	v_fmac_f32_e32 v179, v133, v112
	v_fmac_f32_e32 v180, v148, v112
	v_fmac_f32_e32 v181, v149, v112
	v_fmac_f32_e32 v178, v134, v113
	v_fmac_f32_e32 v179, v135, v113
	v_fmac_f32_e32 v180, v150, v113
	v_fmac_f32_e32 v181, v151, v113
	v_fmac_f32_e32 v178, v136, v114
	v_fmac_f32_e32 v179, v137, v114
	v_fmac_f32_e32 v180, v152, v114
	v_fmac_f32_e32 v181, v153, v114
	v_fmac_f32_e32 v178, v138, v115
	v_fmac_f32_e32 v179, v139, v115
	v_fmac_f32_e32 v180, v154, v115
	v_fmac_f32_e32 v181, v155, v115
	s_waitcnt vmcnt(34)
	v_cvt_f32_ubyte0_e32 v124, v32
	v_cvt_f32_ubyte1_e32 v126, v32
	v_cvt_f32_ubyte2_e32 v128, v32
	v_cvt_f32_ubyte3_e32 v130, v32
	v_cvt_f32_ubyte0_e32 v132, v33
	v_cvt_f32_ubyte1_e32 v134, v33
	v_cvt_f32_ubyte2_e32 v136, v33
	v_cvt_f32_ubyte3_e32 v138, v33
	s_lshl_b32 s30, s72, 12
	s_add_u32 s28, s26, s30
	s_addc_u32 s29, s27, 0
	global_load_dwordx2 v[32:33], v162, s[28:29]
	s_waitcnt vmcnt(34)
	v_cvt_f32_ubyte0_e32 v125, v34
	v_cvt_f32_ubyte1_e32 v127, v34
	v_cvt_f32_ubyte2_e32 v129, v34
	v_cvt_f32_ubyte3_e32 v131, v34
	v_cvt_f32_ubyte0_e32 v133, v35
	v_cvt_f32_ubyte1_e32 v135, v35
	v_cvt_f32_ubyte2_e32 v137, v35
	v_cvt_f32_ubyte3_e32 v139, v35
	s_lshl_b32 s30, s73, 12
	s_add_u32 s28, s26, s30
	s_addc_u32 s29, s27, 0
	global_load_dwordx2 v[34:35], v162, s[28:29]
	s_waitcnt vmcnt(34)
	v_cvt_f32_ubyte0_e32 v140, v36
	v_cvt_f32_ubyte1_e32 v142, v36
	v_cvt_f32_ubyte2_e32 v144, v36
	v_cvt_f32_ubyte3_e32 v146, v36
	v_cvt_f32_ubyte0_e32 v148, v37
	v_cvt_f32_ubyte1_e32 v150, v37
	v_cvt_f32_ubyte2_e32 v152, v37
	v_cvt_f32_ubyte3_e32 v154, v37
	s_lshl_b32 s30, s74, 12
	s_add_u32 s28, s26, s30
	s_addc_u32 s29, s27, 0
	global_load_dwordx2 v[36:37], v162, s[28:29]
	s_waitcnt vmcnt(34)
	v_cvt_f32_ubyte0_e32 v141, v38
	v_cvt_f32_ubyte1_e32 v143, v38
	v_cvt_f32_ubyte2_e32 v145, v38
	v_cvt_f32_ubyte3_e32 v147, v38
	v_cvt_f32_ubyte0_e32 v149, v39
	v_cvt_f32_ubyte1_e32 v151, v39
	v_cvt_f32_ubyte2_e32 v153, v39
	v_cvt_f32_ubyte3_e32 v155, v39
	s_lshl_b32 s30, s75, 12
	s_add_u32 s28, s26, s30
	s_addc_u32 s29, s27, 0
	global_load_dwordx2 v[38:39], v162, s[28:29]
	v_mul_f32_e32 v182, v124, v108
	v_mul_f32_e32 v183, v125, v108
	v_mul_f32_e32 v184, v140, v108
	v_mul_f32_e32 v185, v141, v108
	v_fmac_f32_e32 v182, v126, v109
	v_fmac_f32_e32 v183, v127, v109
	v_fmac_f32_e32 v184, v142, v109
	v_fmac_f32_e32 v185, v143, v109
	v_fmac_f32_e32 v182, v128, v110
	v_fmac_f32_e32 v183, v129, v110
	v_fmac_f32_e32 v184, v144, v110
	v_fmac_f32_e32 v185, v145, v110
	v_fmac_f32_e32 v182, v130, v111
	v_fmac_f32_e32 v183, v131, v111
	v_fmac_f32_e32 v184, v146, v111
	v_fmac_f32_e32 v185, v147, v111
	v_fmac_f32_e32 v182, v132, v112
	v_fmac_f32_e32 v183, v133, v112
	v_fmac_f32_e32 v184, v148, v112
	v_fmac_f32_e32 v185, v149, v112
	v_fmac_f32_e32 v182, v134, v113
	v_fmac_f32_e32 v183, v135, v113
	v_fmac_f32_e32 v184, v150, v113
	v_fmac_f32_e32 v185, v151, v113
	v_fmac_f32_e32 v182, v136, v114
	v_fmac_f32_e32 v183, v137, v114
	v_fmac_f32_e32 v184, v152, v114
	v_fmac_f32_e32 v185, v153, v114
	v_fmac_f32_e32 v182, v138, v115
	v_fmac_f32_e32 v183, v139, v115
	v_fmac_f32_e32 v184, v154, v115
	v_fmac_f32_e32 v185, v155, v115
	s_waitcnt vmcnt(34)
	v_cvt_f32_ubyte0_e32 v124, v40
	v_cvt_f32_ubyte1_e32 v126, v40
	v_cvt_f32_ubyte2_e32 v128, v40
	v_cvt_f32_ubyte3_e32 v130, v40
	v_cvt_f32_ubyte0_e32 v132, v41
	v_cvt_f32_ubyte1_e32 v134, v41
	v_cvt_f32_ubyte2_e32 v136, v41
	v_cvt_f32_ubyte3_e32 v138, v41
	s_lshl_b32 s30, s76, 12
	s_add_u32 s28, s26, s30
	s_addc_u32 s29, s27, 0
	global_load_dwordx2 v[40:41], v162, s[28:29]
	s_waitcnt vmcnt(34)
	v_cvt_f32_ubyte0_e32 v125, v42
	v_cvt_f32_ubyte1_e32 v127, v42
	v_cvt_f32_ubyte2_e32 v129, v42
	v_cvt_f32_ubyte3_e32 v131, v42
	v_cvt_f32_ubyte0_e32 v133, v43
	v_cvt_f32_ubyte1_e32 v135, v43
	v_cvt_f32_ubyte2_e32 v137, v43
	v_cvt_f32_ubyte3_e32 v139, v43
	s_lshl_b32 s30, s77, 12
	s_add_u32 s28, s26, s30
	s_addc_u32 s29, s27, 0
	global_load_dwordx2 v[42:43], v162, s[28:29]
	s_waitcnt vmcnt(34)
	v_cvt_f32_ubyte0_e32 v140, v44
	v_cvt_f32_ubyte1_e32 v142, v44
	v_cvt_f32_ubyte2_e32 v144, v44
	v_cvt_f32_ubyte3_e32 v146, v44
	v_cvt_f32_ubyte0_e32 v148, v45
	v_cvt_f32_ubyte1_e32 v150, v45
	v_cvt_f32_ubyte2_e32 v152, v45
	v_cvt_f32_ubyte3_e32 v154, v45
	s_lshl_b32 s30, s78, 12
	s_add_u32 s28, s26, s30
	s_addc_u32 s29, s27, 0
	global_load_dwordx2 v[44:45], v162, s[28:29]
	s_waitcnt vmcnt(34)
	v_cvt_f32_ubyte0_e32 v141, v46
	v_cvt_f32_ubyte1_e32 v143, v46
	v_cvt_f32_ubyte2_e32 v145, v46
	v_cvt_f32_ubyte3_e32 v147, v46
	v_cvt_f32_ubyte0_e32 v149, v47
	v_cvt_f32_ubyte1_e32 v151, v47
	v_cvt_f32_ubyte2_e32 v153, v47
	v_cvt_f32_ubyte3_e32 v155, v47
	s_lshl_b32 s30, s79, 12
	s_add_u32 s28, s26, s30
	s_addc_u32 s29, s27, 0
	global_load_dwordx2 v[46:47], v162, s[28:29]
	v_mul_f32_e32 v186, v124, v108
	v_mul_f32_e32 v187, v125, v108
	v_mul_f32_e32 v188, v140, v108
	v_mul_f32_e32 v189, v141, v108
	v_fmac_f32_e32 v186, v126, v109
	v_fmac_f32_e32 v187, v127, v109
	v_fmac_f32_e32 v188, v142, v109
	v_fmac_f32_e32 v189, v143, v109
	v_fmac_f32_e32 v186, v128, v110
	v_fmac_f32_e32 v187, v129, v110
	v_fmac_f32_e32 v188, v144, v110
	v_fmac_f32_e32 v189, v145, v110
	v_fmac_f32_e32 v186, v130, v111
	v_fmac_f32_e32 v187, v131, v111
	v_fmac_f32_e32 v188, v146, v111
	v_fmac_f32_e32 v189, v147, v111
	v_fmac_f32_e32 v186, v132, v112
	v_fmac_f32_e32 v187, v133, v112
	v_fmac_f32_e32 v188, v148, v112
	v_fmac_f32_e32 v189, v149, v112
	v_fmac_f32_e32 v186, v134, v113
	v_fmac_f32_e32 v187, v135, v113
	v_fmac_f32_e32 v188, v150, v113
	v_fmac_f32_e32 v189, v151, v113
	v_fmac_f32_e32 v186, v136, v114
	v_fmac_f32_e32 v187, v137, v114
	v_fmac_f32_e32 v188, v152, v114
	v_fmac_f32_e32 v189, v153, v114
	v_fmac_f32_e32 v186, v138, v115
	v_fmac_f32_e32 v187, v139, v115
	v_fmac_f32_e32 v188, v154, v115
	v_fmac_f32_e32 v189, v155, v115
	s_waitcnt vmcnt(34)
	v_cvt_f32_ubyte0_e32 v124, v48
	v_cvt_f32_ubyte1_e32 v126, v48
	v_cvt_f32_ubyte2_e32 v128, v48
	v_cvt_f32_ubyte3_e32 v130, v48
	v_cvt_f32_ubyte0_e32 v132, v49
	v_cvt_f32_ubyte1_e32 v134, v49
	v_cvt_f32_ubyte2_e32 v136, v49
	v_cvt_f32_ubyte3_e32 v138, v49
	s_lshl_b32 s30, s80, 12
	s_add_u32 s28, s26, s30
	s_addc_u32 s29, s27, 0
	global_load_dwordx2 v[48:49], v162, s[28:29]
	s_waitcnt vmcnt(34)
	v_cvt_f32_ubyte0_e32 v125, v50
	v_cvt_f32_ubyte1_e32 v127, v50
	v_cvt_f32_ubyte2_e32 v129, v50
	v_cvt_f32_ubyte3_e32 v131, v50
	v_cvt_f32_ubyte0_e32 v133, v51
	v_cvt_f32_ubyte1_e32 v135, v51
	v_cvt_f32_ubyte2_e32 v137, v51
	v_cvt_f32_ubyte3_e32 v139, v51
	s_lshl_b32 s30, s81, 12
	s_add_u32 s28, s26, s30
	s_addc_u32 s29, s27, 0
	global_load_dwordx2 v[50:51], v162, s[28:29]
	s_waitcnt vmcnt(34)
	v_cvt_f32_ubyte0_e32 v140, v52
	v_cvt_f32_ubyte1_e32 v142, v52
	v_cvt_f32_ubyte2_e32 v144, v52
	v_cvt_f32_ubyte3_e32 v146, v52
	v_cvt_f32_ubyte0_e32 v148, v53
	v_cvt_f32_ubyte1_e32 v150, v53
	v_cvt_f32_ubyte2_e32 v152, v53
	v_cvt_f32_ubyte3_e32 v154, v53
	s_lshl_b32 s30, s82, 12
	s_add_u32 s28, s26, s30
	s_addc_u32 s29, s27, 0
	global_load_dwordx2 v[52:53], v162, s[28:29]
	s_waitcnt vmcnt(34)
	v_cvt_f32_ubyte0_e32 v141, v54
	v_cvt_f32_ubyte1_e32 v143, v54
	v_cvt_f32_ubyte2_e32 v145, v54
	v_cvt_f32_ubyte3_e32 v147, v54
	v_cvt_f32_ubyte0_e32 v149, v55
	v_cvt_f32_ubyte1_e32 v151, v55
	v_cvt_f32_ubyte2_e32 v153, v55
	v_cvt_f32_ubyte3_e32 v155, v55
	s_lshl_b32 s30, s83, 12
	s_add_u32 s28, s26, s30
	s_addc_u32 s29, s27, 0
	global_load_dwordx2 v[54:55], v162, s[28:29]
	v_mul_f32_e32 v190, v124, v108
	v_mul_f32_e32 v191, v125, v108
	v_mul_f32_e32 v192, v140, v108
	v_mul_f32_e32 v193, v141, v108
	v_fmac_f32_e32 v190, v126, v109
	v_fmac_f32_e32 v191, v127, v109
	v_fmac_f32_e32 v192, v142, v109
	v_fmac_f32_e32 v193, v143, v109
	v_fmac_f32_e32 v190, v128, v110
	v_fmac_f32_e32 v191, v129, v110
	v_fmac_f32_e32 v192, v144, v110
	v_fmac_f32_e32 v193, v145, v110
	v_fmac_f32_e32 v190, v130, v111
	v_fmac_f32_e32 v191, v131, v111
	v_fmac_f32_e32 v192, v146, v111
	v_fmac_f32_e32 v193, v147, v111
	v_fmac_f32_e32 v190, v132, v112
	v_fmac_f32_e32 v191, v133, v112
	v_fmac_f32_e32 v192, v148, v112
	v_fmac_f32_e32 v193, v149, v112
	v_fmac_f32_e32 v190, v134, v113
	v_fmac_f32_e32 v191, v135, v113
	v_fmac_f32_e32 v192, v150, v113
	v_fmac_f32_e32 v193, v151, v113
	v_fmac_f32_e32 v190, v136, v114
	v_fmac_f32_e32 v191, v137, v114
	v_fmac_f32_e32 v192, v152, v114
	v_fmac_f32_e32 v193, v153, v114
	v_fmac_f32_e32 v190, v138, v115
	v_fmac_f32_e32 v191, v139, v115
	v_fmac_f32_e32 v192, v154, v115
	v_fmac_f32_e32 v193, v155, v115
	s_waitcnt vmcnt(34)
	v_cvt_f32_ubyte0_e32 v124, v56
	v_cvt_f32_ubyte1_e32 v126, v56
	v_cvt_f32_ubyte2_e32 v128, v56
	v_cvt_f32_ubyte3_e32 v130, v56
	v_cvt_f32_ubyte0_e32 v132, v57
	v_cvt_f32_ubyte1_e32 v134, v57
	v_cvt_f32_ubyte2_e32 v136, v57
	v_cvt_f32_ubyte3_e32 v138, v57
	s_waitcnt lgkmcnt(0)
	s_load_dwordx16 s[68:83], s[36:37], 0x100
	s_lshl_b32 s30, s84, 12
	s_add_u32 s28, s26, s30
	s_addc_u32 s29, s27, 0
	global_load_dwordx2 v[56:57], v162, s[28:29]
	s_waitcnt vmcnt(34)
	v_cvt_f32_ubyte0_e32 v125, v58
	v_cvt_f32_ubyte1_e32 v127, v58
	v_cvt_f32_ubyte2_e32 v129, v58
	v_cvt_f32_ubyte3_e32 v131, v58
	v_cvt_f32_ubyte0_e32 v133, v59
	v_cvt_f32_ubyte1_e32 v135, v59
	v_cvt_f32_ubyte2_e32 v137, v59
	v_cvt_f32_ubyte3_e32 v139, v59
	s_lshl_b32 s30, s85, 12
	s_add_u32 s28, s26, s30
	s_addc_u32 s29, s27, 0
	global_load_dwordx2 v[58:59], v162, s[28:29]
	s_waitcnt vmcnt(34)
	v_cvt_f32_ubyte0_e32 v140, v60
	v_cvt_f32_ubyte1_e32 v142, v60
	v_cvt_f32_ubyte2_e32 v144, v60
	v_cvt_f32_ubyte3_e32 v146, v60
	v_cvt_f32_ubyte0_e32 v148, v61
	v_cvt_f32_ubyte1_e32 v150, v61
	v_cvt_f32_ubyte2_e32 v152, v61
	v_cvt_f32_ubyte3_e32 v154, v61
	s_lshl_b32 s30, s86, 12
	s_add_u32 s28, s26, s30
	s_addc_u32 s29, s27, 0
	global_load_dwordx2 v[60:61], v162, s[28:29]
	s_waitcnt vmcnt(34)
	v_cvt_f32_ubyte0_e32 v141, v62
	v_cvt_f32_ubyte1_e32 v143, v62
	v_cvt_f32_ubyte2_e32 v145, v62
	v_cvt_f32_ubyte3_e32 v147, v62
	v_cvt_f32_ubyte0_e32 v149, v63
	v_cvt_f32_ubyte1_e32 v151, v63
	v_cvt_f32_ubyte2_e32 v153, v63
	v_cvt_f32_ubyte3_e32 v155, v63
	s_lshl_b32 s30, s87, 12
	s_add_u32 s28, s26, s30
	s_addc_u32 s29, s27, 0
	global_load_dwordx2 v[62:63], v162, s[28:29]
	v_mul_f32_e32 v194, v124, v108
	v_mul_f32_e32 v195, v125, v108
	v_mul_f32_e32 v196, v140, v108
	v_mul_f32_e32 v197, v141, v108
	v_fmac_f32_e32 v194, v126, v109
	v_fmac_f32_e32 v195, v127, v109
	v_fmac_f32_e32 v196, v142, v109
	v_fmac_f32_e32 v197, v143, v109
	v_fmac_f32_e32 v194, v128, v110
	v_fmac_f32_e32 v195, v129, v110
	v_fmac_f32_e32 v196, v144, v110
	v_fmac_f32_e32 v197, v145, v110
	v_fmac_f32_e32 v194, v130, v111
	v_fmac_f32_e32 v195, v131, v111
	v_fmac_f32_e32 v196, v146, v111
	v_fmac_f32_e32 v197, v147, v111
	v_fmac_f32_e32 v194, v132, v112
	v_fmac_f32_e32 v195, v133, v112
	v_fmac_f32_e32 v196, v148, v112
	v_fmac_f32_e32 v197, v149, v112
	v_fmac_f32_e32 v194, v134, v113
	v_fmac_f32_e32 v195, v135, v113
	v_fmac_f32_e32 v196, v150, v113
	v_fmac_f32_e32 v197, v151, v113
	v_fmac_f32_e32 v194, v136, v114
	v_fmac_f32_e32 v195, v137, v114
	v_fmac_f32_e32 v196, v152, v114
	v_fmac_f32_e32 v197, v153, v114
	v_fmac_f32_e32 v194, v138, v115
	v_fmac_f32_e32 v195, v139, v115
	v_fmac_f32_e32 v196, v154, v115
	v_fmac_f32_e32 v197, v155, v115
	s_waitcnt vmcnt(34)
	v_cvt_f32_ubyte0_e32 v124, v64
	v_cvt_f32_ubyte1_e32 v126, v64
	v_cvt_f32_ubyte2_e32 v128, v64
	v_cvt_f32_ubyte3_e32 v130, v64
	v_cvt_f32_ubyte0_e32 v132, v65
	v_cvt_f32_ubyte1_e32 v134, v65
	v_cvt_f32_ubyte2_e32 v136, v65
	v_cvt_f32_ubyte3_e32 v138, v65
	s_lshl_b32 s30, s88, 12
	s_add_u32 s28, s26, s30
	s_addc_u32 s29, s27, 0
	global_load_dwordx2 v[64:65], v162, s[28:29]
	s_waitcnt vmcnt(34)
	v_cvt_f32_ubyte0_e32 v125, v66
	v_cvt_f32_ubyte1_e32 v127, v66
	v_cvt_f32_ubyte2_e32 v129, v66
	v_cvt_f32_ubyte3_e32 v131, v66
	v_cvt_f32_ubyte0_e32 v133, v67
	v_cvt_f32_ubyte1_e32 v135, v67
	v_cvt_f32_ubyte2_e32 v137, v67
	v_cvt_f32_ubyte3_e32 v139, v67
	s_lshl_b32 s30, s89, 12
	s_add_u32 s28, s26, s30
	s_addc_u32 s29, s27, 0
	global_load_dwordx2 v[66:67], v162, s[28:29]
	s_waitcnt vmcnt(34)
	v_cvt_f32_ubyte0_e32 v140, v68
	v_cvt_f32_ubyte1_e32 v142, v68
	v_cvt_f32_ubyte2_e32 v144, v68
	v_cvt_f32_ubyte3_e32 v146, v68
	v_cvt_f32_ubyte0_e32 v148, v69
	v_cvt_f32_ubyte1_e32 v150, v69
	v_cvt_f32_ubyte2_e32 v152, v69
	v_cvt_f32_ubyte3_e32 v154, v69
	s_lshl_b32 s30, s90, 12
	s_add_u32 s28, s26, s30
	s_addc_u32 s29, s27, 0
	global_load_dwordx2 v[68:69], v162, s[28:29]
	s_waitcnt vmcnt(34)
	v_cvt_f32_ubyte0_e32 v141, v70
	v_cvt_f32_ubyte1_e32 v143, v70
	v_cvt_f32_ubyte2_e32 v145, v70
	v_cvt_f32_ubyte3_e32 v147, v70
	v_cvt_f32_ubyte0_e32 v149, v71
	v_cvt_f32_ubyte1_e32 v151, v71
	v_cvt_f32_ubyte2_e32 v153, v71
	v_cvt_f32_ubyte3_e32 v155, v71
	s_lshl_b32 s30, s91, 12
	s_add_u32 s28, s26, s30
	s_addc_u32 s29, s27, 0
	global_load_dwordx2 v[70:71], v162, s[28:29]
	v_mul_f32_e32 v198, v124, v108
	v_mul_f32_e32 v199, v125, v108
	v_mul_f32_e32 v200, v140, v108
	v_mul_f32_e32 v201, v141, v108
	v_fmac_f32_e32 v198, v126, v109
	v_fmac_f32_e32 v199, v127, v109
	v_fmac_f32_e32 v200, v142, v109
	v_fmac_f32_e32 v201, v143, v109
	v_fmac_f32_e32 v198, v128, v110
	v_fmac_f32_e32 v199, v129, v110
	v_fmac_f32_e32 v200, v144, v110
	v_fmac_f32_e32 v201, v145, v110
	v_fmac_f32_e32 v198, v130, v111
	v_fmac_f32_e32 v199, v131, v111
	v_fmac_f32_e32 v200, v146, v111
	v_fmac_f32_e32 v201, v147, v111
	v_fmac_f32_e32 v198, v132, v112
	v_fmac_f32_e32 v199, v133, v112
	v_fmac_f32_e32 v200, v148, v112
	v_fmac_f32_e32 v201, v149, v112
	v_fmac_f32_e32 v198, v134, v113
	v_fmac_f32_e32 v199, v135, v113
	v_fmac_f32_e32 v200, v150, v113
	v_fmac_f32_e32 v201, v151, v113
	v_fmac_f32_e32 v198, v136, v114
	v_fmac_f32_e32 v199, v137, v114
	v_fmac_f32_e32 v200, v152, v114
	v_fmac_f32_e32 v201, v153, v114
	v_fmac_f32_e32 v198, v138, v115
	v_fmac_f32_e32 v199, v139, v115
	v_fmac_f32_e32 v200, v154, v115
	v_fmac_f32_e32 v201, v155, v115
	s_waitcnt vmcnt(34)
	v_cvt_f32_ubyte0_e32 v124, v72
	v_cvt_f32_ubyte1_e32 v126, v72
	v_cvt_f32_ubyte2_e32 v128, v72
	v_cvt_f32_ubyte3_e32 v130, v72
	v_cvt_f32_ubyte0_e32 v132, v73
	v_cvt_f32_ubyte1_e32 v134, v73
	v_cvt_f32_ubyte2_e32 v136, v73
	v_cvt_f32_ubyte3_e32 v138, v73
	s_lshl_b32 s30, s92, 12
	s_add_u32 s28, s26, s30
	s_addc_u32 s29, s27, 0
	global_load_dwordx2 v[72:73], v162, s[28:29]
	s_waitcnt vmcnt(34)
	v_cvt_f32_ubyte0_e32 v125, v74
	v_cvt_f32_ubyte1_e32 v127, v74
	v_cvt_f32_ubyte2_e32 v129, v74
	v_cvt_f32_ubyte3_e32 v131, v74
	v_cvt_f32_ubyte0_e32 v133, v75
	v_cvt_f32_ubyte1_e32 v135, v75
	v_cvt_f32_ubyte2_e32 v137, v75
	v_cvt_f32_ubyte3_e32 v139, v75
	s_lshl_b32 s30, s93, 12
	s_add_u32 s28, s26, s30
	s_addc_u32 s29, s27, 0
	global_load_dwordx2 v[74:75], v162, s[28:29]
	s_waitcnt vmcnt(34)
	v_cvt_f32_ubyte0_e32 v140, v76
	v_cvt_f32_ubyte1_e32 v142, v76
	v_cvt_f32_ubyte2_e32 v144, v76
	v_cvt_f32_ubyte3_e32 v146, v76
	v_cvt_f32_ubyte0_e32 v148, v77
	v_cvt_f32_ubyte1_e32 v150, v77
	v_cvt_f32_ubyte2_e32 v152, v77
	v_cvt_f32_ubyte3_e32 v154, v77
	s_lshl_b32 s30, s94, 12
	s_add_u32 s28, s26, s30
	s_addc_u32 s29, s27, 0
	global_load_dwordx2 v[76:77], v162, s[28:29]
	s_waitcnt vmcnt(34)
	v_cvt_f32_ubyte0_e32 v141, v78
	v_cvt_f32_ubyte1_e32 v143, v78
	v_cvt_f32_ubyte2_e32 v145, v78
	v_cvt_f32_ubyte3_e32 v147, v78
	v_cvt_f32_ubyte0_e32 v149, v79
	v_cvt_f32_ubyte1_e32 v151, v79
	v_cvt_f32_ubyte2_e32 v153, v79
	v_cvt_f32_ubyte3_e32 v155, v79
	s_lshl_b32 s30, s95, 12
	s_add_u32 s28, s26, s30
	s_addc_u32 s29, s27, 0
	global_load_dwordx2 v[78:79], v162, s[28:29]
	v_mul_f32_e32 v202, v124, v108
	v_mul_f32_e32 v203, v125, v108
	v_mul_f32_e32 v204, v140, v108
	v_mul_f32_e32 v205, v141, v108
	v_fmac_f32_e32 v202, v126, v109
	v_fmac_f32_e32 v203, v127, v109
	v_fmac_f32_e32 v204, v142, v109
	v_fmac_f32_e32 v205, v143, v109
	v_fmac_f32_e32 v202, v128, v110
	v_fmac_f32_e32 v203, v129, v110
	v_fmac_f32_e32 v204, v144, v110
	v_fmac_f32_e32 v205, v145, v110
	v_fmac_f32_e32 v202, v130, v111
	v_fmac_f32_e32 v203, v131, v111
	v_fmac_f32_e32 v204, v146, v111
	v_fmac_f32_e32 v205, v147, v111
	v_fmac_f32_e32 v202, v132, v112
	v_fmac_f32_e32 v203, v133, v112
	v_fmac_f32_e32 v204, v148, v112
	v_fmac_f32_e32 v205, v149, v112
	v_fmac_f32_e32 v202, v134, v113
	v_fmac_f32_e32 v203, v135, v113
	v_fmac_f32_e32 v204, v150, v113
	v_fmac_f32_e32 v205, v151, v113
	v_fmac_f32_e32 v202, v136, v114
	v_fmac_f32_e32 v203, v137, v114
	v_fmac_f32_e32 v204, v152, v114
	v_fmac_f32_e32 v205, v153, v114
	v_fmac_f32_e32 v202, v138, v115
	v_fmac_f32_e32 v203, v139, v115
	v_fmac_f32_e32 v204, v154, v115
	v_fmac_f32_e32 v205, v155, v115
	s_waitcnt vmcnt(34)
	v_cvt_f32_ubyte0_e32 v124, v80
	v_cvt_f32_ubyte1_e32 v126, v80
	v_cvt_f32_ubyte2_e32 v128, v80
	v_cvt_f32_ubyte3_e32 v130, v80
	v_cvt_f32_ubyte0_e32 v132, v81
	v_cvt_f32_ubyte1_e32 v134, v81
	v_cvt_f32_ubyte2_e32 v136, v81
	v_cvt_f32_ubyte3_e32 v138, v81
	s_lshl_b32 s30, s96, 12
	s_add_u32 s28, s26, s30
	s_addc_u32 s29, s27, 0
	global_load_dwordx2 v[80:81], v162, s[28:29]
	s_waitcnt vmcnt(34)
	v_cvt_f32_ubyte0_e32 v125, v82
	v_cvt_f32_ubyte1_e32 v127, v82
	v_cvt_f32_ubyte2_e32 v129, v82
	v_cvt_f32_ubyte3_e32 v131, v82
	v_cvt_f32_ubyte0_e32 v133, v83
	v_cvt_f32_ubyte1_e32 v135, v83
	v_cvt_f32_ubyte2_e32 v137, v83
	v_cvt_f32_ubyte3_e32 v139, v83
	s_lshl_b32 s30, s97, 12
	s_add_u32 s28, s26, s30
	s_addc_u32 s29, s27, 0
	global_load_dwordx2 v[82:83], v162, s[28:29]
	s_waitcnt vmcnt(34)
	v_cvt_f32_ubyte0_e32 v140, v84
	v_cvt_f32_ubyte1_e32 v142, v84
	v_cvt_f32_ubyte2_e32 v144, v84
	v_cvt_f32_ubyte3_e32 v146, v84
	v_cvt_f32_ubyte0_e32 v148, v85
	v_cvt_f32_ubyte1_e32 v150, v85
	v_cvt_f32_ubyte2_e32 v152, v85
	v_cvt_f32_ubyte3_e32 v154, v85
	s_lshl_b32 s30, s98, 12
	s_add_u32 s28, s26, s30
	s_addc_u32 s29, s27, 0
	global_load_dwordx2 v[84:85], v162, s[28:29]
	s_waitcnt vmcnt(34)
	v_cvt_f32_ubyte0_e32 v141, v86
	v_cvt_f32_ubyte1_e32 v143, v86
	v_cvt_f32_ubyte2_e32 v145, v86
	v_cvt_f32_ubyte3_e32 v147, v86
	v_cvt_f32_ubyte0_e32 v149, v87
	v_cvt_f32_ubyte1_e32 v151, v87
	v_cvt_f32_ubyte2_e32 v153, v87
	v_cvt_f32_ubyte3_e32 v155, v87
	s_lshl_b32 s30, s99, 12
	s_add_u32 s28, s26, s30
	s_addc_u32 s29, s27, 0
	global_load_dwordx2 v[86:87], v162, s[28:29]
	v_mul_f32_e32 v206, v124, v108
	v_mul_f32_e32 v207, v125, v108
	v_mul_f32_e32 v208, v140, v108
	v_mul_f32_e32 v209, v141, v108
	v_fmac_f32_e32 v206, v126, v109
	v_fmac_f32_e32 v207, v127, v109
	v_fmac_f32_e32 v208, v142, v109
	v_fmac_f32_e32 v209, v143, v109
	v_fmac_f32_e32 v206, v128, v110
	v_fmac_f32_e32 v207, v129, v110
	v_fmac_f32_e32 v208, v144, v110
	v_fmac_f32_e32 v209, v145, v110
	v_fmac_f32_e32 v206, v130, v111
	v_fmac_f32_e32 v207, v131, v111
	v_fmac_f32_e32 v208, v146, v111
	v_fmac_f32_e32 v209, v147, v111
	v_fmac_f32_e32 v206, v132, v112
	v_fmac_f32_e32 v207, v133, v112
	v_fmac_f32_e32 v208, v148, v112
	v_fmac_f32_e32 v209, v149, v112
	v_fmac_f32_e32 v206, v134, v113
	v_fmac_f32_e32 v207, v135, v113
	v_fmac_f32_e32 v208, v150, v113
	v_fmac_f32_e32 v209, v151, v113
	v_fmac_f32_e32 v206, v136, v114
	v_fmac_f32_e32 v207, v137, v114
	v_fmac_f32_e32 v208, v152, v114
	v_fmac_f32_e32 v209, v153, v114
	v_fmac_f32_e32 v206, v138, v115
	v_fmac_f32_e32 v207, v139, v115
	v_fmac_f32_e32 v208, v154, v115
	v_fmac_f32_e32 v209, v155, v115
	v_permlane32_swap_b32_e32 v178, v194
	v_permlane32_swap_b32_e32 v179, v195
	v_permlane32_swap_b32_e32 v180, v196
	v_permlane32_swap_b32_e32 v181, v197
	v_permlane32_swap_b32_e32 v182, v198
	v_permlane32_swap_b32_e32 v183, v199
	v_permlane32_swap_b32_e32 v184, v200
	v_permlane32_swap_b32_e32 v185, v201
	v_permlane32_swap_b32_e32 v186, v202
	v_permlane32_swap_b32_e32 v187, v203
	v_permlane32_swap_b32_e32 v188, v204
	v_permlane32_swap_b32_e32 v189, v205
	v_permlane32_swap_b32_e32 v190, v206
	v_permlane32_swap_b32_e32 v191, v207
	v_permlane32_swap_b32_e32 v192, v208
	v_permlane32_swap_b32_e32 v193, v209
	v_add_f32_e32 v178, v178, v194
	v_add_f32_e32 v179, v179, v195
	v_add_f32_e32 v180, v180, v196
	v_add_f32_e32 v181, v181, v197
	v_add_f32_e32 v182, v182, v198
	v_add_f32_e32 v183, v183, v199
	v_add_f32_e32 v184, v184, v200
	v_add_f32_e32 v185, v185, v201
	v_add_f32_e32 v186, v186, v202
	v_add_f32_e32 v187, v187, v203
	v_add_f32_e32 v188, v188, v204
	v_add_f32_e32 v189, v189, v205
	v_add_f32_e32 v190, v190, v206
	v_add_f32_e32 v191, v191, v207
	v_add_f32_e32 v192, v192, v208
	v_add_f32_e32 v193, v193, v209
	v_permlane16_swap_b32_e32 v178, v186
	v_permlane16_swap_b32_e32 v179, v187
	v_permlane16_swap_b32_e32 v180, v188
	v_permlane16_swap_b32_e32 v181, v189
	v_permlane16_swap_b32_e32 v182, v190
	v_permlane16_swap_b32_e32 v183, v191
	v_permlane16_swap_b32_e32 v184, v192
	v_permlane16_swap_b32_e32 v185, v193
	v_add_f32_e32 v178, v178, v186
	v_add_f32_e32 v179, v179, v187
	v_add_f32_e32 v180, v180, v188
	v_add_f32_e32 v181, v181, v189
	v_add_f32_e32 v182, v182, v190
	v_add_f32_e32 v183, v183, v191
	v_add_f32_e32 v184, v184, v192
	v_add_f32_e32 v185, v185, v193
	v_cndmask_b32_e64 v2, v178, v182, s[8:9]
	v_cndmask_b32_e64 v3, v179, v183, s[8:9]
	v_cndmask_b32_e64 v4, v180, v184, s[8:9]
	v_cndmask_b32_e64 v5, v181, v185, s[8:9]
	v_cndmask_b32_e64 v6, v182, v178, s[8:9]
	v_cndmask_b32_e64 v7, v183, v179, s[8:9]
	v_cndmask_b32_e64 v8, v184, v180, s[8:9]
	v_cndmask_b32_e64 v9, v185, v181, s[8:9]
	v_add_f32_dpp v6, v2, v6 row_ror:8 row_mask:0xf bank_mask:0xf
	v_add_f32_dpp v7, v3, v7 row_ror:8 row_mask:0xf bank_mask:0xf
	v_add_f32_dpp v8, v4, v8 row_ror:8 row_mask:0xf bank_mask:0xf
	v_add_f32_dpp v9, v5, v9 row_ror:8 row_mask:0xf bank_mask:0xf
	v_cndmask_b32_e64 v2, v6, v8, s[10:11]
	v_cndmask_b32_e64 v3, v7, v9, s[10:11]
	v_cndmask_b32_e64 v4, v8, v6, s[10:11]
	v_cndmask_b32_e64 v5, v9, v7, s[10:11]
	v_add_f32_dpp v4, v2, v4 row_half_mirror row_mask:0xf bank_mask:0xf
	v_add_f32_dpp v5, v3, v5 row_half_mirror row_mask:0xf bank_mask:0xf
	v_cndmask_b32_e64 v2, v4, v5, s[14:15]
	v_cndmask_b32_e64 v3, v5, v4, s[14:15]
	s_nop 0
	v_add_f32_dpp v3, v2, v3 quad_perm:[2,3,0,1] row_mask:0xf bank_mask:0xf
	s_nop 1
	v_add_f32_dpp v11, v3, v3 quad_perm:[1,0,3,2] row_mask:0xf bank_mask:0xf
	s_mov_b64 exec, s[2:3]
	global_store_dword v[22:23], v11, off
	s_mov_b64 exec, -1
	s_waitcnt vmcnt(32)
	v_cvt_f32_ubyte0_e32 v124, v24
	v_cvt_f32_ubyte1_e32 v126, v24
	v_cvt_f32_ubyte2_e32 v128, v24
	v_cvt_f32_ubyte3_e32 v130, v24
	v_cvt_f32_ubyte0_e32 v132, v25
	v_cvt_f32_ubyte1_e32 v134, v25
	v_cvt_f32_ubyte2_e32 v136, v25
	v_cvt_f32_ubyte3_e32 v138, v25
	s_waitcnt lgkmcnt(0)
	s_load_dwordx16 s[84:99], s[36:37], 0x140
	s_lshl_b32 s30, s68, 12
	s_add_u32 s28, s26, s30
	s_addc_u32 s29, s27, 0
	global_load_dwordx2 v[24:25], v162, s[28:29]
	s_waitcnt vmcnt(32)
	v_cvt_f32_ubyte0_e32 v125, v26
	v_cvt_f32_ubyte1_e32 v127, v26
	v_cvt_f32_ubyte2_e32 v129, v26
	v_cvt_f32_ubyte3_e32 v131, v26
	v_cvt_f32_ubyte0_e32 v133, v27
	v_cvt_f32_ubyte1_e32 v135, v27
	v_cvt_f32_ubyte2_e32 v137, v27
	v_cvt_f32_ubyte3_e32 v139, v27
	s_lshl_b32 s30, s69, 12
	s_add_u32 s28, s26, s30
	s_addc_u32 s29, s27, 0
	global_load_dwordx2 v[26:27], v162, s[28:29]
	s_waitcnt vmcnt(32)
	v_cvt_f32_ubyte0_e32 v140, v28
	v_cvt_f32_ubyte1_e32 v142, v28
	v_cvt_f32_ubyte2_e32 v144, v28
	v_cvt_f32_ubyte3_e32 v146, v28
	v_cvt_f32_ubyte0_e32 v148, v29
	v_cvt_f32_ubyte1_e32 v150, v29
	v_cvt_f32_ubyte2_e32 v152, v29
	v_cvt_f32_ubyte3_e32 v154, v29
	s_lshl_b32 s30, s70, 12
	s_add_u32 s28, s26, s30
	s_addc_u32 s29, s27, 0
	global_load_dwordx2 v[28:29], v162, s[28:29]
	s_waitcnt vmcnt(32)
	v_cvt_f32_ubyte0_e32 v141, v30
	v_cvt_f32_ubyte1_e32 v143, v30
	v_cvt_f32_ubyte2_e32 v145, v30
	v_cvt_f32_ubyte3_e32 v147, v30
	v_cvt_f32_ubyte0_e32 v149, v31
	v_cvt_f32_ubyte1_e32 v151, v31
	v_cvt_f32_ubyte2_e32 v153, v31
	v_cvt_f32_ubyte3_e32 v155, v31
	s_lshl_b32 s30, s71, 12
	s_add_u32 s28, s26, s30
	s_addc_u32 s29, s27, 0
	global_load_dwordx2 v[30:31], v162, s[28:29]
	v_mul_f32_e32 v178, v124, v108
	v_mul_f32_e32 v179, v125, v108
	v_mul_f32_e32 v180, v140, v108
	v_mul_f32_e32 v181, v141, v108
	v_fmac_f32_e32 v178, v126, v109
	v_fmac_f32_e32 v179, v127, v109
	v_fmac_f32_e32 v180, v142, v109
	v_fmac_f32_e32 v181, v143, v109
	v_fmac_f32_e32 v178, v128, v110
	v_fmac_f32_e32 v179, v129, v110
	v_fmac_f32_e32 v180, v144, v110
	v_fmac_f32_e32 v181, v145, v110
	v_fmac_f32_e32 v178, v130, v111
	v_fmac_f32_e32 v179, v131, v111
	v_fmac_f32_e32 v180, v146, v111
	v_fmac_f32_e32 v181, v147, v111
	v_fmac_f32_e32 v178, v132, v112
	v_fmac_f32_e32 v179, v133, v112
	v_fmac_f32_e32 v180, v148, v112
	v_fmac_f32_e32 v181, v149, v112
	v_fmac_f32_e32 v178, v134, v113
	v_fmac_f32_e32 v179, v135, v113
	v_fmac_f32_e32 v180, v150, v113
	v_fmac_f32_e32 v181, v151, v113
	v_fmac_f32_e32 v178, v136, v114
	v_fmac_f32_e32 v179, v137, v114
	v_fmac_f32_e32 v180, v152, v114
	v_fmac_f32_e32 v181, v153, v114
	v_fmac_f32_e32 v178, v138, v115
	v_fmac_f32_e32 v179, v139, v115
	v_fmac_f32_e32 v180, v154, v115
	v_fmac_f32_e32 v181, v155, v115
	s_waitcnt vmcnt(32)
	v_cvt_f32_ubyte0_e32 v124, v32
	v_cvt_f32_ubyte1_e32 v126, v32
	v_cvt_f32_ubyte2_e32 v128, v32
	v_cvt_f32_ubyte3_e32 v130, v32
	v_cvt_f32_ubyte0_e32 v132, v33
	v_cvt_f32_ubyte1_e32 v134, v33
	v_cvt_f32_ubyte2_e32 v136, v33
	v_cvt_f32_ubyte3_e32 v138, v33
	s_lshl_b32 s30, s72, 12
	s_add_u32 s28, s26, s30
	s_addc_u32 s29, s27, 0
	global_load_dwordx2 v[32:33], v162, s[28:29]
	s_waitcnt vmcnt(32)
	v_cvt_f32_ubyte0_e32 v125, v34
	v_cvt_f32_ubyte1_e32 v127, v34
	v_cvt_f32_ubyte2_e32 v129, v34
	v_cvt_f32_ubyte3_e32 v131, v34
	v_cvt_f32_ubyte0_e32 v133, v35
	v_cvt_f32_ubyte1_e32 v135, v35
	v_cvt_f32_ubyte2_e32 v137, v35
	v_cvt_f32_ubyte3_e32 v139, v35
	s_lshl_b32 s30, s73, 12
	s_add_u32 s28, s26, s30
	s_addc_u32 s29, s27, 0
	global_load_dwordx2 v[34:35], v162, s[28:29]
	s_waitcnt vmcnt(32)
	v_cvt_f32_ubyte0_e32 v140, v36
	v_cvt_f32_ubyte1_e32 v142, v36
	v_cvt_f32_ubyte2_e32 v144, v36
	v_cvt_f32_ubyte3_e32 v146, v36
	v_cvt_f32_ubyte0_e32 v148, v37
	v_cvt_f32_ubyte1_e32 v150, v37
	v_cvt_f32_ubyte2_e32 v152, v37
	v_cvt_f32_ubyte3_e32 v154, v37
	s_lshl_b32 s30, s74, 12
	s_add_u32 s28, s26, s30
	s_addc_u32 s29, s27, 0
	global_load_dwordx2 v[36:37], v162, s[28:29]
	s_waitcnt vmcnt(32)
	v_cvt_f32_ubyte0_e32 v141, v38
	v_cvt_f32_ubyte1_e32 v143, v38
	v_cvt_f32_ubyte2_e32 v145, v38
	v_cvt_f32_ubyte3_e32 v147, v38
	v_cvt_f32_ubyte0_e32 v149, v39
	v_cvt_f32_ubyte1_e32 v151, v39
	v_cvt_f32_ubyte2_e32 v153, v39
	v_cvt_f32_ubyte3_e32 v155, v39
	s_lshl_b32 s30, s75, 12
	s_add_u32 s28, s26, s30
	s_addc_u32 s29, s27, 0
	global_load_dwordx2 v[38:39], v162, s[28:29]
	v_mul_f32_e32 v182, v124, v108
	v_mul_f32_e32 v183, v125, v108
	v_mul_f32_e32 v184, v140, v108
	v_mul_f32_e32 v185, v141, v108
	v_fmac_f32_e32 v182, v126, v109
	v_fmac_f32_e32 v183, v127, v109
	v_fmac_f32_e32 v184, v142, v109
	v_fmac_f32_e32 v185, v143, v109
	v_fmac_f32_e32 v182, v128, v110
	v_fmac_f32_e32 v183, v129, v110
	v_fmac_f32_e32 v184, v144, v110
	v_fmac_f32_e32 v185, v145, v110
	v_fmac_f32_e32 v182, v130, v111
	v_fmac_f32_e32 v183, v131, v111
	v_fmac_f32_e32 v184, v146, v111
	v_fmac_f32_e32 v185, v147, v111
	v_fmac_f32_e32 v182, v132, v112
	v_fmac_f32_e32 v183, v133, v112
	v_fmac_f32_e32 v184, v148, v112
	v_fmac_f32_e32 v185, v149, v112
	v_fmac_f32_e32 v182, v134, v113
	v_fmac_f32_e32 v183, v135, v113
	v_fmac_f32_e32 v184, v150, v113
	v_fmac_f32_e32 v185, v151, v113
	v_fmac_f32_e32 v182, v136, v114
	v_fmac_f32_e32 v183, v137, v114
	v_fmac_f32_e32 v184, v152, v114
	v_fmac_f32_e32 v185, v153, v114
	v_fmac_f32_e32 v182, v138, v115
	v_fmac_f32_e32 v183, v139, v115
	v_fmac_f32_e32 v184, v154, v115
	v_fmac_f32_e32 v185, v155, v115
	s_waitcnt vmcnt(32)
	v_cvt_f32_ubyte0_e32 v124, v40
	v_cvt_f32_ubyte1_e32 v126, v40
	v_cvt_f32_ubyte2_e32 v128, v40
	v_cvt_f32_ubyte3_e32 v130, v40
	v_cvt_f32_ubyte0_e32 v132, v41
	v_cvt_f32_ubyte1_e32 v134, v41
	v_cvt_f32_ubyte2_e32 v136, v41
	v_cvt_f32_ubyte3_e32 v138, v41
	s_lshl_b32 s30, s76, 12
	s_add_u32 s28, s26, s30
	s_addc_u32 s29, s27, 0
	global_load_dwordx2 v[40:41], v162, s[28:29]
	s_waitcnt vmcnt(32)
	v_cvt_f32_ubyte0_e32 v125, v42
	v_cvt_f32_ubyte1_e32 v127, v42
	v_cvt_f32_ubyte2_e32 v129, v42
	v_cvt_f32_ubyte3_e32 v131, v42
	v_cvt_f32_ubyte0_e32 v133, v43
	v_cvt_f32_ubyte1_e32 v135, v43
	v_cvt_f32_ubyte2_e32 v137, v43
	v_cvt_f32_ubyte3_e32 v139, v43
	s_lshl_b32 s30, s77, 12
	s_add_u32 s28, s26, s30
	s_addc_u32 s29, s27, 0
	global_load_dwordx2 v[42:43], v162, s[28:29]
	s_waitcnt vmcnt(32)
	v_cvt_f32_ubyte0_e32 v140, v44
	v_cvt_f32_ubyte1_e32 v142, v44
	v_cvt_f32_ubyte2_e32 v144, v44
	v_cvt_f32_ubyte3_e32 v146, v44
	v_cvt_f32_ubyte0_e32 v148, v45
	v_cvt_f32_ubyte1_e32 v150, v45
	v_cvt_f32_ubyte2_e32 v152, v45
	v_cvt_f32_ubyte3_e32 v154, v45
	s_lshl_b32 s30, s78, 12
	s_add_u32 s28, s26, s30
	s_addc_u32 s29, s27, 0
	global_load_dwordx2 v[44:45], v162, s[28:29]
	s_waitcnt vmcnt(32)
	v_cvt_f32_ubyte0_e32 v141, v46
	v_cvt_f32_ubyte1_e32 v143, v46
	v_cvt_f32_ubyte2_e32 v145, v46
	v_cvt_f32_ubyte3_e32 v147, v46
	v_cvt_f32_ubyte0_e32 v149, v47
	v_cvt_f32_ubyte1_e32 v151, v47
	v_cvt_f32_ubyte2_e32 v153, v47
	v_cvt_f32_ubyte3_e32 v155, v47
	s_lshl_b32 s30, s79, 12
	s_add_u32 s28, s26, s30
	s_addc_u32 s29, s27, 0
	global_load_dwordx2 v[46:47], v162, s[28:29]
	v_mul_f32_e32 v186, v124, v108
	v_mul_f32_e32 v187, v125, v108
	v_mul_f32_e32 v188, v140, v108
	v_mul_f32_e32 v189, v141, v108
	v_fmac_f32_e32 v186, v126, v109
	v_fmac_f32_e32 v187, v127, v109
	v_fmac_f32_e32 v188, v142, v109
	v_fmac_f32_e32 v189, v143, v109
	v_fmac_f32_e32 v186, v128, v110
	v_fmac_f32_e32 v187, v129, v110
	v_fmac_f32_e32 v188, v144, v110
	v_fmac_f32_e32 v189, v145, v110
	v_fmac_f32_e32 v186, v130, v111
	v_fmac_f32_e32 v187, v131, v111
	v_fmac_f32_e32 v188, v146, v111
	v_fmac_f32_e32 v189, v147, v111
	v_fmac_f32_e32 v186, v132, v112
	v_fmac_f32_e32 v187, v133, v112
	v_fmac_f32_e32 v188, v148, v112
	v_fmac_f32_e32 v189, v149, v112
	v_fmac_f32_e32 v186, v134, v113
	v_fmac_f32_e32 v187, v135, v113
	v_fmac_f32_e32 v188, v150, v113
	v_fmac_f32_e32 v189, v151, v113
	v_fmac_f32_e32 v186, v136, v114
	v_fmac_f32_e32 v187, v137, v114
	v_fmac_f32_e32 v188, v152, v114
	v_fmac_f32_e32 v189, v153, v114
	v_fmac_f32_e32 v186, v138, v115
	v_fmac_f32_e32 v187, v139, v115
	v_fmac_f32_e32 v188, v154, v115
	v_fmac_f32_e32 v189, v155, v115
	s_waitcnt vmcnt(32)
	v_cvt_f32_ubyte0_e32 v124, v48
	v_cvt_f32_ubyte1_e32 v126, v48
	v_cvt_f32_ubyte2_e32 v128, v48
	v_cvt_f32_ubyte3_e32 v130, v48
	v_cvt_f32_ubyte0_e32 v132, v49
	v_cvt_f32_ubyte1_e32 v134, v49
	v_cvt_f32_ubyte2_e32 v136, v49
	v_cvt_f32_ubyte3_e32 v138, v49
	s_lshl_b32 s30, s80, 12
	s_add_u32 s28, s26, s30
	s_addc_u32 s29, s27, 0
	global_load_dwordx2 v[48:49], v162, s[28:29]
	s_waitcnt vmcnt(32)
	v_cvt_f32_ubyte0_e32 v125, v50
	v_cvt_f32_ubyte1_e32 v127, v50
	v_cvt_f32_ubyte2_e32 v129, v50
	v_cvt_f32_ubyte3_e32 v131, v50
	v_cvt_f32_ubyte0_e32 v133, v51
	v_cvt_f32_ubyte1_e32 v135, v51
	v_cvt_f32_ubyte2_e32 v137, v51
	v_cvt_f32_ubyte3_e32 v139, v51
	s_lshl_b32 s30, s81, 12
	s_add_u32 s28, s26, s30
	s_addc_u32 s29, s27, 0
	global_load_dwordx2 v[50:51], v162, s[28:29]
	s_waitcnt vmcnt(32)
	v_cvt_f32_ubyte0_e32 v140, v52
	v_cvt_f32_ubyte1_e32 v142, v52
	v_cvt_f32_ubyte2_e32 v144, v52
	v_cvt_f32_ubyte3_e32 v146, v52
	v_cvt_f32_ubyte0_e32 v148, v53
	v_cvt_f32_ubyte1_e32 v150, v53
	v_cvt_f32_ubyte2_e32 v152, v53
	v_cvt_f32_ubyte3_e32 v154, v53
	s_lshl_b32 s30, s82, 12
	s_add_u32 s28, s26, s30
	s_addc_u32 s29, s27, 0
	global_load_dwordx2 v[52:53], v162, s[28:29]
	s_waitcnt vmcnt(32)
	v_cvt_f32_ubyte0_e32 v141, v54
	v_cvt_f32_ubyte1_e32 v143, v54
	v_cvt_f32_ubyte2_e32 v145, v54
	v_cvt_f32_ubyte3_e32 v147, v54
	v_cvt_f32_ubyte0_e32 v149, v55
	v_cvt_f32_ubyte1_e32 v151, v55
	v_cvt_f32_ubyte2_e32 v153, v55
	v_cvt_f32_ubyte3_e32 v155, v55
	s_lshl_b32 s30, s83, 12
	s_add_u32 s28, s26, s30
	s_addc_u32 s29, s27, 0
	global_load_dwordx2 v[54:55], v162, s[28:29]
	v_mul_f32_e32 v190, v124, v108
	v_mul_f32_e32 v191, v125, v108
	v_mul_f32_e32 v192, v140, v108
	v_mul_f32_e32 v193, v141, v108
	v_fmac_f32_e32 v190, v126, v109
	v_fmac_f32_e32 v191, v127, v109
	v_fmac_f32_e32 v192, v142, v109
	v_fmac_f32_e32 v193, v143, v109
	v_fmac_f32_e32 v190, v128, v110
	v_fmac_f32_e32 v191, v129, v110
	v_fmac_f32_e32 v192, v144, v110
	v_fmac_f32_e32 v193, v145, v110
	v_fmac_f32_e32 v190, v130, v111
	v_fmac_f32_e32 v191, v131, v111
	v_fmac_f32_e32 v192, v146, v111
	v_fmac_f32_e32 v193, v147, v111
	v_fmac_f32_e32 v190, v132, v112
	v_fmac_f32_e32 v191, v133, v112
	v_fmac_f32_e32 v192, v148, v112
	v_fmac_f32_e32 v193, v149, v112
	v_fmac_f32_e32 v190, v134, v113
	v_fmac_f32_e32 v191, v135, v113
	v_fmac_f32_e32 v192, v150, v113
	v_fmac_f32_e32 v193, v151, v113
	v_fmac_f32_e32 v190, v136, v114
	v_fmac_f32_e32 v191, v137, v114
	v_fmac_f32_e32 v192, v152, v114
	v_fmac_f32_e32 v193, v153, v114
	v_fmac_f32_e32 v190, v138, v115
	v_fmac_f32_e32 v191, v139, v115
	v_fmac_f32_e32 v192, v154, v115
	v_fmac_f32_e32 v193, v155, v115
	s_waitcnt vmcnt(32)
	v_cvt_f32_ubyte0_e32 v124, v56
	v_cvt_f32_ubyte1_e32 v126, v56
	v_cvt_f32_ubyte2_e32 v128, v56
	v_cvt_f32_ubyte3_e32 v130, v56
	v_cvt_f32_ubyte0_e32 v132, v57
	v_cvt_f32_ubyte1_e32 v134, v57
	v_cvt_f32_ubyte2_e32 v136, v57
	v_cvt_f32_ubyte3_e32 v138, v57
	s_waitcnt lgkmcnt(0)
	s_load_dwordx16 s[68:83], s[36:37], 0x180
	s_lshl_b32 s30, s84, 12
	s_add_u32 s28, s26, s30
	s_addc_u32 s29, s27, 0
	global_load_dwordx2 v[56:57], v162, s[28:29]
	s_waitcnt vmcnt(32)
	v_cvt_f32_ubyte0_e32 v125, v58
	v_cvt_f32_ubyte1_e32 v127, v58
	v_cvt_f32_ubyte2_e32 v129, v58
	v_cvt_f32_ubyte3_e32 v131, v58
	v_cvt_f32_ubyte0_e32 v133, v59
	v_cvt_f32_ubyte1_e32 v135, v59
	v_cvt_f32_ubyte2_e32 v137, v59
	v_cvt_f32_ubyte3_e32 v139, v59
	s_lshl_b32 s30, s85, 12
	s_add_u32 s28, s26, s30
	s_addc_u32 s29, s27, 0
	global_load_dwordx2 v[58:59], v162, s[28:29]
	s_waitcnt vmcnt(32)
	v_cvt_f32_ubyte0_e32 v140, v60
	v_cvt_f32_ubyte1_e32 v142, v60
	v_cvt_f32_ubyte2_e32 v144, v60
	v_cvt_f32_ubyte3_e32 v146, v60
	v_cvt_f32_ubyte0_e32 v148, v61
	v_cvt_f32_ubyte1_e32 v150, v61
	v_cvt_f32_ubyte2_e32 v152, v61
	v_cvt_f32_ubyte3_e32 v154, v61
	s_lshl_b32 s30, s86, 12
	s_add_u32 s28, s26, s30
	s_addc_u32 s29, s27, 0
	global_load_dwordx2 v[60:61], v162, s[28:29]
	s_waitcnt vmcnt(32)
	v_cvt_f32_ubyte0_e32 v141, v62
	v_cvt_f32_ubyte1_e32 v143, v62
	v_cvt_f32_ubyte2_e32 v145, v62
	v_cvt_f32_ubyte3_e32 v147, v62
	v_cvt_f32_ubyte0_e32 v149, v63
	v_cvt_f32_ubyte1_e32 v151, v63
	v_cvt_f32_ubyte2_e32 v153, v63
	v_cvt_f32_ubyte3_e32 v155, v63
	s_lshl_b32 s30, s87, 12
	s_add_u32 s28, s26, s30
	s_addc_u32 s29, s27, 0
	global_load_dwordx2 v[62:63], v162, s[28:29]
	v_mul_f32_e32 v194, v124, v108
	v_mul_f32_e32 v195, v125, v108
	v_mul_f32_e32 v196, v140, v108
	v_mul_f32_e32 v197, v141, v108
	v_fmac_f32_e32 v194, v126, v109
	v_fmac_f32_e32 v195, v127, v109
	v_fmac_f32_e32 v196, v142, v109
	v_fmac_f32_e32 v197, v143, v109
	v_fmac_f32_e32 v194, v128, v110
	v_fmac_f32_e32 v195, v129, v110
	v_fmac_f32_e32 v196, v144, v110
	v_fmac_f32_e32 v197, v145, v110
	v_fmac_f32_e32 v194, v130, v111
	v_fmac_f32_e32 v195, v131, v111
	v_fmac_f32_e32 v196, v146, v111
	v_fmac_f32_e32 v197, v147, v111
	v_fmac_f32_e32 v194, v132, v112
	v_fmac_f32_e32 v195, v133, v112
	v_fmac_f32_e32 v196, v148, v112
	v_fmac_f32_e32 v197, v149, v112
	v_fmac_f32_e32 v194, v134, v113
	v_fmac_f32_e32 v195, v135, v113
	v_fmac_f32_e32 v196, v150, v113
	v_fmac_f32_e32 v197, v151, v113
	v_fmac_f32_e32 v194, v136, v114
	v_fmac_f32_e32 v195, v137, v114
	v_fmac_f32_e32 v196, v152, v114
	v_fmac_f32_e32 v197, v153, v114
	v_fmac_f32_e32 v194, v138, v115
	v_fmac_f32_e32 v195, v139, v115
	v_fmac_f32_e32 v196, v154, v115
	v_fmac_f32_e32 v197, v155, v115
	s_waitcnt vmcnt(32)
	v_cvt_f32_ubyte0_e32 v124, v64
	v_cvt_f32_ubyte1_e32 v126, v64
	v_cvt_f32_ubyte2_e32 v128, v64
	v_cvt_f32_ubyte3_e32 v130, v64
	v_cvt_f32_ubyte0_e32 v132, v65
	v_cvt_f32_ubyte1_e32 v134, v65
	v_cvt_f32_ubyte2_e32 v136, v65
	v_cvt_f32_ubyte3_e32 v138, v65
	s_lshl_b32 s30, s88, 12
	s_add_u32 s28, s26, s30
	s_addc_u32 s29, s27, 0
	global_load_dwordx2 v[64:65], v162, s[28:29]
	s_waitcnt vmcnt(32)
	v_cvt_f32_ubyte0_e32 v125, v66
	v_cvt_f32_ubyte1_e32 v127, v66
	v_cvt_f32_ubyte2_e32 v129, v66
	v_cvt_f32_ubyte3_e32 v131, v66
	v_cvt_f32_ubyte0_e32 v133, v67
	v_cvt_f32_ubyte1_e32 v135, v67
	v_cvt_f32_ubyte2_e32 v137, v67
	v_cvt_f32_ubyte3_e32 v139, v67
	s_lshl_b32 s30, s89, 12
	s_add_u32 s28, s26, s30
	s_addc_u32 s29, s27, 0
	global_load_dwordx2 v[66:67], v162, s[28:29]
	s_waitcnt vmcnt(32)
	v_cvt_f32_ubyte0_e32 v140, v68
	v_cvt_f32_ubyte1_e32 v142, v68
	v_cvt_f32_ubyte2_e32 v144, v68
	v_cvt_f32_ubyte3_e32 v146, v68
	v_cvt_f32_ubyte0_e32 v148, v69
	v_cvt_f32_ubyte1_e32 v150, v69
	v_cvt_f32_ubyte2_e32 v152, v69
	v_cvt_f32_ubyte3_e32 v154, v69
	s_lshl_b32 s30, s90, 12
	s_add_u32 s28, s26, s30
	s_addc_u32 s29, s27, 0
	global_load_dwordx2 v[68:69], v162, s[28:29]
	s_waitcnt vmcnt(32)
	v_cvt_f32_ubyte0_e32 v141, v70
	v_cvt_f32_ubyte1_e32 v143, v70
	v_cvt_f32_ubyte2_e32 v145, v70
	v_cvt_f32_ubyte3_e32 v147, v70
	v_cvt_f32_ubyte0_e32 v149, v71
	v_cvt_f32_ubyte1_e32 v151, v71
	v_cvt_f32_ubyte2_e32 v153, v71
	v_cvt_f32_ubyte3_e32 v155, v71
	s_lshl_b32 s30, s91, 12
	s_add_u32 s28, s26, s30
	s_addc_u32 s29, s27, 0
	global_load_dwordx2 v[70:71], v162, s[28:29]
	v_mul_f32_e32 v198, v124, v108
	v_mul_f32_e32 v199, v125, v108
	v_mul_f32_e32 v200, v140, v108
	v_mul_f32_e32 v201, v141, v108
	v_fmac_f32_e32 v198, v126, v109
	v_fmac_f32_e32 v199, v127, v109
	v_fmac_f32_e32 v200, v142, v109
	v_fmac_f32_e32 v201, v143, v109
	v_fmac_f32_e32 v198, v128, v110
	v_fmac_f32_e32 v199, v129, v110
	v_fmac_f32_e32 v200, v144, v110
	v_fmac_f32_e32 v201, v145, v110
	v_fmac_f32_e32 v198, v130, v111
	v_fmac_f32_e32 v199, v131, v111
	v_fmac_f32_e32 v200, v146, v111
	v_fmac_f32_e32 v201, v147, v111
	v_fmac_f32_e32 v198, v132, v112
	v_fmac_f32_e32 v199, v133, v112
	v_fmac_f32_e32 v200, v148, v112
	v_fmac_f32_e32 v201, v149, v112
	v_fmac_f32_e32 v198, v134, v113
	v_fmac_f32_e32 v199, v135, v113
	v_fmac_f32_e32 v200, v150, v113
	v_fmac_f32_e32 v201, v151, v113
	v_fmac_f32_e32 v198, v136, v114
	v_fmac_f32_e32 v199, v137, v114
	v_fmac_f32_e32 v200, v152, v114
	v_fmac_f32_e32 v201, v153, v114
	v_fmac_f32_e32 v198, v138, v115
	v_fmac_f32_e32 v199, v139, v115
	v_fmac_f32_e32 v200, v154, v115
	v_fmac_f32_e32 v201, v155, v115
	s_waitcnt vmcnt(32)
	v_cvt_f32_ubyte0_e32 v124, v72
	v_cvt_f32_ubyte1_e32 v126, v72
	v_cvt_f32_ubyte2_e32 v128, v72
	v_cvt_f32_ubyte3_e32 v130, v72
	v_cvt_f32_ubyte0_e32 v132, v73
	v_cvt_f32_ubyte1_e32 v134, v73
	v_cvt_f32_ubyte2_e32 v136, v73
	v_cvt_f32_ubyte3_e32 v138, v73
	s_lshl_b32 s30, s92, 12
	s_add_u32 s28, s26, s30
	s_addc_u32 s29, s27, 0
	global_load_dwordx2 v[72:73], v162, s[28:29]
	s_waitcnt vmcnt(32)
	v_cvt_f32_ubyte0_e32 v125, v74
	v_cvt_f32_ubyte1_e32 v127, v74
	v_cvt_f32_ubyte2_e32 v129, v74
	v_cvt_f32_ubyte3_e32 v131, v74
	v_cvt_f32_ubyte0_e32 v133, v75
	v_cvt_f32_ubyte1_e32 v135, v75
	v_cvt_f32_ubyte2_e32 v137, v75
	v_cvt_f32_ubyte3_e32 v139, v75
	s_lshl_b32 s30, s93, 12
	s_add_u32 s28, s26, s30
	s_addc_u32 s29, s27, 0
	global_load_dwordx2 v[74:75], v162, s[28:29]
	s_waitcnt vmcnt(32)
	v_cvt_f32_ubyte0_e32 v140, v76
	v_cvt_f32_ubyte1_e32 v142, v76
	v_cvt_f32_ubyte2_e32 v144, v76
	v_cvt_f32_ubyte3_e32 v146, v76
	v_cvt_f32_ubyte0_e32 v148, v77
	v_cvt_f32_ubyte1_e32 v150, v77
	v_cvt_f32_ubyte2_e32 v152, v77
	v_cvt_f32_ubyte3_e32 v154, v77
	s_lshl_b32 s30, s94, 12
	s_add_u32 s28, s26, s30
	s_addc_u32 s29, s27, 0
	global_load_dwordx2 v[76:77], v162, s[28:29]
	s_waitcnt vmcnt(32)
	v_cvt_f32_ubyte0_e32 v141, v78
	v_cvt_f32_ubyte1_e32 v143, v78
	v_cvt_f32_ubyte2_e32 v145, v78
	v_cvt_f32_ubyte3_e32 v147, v78
	v_cvt_f32_ubyte0_e32 v149, v79
	v_cvt_f32_ubyte1_e32 v151, v79
	v_cvt_f32_ubyte2_e32 v153, v79
	v_cvt_f32_ubyte3_e32 v155, v79
	s_lshl_b32 s30, s95, 12
	s_add_u32 s28, s26, s30
	s_addc_u32 s29, s27, 0
	global_load_dwordx2 v[78:79], v162, s[28:29]
	v_mul_f32_e32 v202, v124, v108
	v_mul_f32_e32 v203, v125, v108
	v_mul_f32_e32 v204, v140, v108
	v_mul_f32_e32 v205, v141, v108
	v_fmac_f32_e32 v202, v126, v109
	v_fmac_f32_e32 v203, v127, v109
	v_fmac_f32_e32 v204, v142, v109
	v_fmac_f32_e32 v205, v143, v109
	v_fmac_f32_e32 v202, v128, v110
	v_fmac_f32_e32 v203, v129, v110
	v_fmac_f32_e32 v204, v144, v110
	v_fmac_f32_e32 v205, v145, v110
	v_fmac_f32_e32 v202, v130, v111
	v_fmac_f32_e32 v203, v131, v111
	v_fmac_f32_e32 v204, v146, v111
	v_fmac_f32_e32 v205, v147, v111
	v_fmac_f32_e32 v202, v132, v112
	v_fmac_f32_e32 v203, v133, v112
	v_fmac_f32_e32 v204, v148, v112
	v_fmac_f32_e32 v205, v149, v112
	v_fmac_f32_e32 v202, v134, v113
	v_fmac_f32_e32 v203, v135, v113
	v_fmac_f32_e32 v204, v150, v113
	v_fmac_f32_e32 v205, v151, v113
	v_fmac_f32_e32 v202, v136, v114
	v_fmac_f32_e32 v203, v137, v114
	v_fmac_f32_e32 v204, v152, v114
	v_fmac_f32_e32 v205, v153, v114
	v_fmac_f32_e32 v202, v138, v115
	v_fmac_f32_e32 v203, v139, v115
	v_fmac_f32_e32 v204, v154, v115
	v_fmac_f32_e32 v205, v155, v115
	s_waitcnt vmcnt(32)
	v_cvt_f32_ubyte0_e32 v124, v80
	v_cvt_f32_ubyte1_e32 v126, v80
	v_cvt_f32_ubyte2_e32 v128, v80
	v_cvt_f32_ubyte3_e32 v130, v80
	v_cvt_f32_ubyte0_e32 v132, v81
	v_cvt_f32_ubyte1_e32 v134, v81
	v_cvt_f32_ubyte2_e32 v136, v81
	v_cvt_f32_ubyte3_e32 v138, v81
	s_lshl_b32 s30, s96, 12
	s_add_u32 s28, s26, s30
	s_addc_u32 s29, s27, 0
	global_load_dwordx2 v[80:81], v162, s[28:29]
	s_waitcnt vmcnt(32)
	v_cvt_f32_ubyte0_e32 v125, v82
	v_cvt_f32_ubyte1_e32 v127, v82
	v_cvt_f32_ubyte2_e32 v129, v82
	v_cvt_f32_ubyte3_e32 v131, v82
	v_cvt_f32_ubyte0_e32 v133, v83
	v_cvt_f32_ubyte1_e32 v135, v83
	v_cvt_f32_ubyte2_e32 v137, v83
	v_cvt_f32_ubyte3_e32 v139, v83
	s_lshl_b32 s30, s97, 12
	s_add_u32 s28, s26, s30
	s_addc_u32 s29, s27, 0
	global_load_dwordx2 v[82:83], v162, s[28:29]
	s_waitcnt vmcnt(32)
	v_cvt_f32_ubyte0_e32 v140, v84
	v_cvt_f32_ubyte1_e32 v142, v84
	v_cvt_f32_ubyte2_e32 v144, v84
	v_cvt_f32_ubyte3_e32 v146, v84
	v_cvt_f32_ubyte0_e32 v148, v85
	v_cvt_f32_ubyte1_e32 v150, v85
	v_cvt_f32_ubyte2_e32 v152, v85
	v_cvt_f32_ubyte3_e32 v154, v85
	s_lshl_b32 s30, s98, 12
	s_add_u32 s28, s26, s30
	s_addc_u32 s29, s27, 0
	global_load_dwordx2 v[84:85], v162, s[28:29]
	s_waitcnt vmcnt(32)
	v_cvt_f32_ubyte0_e32 v141, v86
	v_cvt_f32_ubyte1_e32 v143, v86
	v_cvt_f32_ubyte2_e32 v145, v86
	v_cvt_f32_ubyte3_e32 v147, v86
	v_cvt_f32_ubyte0_e32 v149, v87
	v_cvt_f32_ubyte1_e32 v151, v87
	v_cvt_f32_ubyte2_e32 v153, v87
	v_cvt_f32_ubyte3_e32 v155, v87
	s_lshl_b32 s30, s99, 12
	s_add_u32 s28, s26, s30
	s_addc_u32 s29, s27, 0
	global_load_dwordx2 v[86:87], v162, s[28:29]
	v_mul_f32_e32 v206, v124, v108
	v_mul_f32_e32 v207, v125, v108
	v_mul_f32_e32 v208, v140, v108
	v_mul_f32_e32 v209, v141, v108
	v_fmac_f32_e32 v206, v126, v109
	v_fmac_f32_e32 v207, v127, v109
	v_fmac_f32_e32 v208, v142, v109
	v_fmac_f32_e32 v209, v143, v109
	v_fmac_f32_e32 v206, v128, v110
	v_fmac_f32_e32 v207, v129, v110
	v_fmac_f32_e32 v208, v144, v110
	v_fmac_f32_e32 v209, v145, v110
	v_fmac_f32_e32 v206, v130, v111
	v_fmac_f32_e32 v207, v131, v111
	v_fmac_f32_e32 v208, v146, v111
	v_fmac_f32_e32 v209, v147, v111
	v_fmac_f32_e32 v206, v132, v112
	v_fmac_f32_e32 v207, v133, v112
	v_fmac_f32_e32 v208, v148, v112
	v_fmac_f32_e32 v209, v149, v112
	v_fmac_f32_e32 v206, v134, v113
	v_fmac_f32_e32 v207, v135, v113
	v_fmac_f32_e32 v208, v150, v113
	v_fmac_f32_e32 v209, v151, v113
	v_fmac_f32_e32 v206, v136, v114
	v_fmac_f32_e32 v207, v137, v114
	v_fmac_f32_e32 v208, v152, v114
	v_fmac_f32_e32 v209, v153, v114
	v_fmac_f32_e32 v206, v138, v115
	v_fmac_f32_e32 v207, v139, v115
	v_fmac_f32_e32 v208, v154, v115
	v_fmac_f32_e32 v209, v155, v115
	v_permlane32_swap_b32_e32 v178, v194
	v_permlane32_swap_b32_e32 v179, v195
	v_permlane32_swap_b32_e32 v180, v196
	v_permlane32_swap_b32_e32 v181, v197
	v_permlane32_swap_b32_e32 v182, v198
	v_permlane32_swap_b32_e32 v183, v199
	v_permlane32_swap_b32_e32 v184, v200
	v_permlane32_swap_b32_e32 v185, v201
	v_permlane32_swap_b32_e32 v186, v202
	v_permlane32_swap_b32_e32 v187, v203
	v_permlane32_swap_b32_e32 v188, v204
	v_permlane32_swap_b32_e32 v189, v205
	v_permlane32_swap_b32_e32 v190, v206
	v_permlane32_swap_b32_e32 v191, v207
	v_permlane32_swap_b32_e32 v192, v208
	v_permlane32_swap_b32_e32 v193, v209
	v_add_f32_e32 v178, v178, v194
	v_add_f32_e32 v179, v179, v195
	v_add_f32_e32 v180, v180, v196
	v_add_f32_e32 v181, v181, v197
	v_add_f32_e32 v182, v182, v198
	v_add_f32_e32 v183, v183, v199
	v_add_f32_e32 v184, v184, v200
	v_add_f32_e32 v185, v185, v201
	v_add_f32_e32 v186, v186, v202
	v_add_f32_e32 v187, v187, v203
	v_add_f32_e32 v188, v188, v204
	v_add_f32_e32 v189, v189, v205
	v_add_f32_e32 v190, v190, v206
	v_add_f32_e32 v191, v191, v207
	v_add_f32_e32 v192, v192, v208
	v_add_f32_e32 v193, v193, v209
	v_permlane16_swap_b32_e32 v178, v186
	v_permlane16_swap_b32_e32 v179, v187
	v_permlane16_swap_b32_e32 v180, v188
	v_permlane16_swap_b32_e32 v181, v189
	v_permlane16_swap_b32_e32 v182, v190
	v_permlane16_swap_b32_e32 v183, v191
	v_permlane16_swap_b32_e32 v184, v192
	v_permlane16_swap_b32_e32 v185, v193
	v_add_f32_e32 v178, v178, v186
	v_add_f32_e32 v179, v179, v187
	v_add_f32_e32 v180, v180, v188
	v_add_f32_e32 v181, v181, v189
	v_add_f32_e32 v182, v182, v190
	v_add_f32_e32 v183, v183, v191
	v_add_f32_e32 v184, v184, v192
	v_add_f32_e32 v185, v185, v193
	v_cndmask_b32_e64 v2, v178, v182, s[8:9]
	v_cndmask_b32_e64 v3, v179, v183, s[8:9]
	v_cndmask_b32_e64 v4, v180, v184, s[8:9]
	v_cndmask_b32_e64 v5, v181, v185, s[8:9]
	v_cndmask_b32_e64 v6, v182, v178, s[8:9]
	v_cndmask_b32_e64 v7, v183, v179, s[8:9]
	v_cndmask_b32_e64 v8, v184, v180, s[8:9]
	v_cndmask_b32_e64 v9, v185, v181, s[8:9]
	v_add_f32_dpp v6, v2, v6 row_ror:8 row_mask:0xf bank_mask:0xf
	v_add_f32_dpp v7, v3, v7 row_ror:8 row_mask:0xf bank_mask:0xf
	v_add_f32_dpp v8, v4, v8 row_ror:8 row_mask:0xf bank_mask:0xf
	v_add_f32_dpp v9, v5, v9 row_ror:8 row_mask:0xf bank_mask:0xf
	v_cndmask_b32_e64 v2, v6, v8, s[10:11]
	v_cndmask_b32_e64 v3, v7, v9, s[10:11]
	v_cndmask_b32_e64 v4, v8, v6, s[10:11]
	v_cndmask_b32_e64 v5, v9, v7, s[10:11]
	v_add_f32_dpp v4, v2, v4 row_half_mirror row_mask:0xf bank_mask:0xf
	v_add_f32_dpp v5, v3, v5 row_half_mirror row_mask:0xf bank_mask:0xf
	v_cndmask_b32_e64 v2, v4, v5, s[14:15]
	v_cndmask_b32_e64 v3, v5, v4, s[14:15]
	s_nop 0
	v_add_f32_dpp v3, v2, v3 quad_perm:[2,3,0,1] row_mask:0xf bank_mask:0xf
	s_nop 1
	v_add_f32_dpp v11, v3, v3 quad_perm:[1,0,3,2] row_mask:0xf bank_mask:0xf
	s_mov_b64 exec, s[2:3]
	global_store_dword v[22:23], v11, off offset:128
	s_mov_b64 exec, -1
	s_waitcnt vmcnt(32)
	v_cvt_f32_ubyte0_e32 v124, v24
	v_cvt_f32_ubyte1_e32 v126, v24
	v_cvt_f32_ubyte2_e32 v128, v24
	v_cvt_f32_ubyte3_e32 v130, v24
	v_cvt_f32_ubyte0_e32 v132, v25
	v_cvt_f32_ubyte1_e32 v134, v25
	v_cvt_f32_ubyte2_e32 v136, v25
	v_cvt_f32_ubyte3_e32 v138, v25
	s_waitcnt lgkmcnt(0)
	s_load_dwordx16 s[84:99], s[36:37], 0x1c0
	s_lshl_b32 s30, s68, 12
	s_add_u32 s28, s26, s30
	s_addc_u32 s29, s27, 0
	global_load_dwordx2 v[24:25], v162, s[28:29]
	s_waitcnt vmcnt(32)
	v_cvt_f32_ubyte0_e32 v125, v26
	v_cvt_f32_ubyte1_e32 v127, v26
	v_cvt_f32_ubyte2_e32 v129, v26
	v_cvt_f32_ubyte3_e32 v131, v26
	v_cvt_f32_ubyte0_e32 v133, v27
	v_cvt_f32_ubyte1_e32 v135, v27
	v_cvt_f32_ubyte2_e32 v137, v27
	v_cvt_f32_ubyte3_e32 v139, v27
	s_lshl_b32 s30, s69, 12
	s_add_u32 s28, s26, s30
	s_addc_u32 s29, s27, 0
	global_load_dwordx2 v[26:27], v162, s[28:29]
	s_waitcnt vmcnt(32)
	v_cvt_f32_ubyte0_e32 v140, v28
	v_cvt_f32_ubyte1_e32 v142, v28
	v_cvt_f32_ubyte2_e32 v144, v28
	v_cvt_f32_ubyte3_e32 v146, v28
	v_cvt_f32_ubyte0_e32 v148, v29
	v_cvt_f32_ubyte1_e32 v150, v29
	v_cvt_f32_ubyte2_e32 v152, v29
	v_cvt_f32_ubyte3_e32 v154, v29
	s_lshl_b32 s30, s70, 12
	s_add_u32 s28, s26, s30
	s_addc_u32 s29, s27, 0
	global_load_dwordx2 v[28:29], v162, s[28:29]
	s_waitcnt vmcnt(32)
	v_cvt_f32_ubyte0_e32 v141, v30
	v_cvt_f32_ubyte1_e32 v143, v30
	v_cvt_f32_ubyte2_e32 v145, v30
	v_cvt_f32_ubyte3_e32 v147, v30
	v_cvt_f32_ubyte0_e32 v149, v31
	v_cvt_f32_ubyte1_e32 v151, v31
	v_cvt_f32_ubyte2_e32 v153, v31
	v_cvt_f32_ubyte3_e32 v155, v31
	s_lshl_b32 s30, s71, 12
	s_add_u32 s28, s26, s30
	s_addc_u32 s29, s27, 0
	global_load_dwordx2 v[30:31], v162, s[28:29]
	v_mul_f32_e32 v178, v124, v108
	v_mul_f32_e32 v179, v125, v108
	v_mul_f32_e32 v180, v140, v108
	v_mul_f32_e32 v181, v141, v108
	v_fmac_f32_e32 v178, v126, v109
	v_fmac_f32_e32 v179, v127, v109
	v_fmac_f32_e32 v180, v142, v109
	v_fmac_f32_e32 v181, v143, v109
	v_fmac_f32_e32 v178, v128, v110
	v_fmac_f32_e32 v179, v129, v110
	v_fmac_f32_e32 v180, v144, v110
	v_fmac_f32_e32 v181, v145, v110
	v_fmac_f32_e32 v178, v130, v111
	v_fmac_f32_e32 v179, v131, v111
	v_fmac_f32_e32 v180, v146, v111
	v_fmac_f32_e32 v181, v147, v111
	v_fmac_f32_e32 v178, v132, v112
	v_fmac_f32_e32 v179, v133, v112
	v_fmac_f32_e32 v180, v148, v112
	v_fmac_f32_e32 v181, v149, v112
	v_fmac_f32_e32 v178, v134, v113
	v_fmac_f32_e32 v179, v135, v113
	v_fmac_f32_e32 v180, v150, v113
	v_fmac_f32_e32 v181, v151, v113
	v_fmac_f32_e32 v178, v136, v114
	v_fmac_f32_e32 v179, v137, v114
	v_fmac_f32_e32 v180, v152, v114
	v_fmac_f32_e32 v181, v153, v114
	v_fmac_f32_e32 v178, v138, v115
	v_fmac_f32_e32 v179, v139, v115
	v_fmac_f32_e32 v180, v154, v115
	v_fmac_f32_e32 v181, v155, v115
	s_waitcnt vmcnt(32)
	v_cvt_f32_ubyte0_e32 v124, v32
	v_cvt_f32_ubyte1_e32 v126, v32
	v_cvt_f32_ubyte2_e32 v128, v32
	v_cvt_f32_ubyte3_e32 v130, v32
	v_cvt_f32_ubyte0_e32 v132, v33
	v_cvt_f32_ubyte1_e32 v134, v33
	v_cvt_f32_ubyte2_e32 v136, v33
	v_cvt_f32_ubyte3_e32 v138, v33
	s_lshl_b32 s30, s72, 12
	s_add_u32 s28, s26, s30
	s_addc_u32 s29, s27, 0
	global_load_dwordx2 v[32:33], v162, s[28:29]
	s_waitcnt vmcnt(32)
	v_cvt_f32_ubyte0_e32 v125, v34
	v_cvt_f32_ubyte1_e32 v127, v34
	v_cvt_f32_ubyte2_e32 v129, v34
	v_cvt_f32_ubyte3_e32 v131, v34
	v_cvt_f32_ubyte0_e32 v133, v35
	v_cvt_f32_ubyte1_e32 v135, v35
	v_cvt_f32_ubyte2_e32 v137, v35
	v_cvt_f32_ubyte3_e32 v139, v35
	s_lshl_b32 s30, s73, 12
	s_add_u32 s28, s26, s30
	s_addc_u32 s29, s27, 0
	global_load_dwordx2 v[34:35], v162, s[28:29]
	s_waitcnt vmcnt(32)
	v_cvt_f32_ubyte0_e32 v140, v36
	v_cvt_f32_ubyte1_e32 v142, v36
	v_cvt_f32_ubyte2_e32 v144, v36
	v_cvt_f32_ubyte3_e32 v146, v36
	v_cvt_f32_ubyte0_e32 v148, v37
	v_cvt_f32_ubyte1_e32 v150, v37
	v_cvt_f32_ubyte2_e32 v152, v37
	v_cvt_f32_ubyte3_e32 v154, v37
	s_lshl_b32 s30, s74, 12
	s_add_u32 s28, s26, s30
	s_addc_u32 s29, s27, 0
	global_load_dwordx2 v[36:37], v162, s[28:29]
	s_waitcnt vmcnt(32)
	v_cvt_f32_ubyte0_e32 v141, v38
	v_cvt_f32_ubyte1_e32 v143, v38
	v_cvt_f32_ubyte2_e32 v145, v38
	v_cvt_f32_ubyte3_e32 v147, v38
	v_cvt_f32_ubyte0_e32 v149, v39
	v_cvt_f32_ubyte1_e32 v151, v39
	v_cvt_f32_ubyte2_e32 v153, v39
	v_cvt_f32_ubyte3_e32 v155, v39
	s_lshl_b32 s30, s75, 12
	s_add_u32 s28, s26, s30
	s_addc_u32 s29, s27, 0
	global_load_dwordx2 v[38:39], v162, s[28:29]
	v_mul_f32_e32 v182, v124, v108
	v_mul_f32_e32 v183, v125, v108
	v_mul_f32_e32 v184, v140, v108
	v_mul_f32_e32 v185, v141, v108
	v_fmac_f32_e32 v182, v126, v109
	v_fmac_f32_e32 v183, v127, v109
	v_fmac_f32_e32 v184, v142, v109
	v_fmac_f32_e32 v185, v143, v109
	v_fmac_f32_e32 v182, v128, v110
	v_fmac_f32_e32 v183, v129, v110
	v_fmac_f32_e32 v184, v144, v110
	v_fmac_f32_e32 v185, v145, v110
	v_fmac_f32_e32 v182, v130, v111
	v_fmac_f32_e32 v183, v131, v111
	v_fmac_f32_e32 v184, v146, v111
	v_fmac_f32_e32 v185, v147, v111
	v_fmac_f32_e32 v182, v132, v112
	v_fmac_f32_e32 v183, v133, v112
	v_fmac_f32_e32 v184, v148, v112
	v_fmac_f32_e32 v185, v149, v112
	v_fmac_f32_e32 v182, v134, v113
	v_fmac_f32_e32 v183, v135, v113
	v_fmac_f32_e32 v184, v150, v113
	v_fmac_f32_e32 v185, v151, v113
	v_fmac_f32_e32 v182, v136, v114
	v_fmac_f32_e32 v183, v137, v114
	v_fmac_f32_e32 v184, v152, v114
	v_fmac_f32_e32 v185, v153, v114
	v_fmac_f32_e32 v182, v138, v115
	v_fmac_f32_e32 v183, v139, v115
	v_fmac_f32_e32 v184, v154, v115
	v_fmac_f32_e32 v185, v155, v115
	s_waitcnt vmcnt(32)
	v_cvt_f32_ubyte0_e32 v124, v40
	v_cvt_f32_ubyte1_e32 v126, v40
	v_cvt_f32_ubyte2_e32 v128, v40
	v_cvt_f32_ubyte3_e32 v130, v40
	v_cvt_f32_ubyte0_e32 v132, v41
	v_cvt_f32_ubyte1_e32 v134, v41
	v_cvt_f32_ubyte2_e32 v136, v41
	v_cvt_f32_ubyte3_e32 v138, v41
	s_lshl_b32 s30, s76, 12
	s_add_u32 s28, s26, s30
	s_addc_u32 s29, s27, 0
	global_load_dwordx2 v[40:41], v162, s[28:29]
	s_waitcnt vmcnt(32)
	v_cvt_f32_ubyte0_e32 v125, v42
	v_cvt_f32_ubyte1_e32 v127, v42
	v_cvt_f32_ubyte2_e32 v129, v42
	v_cvt_f32_ubyte3_e32 v131, v42
	v_cvt_f32_ubyte0_e32 v133, v43
	v_cvt_f32_ubyte1_e32 v135, v43
	v_cvt_f32_ubyte2_e32 v137, v43
	v_cvt_f32_ubyte3_e32 v139, v43
	s_lshl_b32 s30, s77, 12
	s_add_u32 s28, s26, s30
	s_addc_u32 s29, s27, 0
	global_load_dwordx2 v[42:43], v162, s[28:29]
	s_waitcnt vmcnt(32)
	v_cvt_f32_ubyte0_e32 v140, v44
	v_cvt_f32_ubyte1_e32 v142, v44
	v_cvt_f32_ubyte2_e32 v144, v44
	v_cvt_f32_ubyte3_e32 v146, v44
	v_cvt_f32_ubyte0_e32 v148, v45
	v_cvt_f32_ubyte1_e32 v150, v45
	v_cvt_f32_ubyte2_e32 v152, v45
	v_cvt_f32_ubyte3_e32 v154, v45
	s_lshl_b32 s30, s78, 12
	s_add_u32 s28, s26, s30
	s_addc_u32 s29, s27, 0
	global_load_dwordx2 v[44:45], v162, s[28:29]
	s_waitcnt vmcnt(32)
	v_cvt_f32_ubyte0_e32 v141, v46
	v_cvt_f32_ubyte1_e32 v143, v46
	v_cvt_f32_ubyte2_e32 v145, v46
	v_cvt_f32_ubyte3_e32 v147, v46
	v_cvt_f32_ubyte0_e32 v149, v47
	v_cvt_f32_ubyte1_e32 v151, v47
	v_cvt_f32_ubyte2_e32 v153, v47
	v_cvt_f32_ubyte3_e32 v155, v47
	s_lshl_b32 s30, s79, 12
	s_add_u32 s28, s26, s30
	s_addc_u32 s29, s27, 0
	global_load_dwordx2 v[46:47], v162, s[28:29]
	v_mul_f32_e32 v186, v124, v108
	v_mul_f32_e32 v187, v125, v108
	v_mul_f32_e32 v188, v140, v108
	v_mul_f32_e32 v189, v141, v108
	v_fmac_f32_e32 v186, v126, v109
	v_fmac_f32_e32 v187, v127, v109
	v_fmac_f32_e32 v188, v142, v109
	v_fmac_f32_e32 v189, v143, v109
	v_fmac_f32_e32 v186, v128, v110
	v_fmac_f32_e32 v187, v129, v110
	v_fmac_f32_e32 v188, v144, v110
	v_fmac_f32_e32 v189, v145, v110
	v_fmac_f32_e32 v186, v130, v111
	v_fmac_f32_e32 v187, v131, v111
	v_fmac_f32_e32 v188, v146, v111
	v_fmac_f32_e32 v189, v147, v111
	v_fmac_f32_e32 v186, v132, v112
	v_fmac_f32_e32 v187, v133, v112
	v_fmac_f32_e32 v188, v148, v112
	v_fmac_f32_e32 v189, v149, v112
	v_fmac_f32_e32 v186, v134, v113
	v_fmac_f32_e32 v187, v135, v113
	v_fmac_f32_e32 v188, v150, v113
	v_fmac_f32_e32 v189, v151, v113
	v_fmac_f32_e32 v186, v136, v114
	v_fmac_f32_e32 v187, v137, v114
	v_fmac_f32_e32 v188, v152, v114
	v_fmac_f32_e32 v189, v153, v114
	v_fmac_f32_e32 v186, v138, v115
	v_fmac_f32_e32 v187, v139, v115
	v_fmac_f32_e32 v188, v154, v115
	v_fmac_f32_e32 v189, v155, v115
	s_waitcnt vmcnt(32)
	v_cvt_f32_ubyte0_e32 v124, v48
	v_cvt_f32_ubyte1_e32 v126, v48
	v_cvt_f32_ubyte2_e32 v128, v48
	v_cvt_f32_ubyte3_e32 v130, v48
	v_cvt_f32_ubyte0_e32 v132, v49
	v_cvt_f32_ubyte1_e32 v134, v49
	v_cvt_f32_ubyte2_e32 v136, v49
	v_cvt_f32_ubyte3_e32 v138, v49
	s_lshl_b32 s30, s80, 12
	s_add_u32 s28, s26, s30
	s_addc_u32 s29, s27, 0
	global_load_dwordx2 v[48:49], v162, s[28:29]
	s_waitcnt vmcnt(32)
	v_cvt_f32_ubyte0_e32 v125, v50
	v_cvt_f32_ubyte1_e32 v127, v50
	v_cvt_f32_ubyte2_e32 v129, v50
	v_cvt_f32_ubyte3_e32 v131, v50
	v_cvt_f32_ubyte0_e32 v133, v51
	v_cvt_f32_ubyte1_e32 v135, v51
	v_cvt_f32_ubyte2_e32 v137, v51
	v_cvt_f32_ubyte3_e32 v139, v51
	s_lshl_b32 s30, s81, 12
	s_add_u32 s28, s26, s30
	s_addc_u32 s29, s27, 0
	global_load_dwordx2 v[50:51], v162, s[28:29]
	s_waitcnt vmcnt(32)
	v_cvt_f32_ubyte0_e32 v140, v52
	v_cvt_f32_ubyte1_e32 v142, v52
	v_cvt_f32_ubyte2_e32 v144, v52
	v_cvt_f32_ubyte3_e32 v146, v52
	v_cvt_f32_ubyte0_e32 v148, v53
	v_cvt_f32_ubyte1_e32 v150, v53
	v_cvt_f32_ubyte2_e32 v152, v53
	v_cvt_f32_ubyte3_e32 v154, v53
	s_lshl_b32 s30, s82, 12
	s_add_u32 s28, s26, s30
	s_addc_u32 s29, s27, 0
	global_load_dwordx2 v[52:53], v162, s[28:29]
	s_waitcnt vmcnt(32)
	v_cvt_f32_ubyte0_e32 v141, v54
	v_cvt_f32_ubyte1_e32 v143, v54
	v_cvt_f32_ubyte2_e32 v145, v54
	v_cvt_f32_ubyte3_e32 v147, v54
	v_cvt_f32_ubyte0_e32 v149, v55
	v_cvt_f32_ubyte1_e32 v151, v55
	v_cvt_f32_ubyte2_e32 v153, v55
	v_cvt_f32_ubyte3_e32 v155, v55
	s_lshl_b32 s30, s83, 12
	s_add_u32 s28, s26, s30
	s_addc_u32 s29, s27, 0
	global_load_dwordx2 v[54:55], v162, s[28:29]
	v_mul_f32_e32 v190, v124, v108
	v_mul_f32_e32 v191, v125, v108
	v_mul_f32_e32 v192, v140, v108
	v_mul_f32_e32 v193, v141, v108
	v_fmac_f32_e32 v190, v126, v109
	v_fmac_f32_e32 v191, v127, v109
	v_fmac_f32_e32 v192, v142, v109
	v_fmac_f32_e32 v193, v143, v109
	v_fmac_f32_e32 v190, v128, v110
	v_fmac_f32_e32 v191, v129, v110
	v_fmac_f32_e32 v192, v144, v110
	v_fmac_f32_e32 v193, v145, v110
	v_fmac_f32_e32 v190, v130, v111
	v_fmac_f32_e32 v191, v131, v111
	v_fmac_f32_e32 v192, v146, v111
	v_fmac_f32_e32 v193, v147, v111
	v_fmac_f32_e32 v190, v132, v112
	v_fmac_f32_e32 v191, v133, v112
	v_fmac_f32_e32 v192, v148, v112
	v_fmac_f32_e32 v193, v149, v112
	v_fmac_f32_e32 v190, v134, v113
	v_fmac_f32_e32 v191, v135, v113
	v_fmac_f32_e32 v192, v150, v113
	v_fmac_f32_e32 v193, v151, v113
	v_fmac_f32_e32 v190, v136, v114
	v_fmac_f32_e32 v191, v137, v114
	v_fmac_f32_e32 v192, v152, v114
	v_fmac_f32_e32 v193, v153, v114
	v_fmac_f32_e32 v190, v138, v115
	v_fmac_f32_e32 v191, v139, v115
	v_fmac_f32_e32 v192, v154, v115
	v_fmac_f32_e32 v193, v155, v115
	s_waitcnt vmcnt(32)
	v_cvt_f32_ubyte0_e32 v124, v56
	v_cvt_f32_ubyte1_e32 v126, v56
	v_cvt_f32_ubyte2_e32 v128, v56
	v_cvt_f32_ubyte3_e32 v130, v56
	v_cvt_f32_ubyte0_e32 v132, v57
	v_cvt_f32_ubyte1_e32 v134, v57
	v_cvt_f32_ubyte2_e32 v136, v57
	v_cvt_f32_ubyte3_e32 v138, v57
	s_waitcnt lgkmcnt(0)
	s_load_dwordx16 s[68:83], s[38:39], 0x0
	s_lshl_b32 s30, s84, 12
	s_add_u32 s28, s26, s30
	s_addc_u32 s29, s27, 0
	global_load_dwordx2 v[56:57], v162, s[28:29]
	s_waitcnt vmcnt(32)
	v_cvt_f32_ubyte0_e32 v125, v58
	v_cvt_f32_ubyte1_e32 v127, v58
	v_cvt_f32_ubyte2_e32 v129, v58
	v_cvt_f32_ubyte3_e32 v131, v58
	v_cvt_f32_ubyte0_e32 v133, v59
	v_cvt_f32_ubyte1_e32 v135, v59
	v_cvt_f32_ubyte2_e32 v137, v59
	v_cvt_f32_ubyte3_e32 v139, v59
	s_lshl_b32 s30, s85, 12
	s_add_u32 s28, s26, s30
	s_addc_u32 s29, s27, 0
	global_load_dwordx2 v[58:59], v162, s[28:29]
	s_waitcnt vmcnt(32)
	v_cvt_f32_ubyte0_e32 v140, v60
	v_cvt_f32_ubyte1_e32 v142, v60
	v_cvt_f32_ubyte2_e32 v144, v60
	v_cvt_f32_ubyte3_e32 v146, v60
	v_cvt_f32_ubyte0_e32 v148, v61
	v_cvt_f32_ubyte1_e32 v150, v61
	v_cvt_f32_ubyte2_e32 v152, v61
	v_cvt_f32_ubyte3_e32 v154, v61
	s_lshl_b32 s30, s86, 12
	s_add_u32 s28, s26, s30
	s_addc_u32 s29, s27, 0
	global_load_dwordx2 v[60:61], v162, s[28:29]
	s_waitcnt vmcnt(32)
	v_cvt_f32_ubyte0_e32 v141, v62
	v_cvt_f32_ubyte1_e32 v143, v62
	v_cvt_f32_ubyte2_e32 v145, v62
	v_cvt_f32_ubyte3_e32 v147, v62
	v_cvt_f32_ubyte0_e32 v149, v63
	v_cvt_f32_ubyte1_e32 v151, v63
	v_cvt_f32_ubyte2_e32 v153, v63
	v_cvt_f32_ubyte3_e32 v155, v63
	s_lshl_b32 s30, s87, 12
	s_add_u32 s28, s26, s30
	s_addc_u32 s29, s27, 0
	global_load_dwordx2 v[62:63], v162, s[28:29]
	v_mul_f32_e32 v194, v124, v108
	v_mul_f32_e32 v195, v125, v108
	v_mul_f32_e32 v196, v140, v108
	v_mul_f32_e32 v197, v141, v108
	v_fmac_f32_e32 v194, v126, v109
	v_fmac_f32_e32 v195, v127, v109
	v_fmac_f32_e32 v196, v142, v109
	v_fmac_f32_e32 v197, v143, v109
	v_fmac_f32_e32 v194, v128, v110
	v_fmac_f32_e32 v195, v129, v110
	v_fmac_f32_e32 v196, v144, v110
	v_fmac_f32_e32 v197, v145, v110
	v_fmac_f32_e32 v194, v130, v111
	v_fmac_f32_e32 v195, v131, v111
	v_fmac_f32_e32 v196, v146, v111
	v_fmac_f32_e32 v197, v147, v111
	v_fmac_f32_e32 v194, v132, v112
	v_fmac_f32_e32 v195, v133, v112
	v_fmac_f32_e32 v196, v148, v112
	v_fmac_f32_e32 v197, v149, v112
	v_fmac_f32_e32 v194, v134, v113
	v_fmac_f32_e32 v195, v135, v113
	v_fmac_f32_e32 v196, v150, v113
	v_fmac_f32_e32 v197, v151, v113
	v_fmac_f32_e32 v194, v136, v114
	v_fmac_f32_e32 v195, v137, v114
	v_fmac_f32_e32 v196, v152, v114
	v_fmac_f32_e32 v197, v153, v114
	v_fmac_f32_e32 v194, v138, v115
	v_fmac_f32_e32 v195, v139, v115
	v_fmac_f32_e32 v196, v154, v115
	v_fmac_f32_e32 v197, v155, v115
	s_waitcnt vmcnt(32)
	v_cvt_f32_ubyte0_e32 v124, v64
	v_cvt_f32_ubyte1_e32 v126, v64
	v_cvt_f32_ubyte2_e32 v128, v64
	v_cvt_f32_ubyte3_e32 v130, v64
	v_cvt_f32_ubyte0_e32 v132, v65
	v_cvt_f32_ubyte1_e32 v134, v65
	v_cvt_f32_ubyte2_e32 v136, v65
	v_cvt_f32_ubyte3_e32 v138, v65
	s_lshl_b32 s30, s88, 12
	s_add_u32 s28, s26, s30
	s_addc_u32 s29, s27, 0
	global_load_dwordx2 v[64:65], v162, s[28:29]
	s_waitcnt vmcnt(32)
	v_cvt_f32_ubyte0_e32 v125, v66
	v_cvt_f32_ubyte1_e32 v127, v66
	v_cvt_f32_ubyte2_e32 v129, v66
	v_cvt_f32_ubyte3_e32 v131, v66
	v_cvt_f32_ubyte0_e32 v133, v67
	v_cvt_f32_ubyte1_e32 v135, v67
	v_cvt_f32_ubyte2_e32 v137, v67
	v_cvt_f32_ubyte3_e32 v139, v67
	s_lshl_b32 s30, s89, 12
	s_add_u32 s28, s26, s30
	s_addc_u32 s29, s27, 0
	global_load_dwordx2 v[66:67], v162, s[28:29]
	s_waitcnt vmcnt(32)
	v_cvt_f32_ubyte0_e32 v140, v68
	v_cvt_f32_ubyte1_e32 v142, v68
	v_cvt_f32_ubyte2_e32 v144, v68
	v_cvt_f32_ubyte3_e32 v146, v68
	v_cvt_f32_ubyte0_e32 v148, v69
	v_cvt_f32_ubyte1_e32 v150, v69
	v_cvt_f32_ubyte2_e32 v152, v69
	v_cvt_f32_ubyte3_e32 v154, v69
	s_lshl_b32 s30, s90, 12
	s_add_u32 s28, s26, s30
	s_addc_u32 s29, s27, 0
	global_load_dwordx2 v[68:69], v162, s[28:29]
	s_waitcnt vmcnt(32)
	v_cvt_f32_ubyte0_e32 v141, v70
	v_cvt_f32_ubyte1_e32 v143, v70
	v_cvt_f32_ubyte2_e32 v145, v70
	v_cvt_f32_ubyte3_e32 v147, v70
	v_cvt_f32_ubyte0_e32 v149, v71
	v_cvt_f32_ubyte1_e32 v151, v71
	v_cvt_f32_ubyte2_e32 v153, v71
	v_cvt_f32_ubyte3_e32 v155, v71
	s_lshl_b32 s30, s91, 12
	s_add_u32 s28, s26, s30
	s_addc_u32 s29, s27, 0
	global_load_dwordx2 v[70:71], v162, s[28:29]
	v_mul_f32_e32 v198, v124, v108
	v_mul_f32_e32 v199, v125, v108
	v_mul_f32_e32 v200, v140, v108
	v_mul_f32_e32 v201, v141, v108
	v_fmac_f32_e32 v198, v126, v109
	v_fmac_f32_e32 v199, v127, v109
	v_fmac_f32_e32 v200, v142, v109
	v_fmac_f32_e32 v201, v143, v109
	v_fmac_f32_e32 v198, v128, v110
	v_fmac_f32_e32 v199, v129, v110
	v_fmac_f32_e32 v200, v144, v110
	v_fmac_f32_e32 v201, v145, v110
	v_fmac_f32_e32 v198, v130, v111
	v_fmac_f32_e32 v199, v131, v111
	v_fmac_f32_e32 v200, v146, v111
	v_fmac_f32_e32 v201, v147, v111
	v_fmac_f32_e32 v198, v132, v112
	v_fmac_f32_e32 v199, v133, v112
	v_fmac_f32_e32 v200, v148, v112
	v_fmac_f32_e32 v201, v149, v112
	v_fmac_f32_e32 v198, v134, v113
	v_fmac_f32_e32 v199, v135, v113
	v_fmac_f32_e32 v200, v150, v113
	v_fmac_f32_e32 v201, v151, v113
	v_fmac_f32_e32 v198, v136, v114
	v_fmac_f32_e32 v199, v137, v114
	v_fmac_f32_e32 v200, v152, v114
	v_fmac_f32_e32 v201, v153, v114
	v_fmac_f32_e32 v198, v138, v115
	v_fmac_f32_e32 v199, v139, v115
	v_fmac_f32_e32 v200, v154, v115
	v_fmac_f32_e32 v201, v155, v115
	s_waitcnt vmcnt(32)
	v_cvt_f32_ubyte0_e32 v124, v72
	v_cvt_f32_ubyte1_e32 v126, v72
	v_cvt_f32_ubyte2_e32 v128, v72
	v_cvt_f32_ubyte3_e32 v130, v72
	v_cvt_f32_ubyte0_e32 v132, v73
	v_cvt_f32_ubyte1_e32 v134, v73
	v_cvt_f32_ubyte2_e32 v136, v73
	v_cvt_f32_ubyte3_e32 v138, v73
	s_lshl_b32 s30, s92, 12
	s_add_u32 s28, s26, s30
	s_addc_u32 s29, s27, 0
	global_load_dwordx2 v[72:73], v162, s[28:29]
	s_waitcnt vmcnt(32)
	v_cvt_f32_ubyte0_e32 v125, v74
	v_cvt_f32_ubyte1_e32 v127, v74
	v_cvt_f32_ubyte2_e32 v129, v74
	v_cvt_f32_ubyte3_e32 v131, v74
	v_cvt_f32_ubyte0_e32 v133, v75
	v_cvt_f32_ubyte1_e32 v135, v75
	v_cvt_f32_ubyte2_e32 v137, v75
	v_cvt_f32_ubyte3_e32 v139, v75
	s_lshl_b32 s30, s93, 12
	s_add_u32 s28, s26, s30
	s_addc_u32 s29, s27, 0
	global_load_dwordx2 v[74:75], v162, s[28:29]
	s_waitcnt vmcnt(32)
	v_cvt_f32_ubyte0_e32 v140, v76
	v_cvt_f32_ubyte1_e32 v142, v76
	v_cvt_f32_ubyte2_e32 v144, v76
	v_cvt_f32_ubyte3_e32 v146, v76
	v_cvt_f32_ubyte0_e32 v148, v77
	v_cvt_f32_ubyte1_e32 v150, v77
	v_cvt_f32_ubyte2_e32 v152, v77
	v_cvt_f32_ubyte3_e32 v154, v77
	s_lshl_b32 s30, s94, 12
	s_add_u32 s28, s26, s30
	s_addc_u32 s29, s27, 0
	global_load_dwordx2 v[76:77], v162, s[28:29]
	s_waitcnt vmcnt(32)
	v_cvt_f32_ubyte0_e32 v141, v78
	v_cvt_f32_ubyte1_e32 v143, v78
	v_cvt_f32_ubyte2_e32 v145, v78
	v_cvt_f32_ubyte3_e32 v147, v78
	v_cvt_f32_ubyte0_e32 v149, v79
	v_cvt_f32_ubyte1_e32 v151, v79
	v_cvt_f32_ubyte2_e32 v153, v79
	v_cvt_f32_ubyte3_e32 v155, v79
	s_lshl_b32 s30, s95, 12
	s_add_u32 s28, s26, s30
	s_addc_u32 s29, s27, 0
	global_load_dwordx2 v[78:79], v162, s[28:29]
	v_mul_f32_e32 v202, v124, v108
	v_mul_f32_e32 v203, v125, v108
	v_mul_f32_e32 v204, v140, v108
	v_mul_f32_e32 v205, v141, v108
	v_fmac_f32_e32 v202, v126, v109
	v_fmac_f32_e32 v203, v127, v109
	v_fmac_f32_e32 v204, v142, v109
	v_fmac_f32_e32 v205, v143, v109
	v_fmac_f32_e32 v202, v128, v110
	v_fmac_f32_e32 v203, v129, v110
	v_fmac_f32_e32 v204, v144, v110
	v_fmac_f32_e32 v205, v145, v110
	v_fmac_f32_e32 v202, v130, v111
	v_fmac_f32_e32 v203, v131, v111
	v_fmac_f32_e32 v204, v146, v111
	v_fmac_f32_e32 v205, v147, v111
	v_fmac_f32_e32 v202, v132, v112
	v_fmac_f32_e32 v203, v133, v112
	v_fmac_f32_e32 v204, v148, v112
	v_fmac_f32_e32 v205, v149, v112
	v_fmac_f32_e32 v202, v134, v113
	v_fmac_f32_e32 v203, v135, v113
	v_fmac_f32_e32 v204, v150, v113
	v_fmac_f32_e32 v205, v151, v113
	v_fmac_f32_e32 v202, v136, v114
	v_fmac_f32_e32 v203, v137, v114
	v_fmac_f32_e32 v204, v152, v114
	v_fmac_f32_e32 v205, v153, v114
	v_fmac_f32_e32 v202, v138, v115
	v_fmac_f32_e32 v203, v139, v115
	v_fmac_f32_e32 v204, v154, v115
	v_fmac_f32_e32 v205, v155, v115
	s_waitcnt vmcnt(32)
	v_cvt_f32_ubyte0_e32 v124, v80
	v_cvt_f32_ubyte1_e32 v126, v80
	v_cvt_f32_ubyte2_e32 v128, v80
	v_cvt_f32_ubyte3_e32 v130, v80
	v_cvt_f32_ubyte0_e32 v132, v81
	v_cvt_f32_ubyte1_e32 v134, v81
	v_cvt_f32_ubyte2_e32 v136, v81
	v_cvt_f32_ubyte3_e32 v138, v81
	s_lshl_b32 s30, s96, 12
	s_add_u32 s28, s26, s30
	s_addc_u32 s29, s27, 0
	global_load_dwordx2 v[80:81], v162, s[28:29]
	s_waitcnt vmcnt(32)
	v_cvt_f32_ubyte0_e32 v125, v82
	v_cvt_f32_ubyte1_e32 v127, v82
	v_cvt_f32_ubyte2_e32 v129, v82
	v_cvt_f32_ubyte3_e32 v131, v82
	v_cvt_f32_ubyte0_e32 v133, v83
	v_cvt_f32_ubyte1_e32 v135, v83
	v_cvt_f32_ubyte2_e32 v137, v83
	v_cvt_f32_ubyte3_e32 v139, v83
	s_lshl_b32 s30, s97, 12
	s_add_u32 s28, s26, s30
	s_addc_u32 s29, s27, 0
	global_load_dwordx2 v[82:83], v162, s[28:29]
	s_waitcnt vmcnt(32)
	v_cvt_f32_ubyte0_e32 v140, v84
	v_cvt_f32_ubyte1_e32 v142, v84
	v_cvt_f32_ubyte2_e32 v144, v84
	v_cvt_f32_ubyte3_e32 v146, v84
	v_cvt_f32_ubyte0_e32 v148, v85
	v_cvt_f32_ubyte1_e32 v150, v85
	v_cvt_f32_ubyte2_e32 v152, v85
	v_cvt_f32_ubyte3_e32 v154, v85
	s_lshl_b32 s30, s98, 12
	s_add_u32 s28, s26, s30
	s_addc_u32 s29, s27, 0
	global_load_dwordx2 v[84:85], v162, s[28:29]
	s_waitcnt vmcnt(32)
	v_cvt_f32_ubyte0_e32 v141, v86
	v_cvt_f32_ubyte1_e32 v143, v86
	v_cvt_f32_ubyte2_e32 v145, v86
	v_cvt_f32_ubyte3_e32 v147, v86
	v_cvt_f32_ubyte0_e32 v149, v87
	v_cvt_f32_ubyte1_e32 v151, v87
	v_cvt_f32_ubyte2_e32 v153, v87
	v_cvt_f32_ubyte3_e32 v155, v87
	s_lshl_b32 s30, s99, 12
	s_add_u32 s28, s26, s30
	s_addc_u32 s29, s27, 0
	global_load_dwordx2 v[86:87], v162, s[28:29]
	v_mul_f32_e32 v206, v124, v108
	v_mul_f32_e32 v207, v125, v108
	v_mul_f32_e32 v208, v140, v108
	v_mul_f32_e32 v209, v141, v108
	v_fmac_f32_e32 v206, v126, v109
	v_fmac_f32_e32 v207, v127, v109
	v_fmac_f32_e32 v208, v142, v109
	v_fmac_f32_e32 v209, v143, v109
	v_fmac_f32_e32 v206, v128, v110
	v_fmac_f32_e32 v207, v129, v110
	v_fmac_f32_e32 v208, v144, v110
	v_fmac_f32_e32 v209, v145, v110
	v_fmac_f32_e32 v206, v130, v111
	v_fmac_f32_e32 v207, v131, v111
	v_fmac_f32_e32 v208, v146, v111
	v_fmac_f32_e32 v209, v147, v111
	v_fmac_f32_e32 v206, v132, v112
	v_fmac_f32_e32 v207, v133, v112
	v_fmac_f32_e32 v208, v148, v112
	v_fmac_f32_e32 v209, v149, v112
	v_fmac_f32_e32 v206, v134, v113
	v_fmac_f32_e32 v207, v135, v113
	v_fmac_f32_e32 v208, v150, v113
	v_fmac_f32_e32 v209, v151, v113
	v_fmac_f32_e32 v206, v136, v114
	v_fmac_f32_e32 v207, v137, v114
	v_fmac_f32_e32 v208, v152, v114
	v_fmac_f32_e32 v209, v153, v114
	v_fmac_f32_e32 v206, v138, v115
	v_fmac_f32_e32 v207, v139, v115
	v_fmac_f32_e32 v208, v154, v115
	v_fmac_f32_e32 v209, v155, v115
	v_permlane32_swap_b32_e32 v178, v194
	v_permlane32_swap_b32_e32 v179, v195
	v_permlane32_swap_b32_e32 v180, v196
	v_permlane32_swap_b32_e32 v181, v197
	v_permlane32_swap_b32_e32 v182, v198
	v_permlane32_swap_b32_e32 v183, v199
	v_permlane32_swap_b32_e32 v184, v200
	v_permlane32_swap_b32_e32 v185, v201
	v_permlane32_swap_b32_e32 v186, v202
	v_permlane32_swap_b32_e32 v187, v203
	v_permlane32_swap_b32_e32 v188, v204
	v_permlane32_swap_b32_e32 v189, v205
	v_permlane32_swap_b32_e32 v190, v206
	v_permlane32_swap_b32_e32 v191, v207
	v_permlane32_swap_b32_e32 v192, v208
	v_permlane32_swap_b32_e32 v193, v209
	v_add_f32_e32 v178, v178, v194
	v_add_f32_e32 v179, v179, v195
	v_add_f32_e32 v180, v180, v196
	v_add_f32_e32 v181, v181, v197
	v_add_f32_e32 v182, v182, v198
	v_add_f32_e32 v183, v183, v199
	v_add_f32_e32 v184, v184, v200
	v_add_f32_e32 v185, v185, v201
	v_add_f32_e32 v186, v186, v202
	v_add_f32_e32 v187, v187, v203
	v_add_f32_e32 v188, v188, v204
	v_add_f32_e32 v189, v189, v205
	v_add_f32_e32 v190, v190, v206
	v_add_f32_e32 v191, v191, v207
	v_add_f32_e32 v192, v192, v208
	v_add_f32_e32 v193, v193, v209
	v_permlane16_swap_b32_e32 v178, v186
	v_permlane16_swap_b32_e32 v179, v187
	v_permlane16_swap_b32_e32 v180, v188
	v_permlane16_swap_b32_e32 v181, v189
	v_permlane16_swap_b32_e32 v182, v190
	v_permlane16_swap_b32_e32 v183, v191
	v_permlane16_swap_b32_e32 v184, v192
	v_permlane16_swap_b32_e32 v185, v193
	v_add_f32_e32 v178, v178, v186
	v_add_f32_e32 v179, v179, v187
	v_add_f32_e32 v180, v180, v188
	v_add_f32_e32 v181, v181, v189
	v_add_f32_e32 v182, v182, v190
	v_add_f32_e32 v183, v183, v191
	v_add_f32_e32 v184, v184, v192
	v_add_f32_e32 v185, v185, v193
	v_cndmask_b32_e64 v2, v178, v182, s[8:9]
	v_cndmask_b32_e64 v3, v179, v183, s[8:9]
	v_cndmask_b32_e64 v4, v180, v184, s[8:9]
	v_cndmask_b32_e64 v5, v181, v185, s[8:9]
	v_cndmask_b32_e64 v6, v182, v178, s[8:9]
	v_cndmask_b32_e64 v7, v183, v179, s[8:9]
	v_cndmask_b32_e64 v8, v184, v180, s[8:9]
	v_cndmask_b32_e64 v9, v185, v181, s[8:9]
	v_add_f32_dpp v6, v2, v6 row_ror:8 row_mask:0xf bank_mask:0xf
	v_add_f32_dpp v7, v3, v7 row_ror:8 row_mask:0xf bank_mask:0xf
	v_add_f32_dpp v8, v4, v8 row_ror:8 row_mask:0xf bank_mask:0xf
	v_add_f32_dpp v9, v5, v9 row_ror:8 row_mask:0xf bank_mask:0xf
	v_cndmask_b32_e64 v2, v6, v8, s[10:11]
	v_cndmask_b32_e64 v3, v7, v9, s[10:11]
	v_cndmask_b32_e64 v4, v8, v6, s[10:11]
	v_cndmask_b32_e64 v5, v9, v7, s[10:11]
	v_add_f32_dpp v4, v2, v4 row_half_mirror row_mask:0xf bank_mask:0xf
	v_add_f32_dpp v5, v3, v5 row_half_mirror row_mask:0xf bank_mask:0xf
	v_cndmask_b32_e64 v2, v4, v5, s[14:15]
	v_cndmask_b32_e64 v3, v5, v4, s[14:15]
	s_nop 0
	v_add_f32_dpp v3, v2, v3 quad_perm:[2,3,0,1] row_mask:0xf bank_mask:0xf
	s_nop 1
	v_add_f32_dpp v11, v3, v3 quad_perm:[1,0,3,2] row_mask:0xf bank_mask:0xf
	s_mov_b64 exec, s[2:3]
	global_store_dword v[22:23], v11, off offset:256
	s_mov_b64 exec, -1
	s_waitcnt vmcnt(32)
	v_cvt_f32_ubyte0_e32 v124, v24
	v_cvt_f32_ubyte1_e32 v126, v24
	v_cvt_f32_ubyte2_e32 v128, v24
	v_cvt_f32_ubyte3_e32 v130, v24
	v_cvt_f32_ubyte0_e32 v132, v25
	v_cvt_f32_ubyte1_e32 v134, v25
	v_cvt_f32_ubyte2_e32 v136, v25
	v_cvt_f32_ubyte3_e32 v138, v25
	s_waitcnt vmcnt(31)
	v_cvt_f32_ubyte0_e32 v125, v26
	v_cvt_f32_ubyte1_e32 v127, v26
	v_cvt_f32_ubyte2_e32 v129, v26
	v_cvt_f32_ubyte3_e32 v131, v26
	v_cvt_f32_ubyte0_e32 v133, v27
	v_cvt_f32_ubyte1_e32 v135, v27
	v_cvt_f32_ubyte2_e32 v137, v27
	v_cvt_f32_ubyte3_e32 v139, v27
	s_waitcnt vmcnt(30)
	v_cvt_f32_ubyte0_e32 v140, v28
	v_cvt_f32_ubyte1_e32 v142, v28
	v_cvt_f32_ubyte2_e32 v144, v28
	v_cvt_f32_ubyte3_e32 v146, v28
	v_cvt_f32_ubyte0_e32 v148, v29
	v_cvt_f32_ubyte1_e32 v150, v29
	v_cvt_f32_ubyte2_e32 v152, v29
	v_cvt_f32_ubyte3_e32 v154, v29
	s_waitcnt vmcnt(29)
	v_cvt_f32_ubyte0_e32 v141, v30
	v_cvt_f32_ubyte1_e32 v143, v30
	v_cvt_f32_ubyte2_e32 v145, v30
	v_cvt_f32_ubyte3_e32 v147, v30
	v_cvt_f32_ubyte0_e32 v149, v31
	v_cvt_f32_ubyte1_e32 v151, v31
	v_cvt_f32_ubyte2_e32 v153, v31
	v_cvt_f32_ubyte3_e32 v155, v31
	v_mul_f32_e32 v178, v124, v108
	v_mul_f32_e32 v179, v125, v108
	v_mul_f32_e32 v180, v140, v108
	v_mul_f32_e32 v181, v141, v108
	v_fmac_f32_e32 v178, v126, v109
	v_fmac_f32_e32 v179, v127, v109
	v_fmac_f32_e32 v180, v142, v109
	v_fmac_f32_e32 v181, v143, v109
	v_fmac_f32_e32 v178, v128, v110
	v_fmac_f32_e32 v179, v129, v110
	v_fmac_f32_e32 v180, v144, v110
	v_fmac_f32_e32 v181, v145, v110
	v_fmac_f32_e32 v178, v130, v111
	v_fmac_f32_e32 v179, v131, v111
	v_fmac_f32_e32 v180, v146, v111
	v_fmac_f32_e32 v181, v147, v111
	v_fmac_f32_e32 v178, v132, v112
	v_fmac_f32_e32 v179, v133, v112
	v_fmac_f32_e32 v180, v148, v112
	v_fmac_f32_e32 v181, v149, v112
	v_fmac_f32_e32 v178, v134, v113
	v_fmac_f32_e32 v179, v135, v113
	v_fmac_f32_e32 v180, v150, v113
	v_fmac_f32_e32 v181, v151, v113
	v_fmac_f32_e32 v178, v136, v114
	v_fmac_f32_e32 v179, v137, v114
	v_fmac_f32_e32 v180, v152, v114
	v_fmac_f32_e32 v181, v153, v114
	v_fmac_f32_e32 v178, v138, v115
	v_fmac_f32_e32 v179, v139, v115
	v_fmac_f32_e32 v180, v154, v115
	v_fmac_f32_e32 v181, v155, v115
	s_waitcnt vmcnt(28)
	v_cvt_f32_ubyte0_e32 v124, v32
	v_cvt_f32_ubyte1_e32 v126, v32
	v_cvt_f32_ubyte2_e32 v128, v32
	v_cvt_f32_ubyte3_e32 v130, v32
	v_cvt_f32_ubyte0_e32 v132, v33
	v_cvt_f32_ubyte1_e32 v134, v33
	v_cvt_f32_ubyte2_e32 v136, v33
	v_cvt_f32_ubyte3_e32 v138, v33
	s_waitcnt vmcnt(27)
	v_cvt_f32_ubyte0_e32 v125, v34
	v_cvt_f32_ubyte1_e32 v127, v34
	v_cvt_f32_ubyte2_e32 v129, v34
	v_cvt_f32_ubyte3_e32 v131, v34
	v_cvt_f32_ubyte0_e32 v133, v35
	v_cvt_f32_ubyte1_e32 v135, v35
	v_cvt_f32_ubyte2_e32 v137, v35
	v_cvt_f32_ubyte3_e32 v139, v35
	s_waitcnt vmcnt(26)
	v_cvt_f32_ubyte0_e32 v140, v36
	v_cvt_f32_ubyte1_e32 v142, v36
	v_cvt_f32_ubyte2_e32 v144, v36
	v_cvt_f32_ubyte3_e32 v146, v36
	v_cvt_f32_ubyte0_e32 v148, v37
	v_cvt_f32_ubyte1_e32 v150, v37
	v_cvt_f32_ubyte2_e32 v152, v37
	v_cvt_f32_ubyte3_e32 v154, v37
	s_waitcnt vmcnt(25)
	v_cvt_f32_ubyte0_e32 v141, v38
	v_cvt_f32_ubyte1_e32 v143, v38
	v_cvt_f32_ubyte2_e32 v145, v38
	v_cvt_f32_ubyte3_e32 v147, v38
	v_cvt_f32_ubyte0_e32 v149, v39
	v_cvt_f32_ubyte1_e32 v151, v39
	v_cvt_f32_ubyte2_e32 v153, v39
	v_cvt_f32_ubyte3_e32 v155, v39
	v_mul_f32_e32 v182, v124, v108
	v_mul_f32_e32 v183, v125, v108
	v_mul_f32_e32 v184, v140, v108
	v_mul_f32_e32 v185, v141, v108
	v_fmac_f32_e32 v182, v126, v109
	v_fmac_f32_e32 v183, v127, v109
	v_fmac_f32_e32 v184, v142, v109
	v_fmac_f32_e32 v185, v143, v109
	v_fmac_f32_e32 v182, v128, v110
	v_fmac_f32_e32 v183, v129, v110
	v_fmac_f32_e32 v184, v144, v110
	v_fmac_f32_e32 v185, v145, v110
	v_fmac_f32_e32 v182, v130, v111
	v_fmac_f32_e32 v183, v131, v111
	v_fmac_f32_e32 v184, v146, v111
	v_fmac_f32_e32 v185, v147, v111
	v_fmac_f32_e32 v182, v132, v112
	v_fmac_f32_e32 v183, v133, v112
	v_fmac_f32_e32 v184, v148, v112
	v_fmac_f32_e32 v185, v149, v112
	v_fmac_f32_e32 v182, v134, v113
	v_fmac_f32_e32 v183, v135, v113
	v_fmac_f32_e32 v184, v150, v113
	v_fmac_f32_e32 v185, v151, v113
	v_fmac_f32_e32 v182, v136, v114
	v_fmac_f32_e32 v183, v137, v114
	v_fmac_f32_e32 v184, v152, v114
	v_fmac_f32_e32 v185, v153, v114
	v_fmac_f32_e32 v182, v138, v115
	v_fmac_f32_e32 v183, v139, v115
	v_fmac_f32_e32 v184, v154, v115
	v_fmac_f32_e32 v185, v155, v115
	s_waitcnt vmcnt(24)
	v_cvt_f32_ubyte0_e32 v124, v40
	v_cvt_f32_ubyte1_e32 v126, v40
	v_cvt_f32_ubyte2_e32 v128, v40
	v_cvt_f32_ubyte3_e32 v130, v40
	v_cvt_f32_ubyte0_e32 v132, v41
	v_cvt_f32_ubyte1_e32 v134, v41
	v_cvt_f32_ubyte2_e32 v136, v41
	v_cvt_f32_ubyte3_e32 v138, v41
	s_waitcnt vmcnt(23)
	v_cvt_f32_ubyte0_e32 v125, v42
	v_cvt_f32_ubyte1_e32 v127, v42
	v_cvt_f32_ubyte2_e32 v129, v42
	v_cvt_f32_ubyte3_e32 v131, v42
	v_cvt_f32_ubyte0_e32 v133, v43
	v_cvt_f32_ubyte1_e32 v135, v43
	v_cvt_f32_ubyte2_e32 v137, v43
	v_cvt_f32_ubyte3_e32 v139, v43
	s_waitcnt vmcnt(22)
	v_cvt_f32_ubyte0_e32 v140, v44
	v_cvt_f32_ubyte1_e32 v142, v44
	v_cvt_f32_ubyte2_e32 v144, v44
	v_cvt_f32_ubyte3_e32 v146, v44
	v_cvt_f32_ubyte0_e32 v148, v45
	v_cvt_f32_ubyte1_e32 v150, v45
	v_cvt_f32_ubyte2_e32 v152, v45
	v_cvt_f32_ubyte3_e32 v154, v45
	s_waitcnt vmcnt(21)
	v_cvt_f32_ubyte0_e32 v141, v46
	v_cvt_f32_ubyte1_e32 v143, v46
	v_cvt_f32_ubyte2_e32 v145, v46
	v_cvt_f32_ubyte3_e32 v147, v46
	v_cvt_f32_ubyte0_e32 v149, v47
	v_cvt_f32_ubyte1_e32 v151, v47
	v_cvt_f32_ubyte2_e32 v153, v47
	v_cvt_f32_ubyte3_e32 v155, v47
	v_mul_f32_e32 v186, v124, v108
	v_mul_f32_e32 v187, v125, v108
	v_mul_f32_e32 v188, v140, v108
	v_mul_f32_e32 v189, v141, v108
	v_fmac_f32_e32 v186, v126, v109
	v_fmac_f32_e32 v187, v127, v109
	v_fmac_f32_e32 v188, v142, v109
	v_fmac_f32_e32 v189, v143, v109
	v_fmac_f32_e32 v186, v128, v110
	v_fmac_f32_e32 v187, v129, v110
	v_fmac_f32_e32 v188, v144, v110
	v_fmac_f32_e32 v189, v145, v110
	v_fmac_f32_e32 v186, v130, v111
	v_fmac_f32_e32 v187, v131, v111
	v_fmac_f32_e32 v188, v146, v111
	v_fmac_f32_e32 v189, v147, v111
	v_fmac_f32_e32 v186, v132, v112
	v_fmac_f32_e32 v187, v133, v112
	v_fmac_f32_e32 v188, v148, v112
	v_fmac_f32_e32 v189, v149, v112
	v_fmac_f32_e32 v186, v134, v113
	v_fmac_f32_e32 v187, v135, v113
	v_fmac_f32_e32 v188, v150, v113
	v_fmac_f32_e32 v189, v151, v113
	v_fmac_f32_e32 v186, v136, v114
	v_fmac_f32_e32 v187, v137, v114
	v_fmac_f32_e32 v188, v152, v114
	v_fmac_f32_e32 v189, v153, v114
	v_fmac_f32_e32 v186, v138, v115
	v_fmac_f32_e32 v187, v139, v115
	v_fmac_f32_e32 v188, v154, v115
	v_fmac_f32_e32 v189, v155, v115
	s_waitcnt vmcnt(20)
	v_cvt_f32_ubyte0_e32 v124, v48
	v_cvt_f32_ubyte1_e32 v126, v48
	v_cvt_f32_ubyte2_e32 v128, v48
	v_cvt_f32_ubyte3_e32 v130, v48
	v_cvt_f32_ubyte0_e32 v132, v49
	v_cvt_f32_ubyte1_e32 v134, v49
	v_cvt_f32_ubyte2_e32 v136, v49
	v_cvt_f32_ubyte3_e32 v138, v49
	s_waitcnt vmcnt(19)
	v_cvt_f32_ubyte0_e32 v125, v50
	v_cvt_f32_ubyte1_e32 v127, v50
	v_cvt_f32_ubyte2_e32 v129, v50
	v_cvt_f32_ubyte3_e32 v131, v50
	v_cvt_f32_ubyte0_e32 v133, v51
	v_cvt_f32_ubyte1_e32 v135, v51
	v_cvt_f32_ubyte2_e32 v137, v51
	v_cvt_f32_ubyte3_e32 v139, v51
	s_waitcnt vmcnt(18)
	v_cvt_f32_ubyte0_e32 v140, v52
	v_cvt_f32_ubyte1_e32 v142, v52
	v_cvt_f32_ubyte2_e32 v144, v52
	v_cvt_f32_ubyte3_e32 v146, v52
	v_cvt_f32_ubyte0_e32 v148, v53
	v_cvt_f32_ubyte1_e32 v150, v53
	v_cvt_f32_ubyte2_e32 v152, v53
	v_cvt_f32_ubyte3_e32 v154, v53
	s_waitcnt vmcnt(17)
	v_cvt_f32_ubyte0_e32 v141, v54
	v_cvt_f32_ubyte1_e32 v143, v54
	v_cvt_f32_ubyte2_e32 v145, v54
	v_cvt_f32_ubyte3_e32 v147, v54
	v_cvt_f32_ubyte0_e32 v149, v55
	v_cvt_f32_ubyte1_e32 v151, v55
	v_cvt_f32_ubyte2_e32 v153, v55
	v_cvt_f32_ubyte3_e32 v155, v55
	v_mul_f32_e32 v190, v124, v108
	v_mul_f32_e32 v191, v125, v108
	v_mul_f32_e32 v192, v140, v108
	v_mul_f32_e32 v193, v141, v108
	v_fmac_f32_e32 v190, v126, v109
	v_fmac_f32_e32 v191, v127, v109
	v_fmac_f32_e32 v192, v142, v109
	v_fmac_f32_e32 v193, v143, v109
	v_fmac_f32_e32 v190, v128, v110
	v_fmac_f32_e32 v191, v129, v110
	v_fmac_f32_e32 v192, v144, v110
	v_fmac_f32_e32 v193, v145, v110
	v_fmac_f32_e32 v190, v130, v111
	v_fmac_f32_e32 v191, v131, v111
	v_fmac_f32_e32 v192, v146, v111
	v_fmac_f32_e32 v193, v147, v111
	v_fmac_f32_e32 v190, v132, v112
	v_fmac_f32_e32 v191, v133, v112
	v_fmac_f32_e32 v192, v148, v112
	v_fmac_f32_e32 v193, v149, v112
	v_fmac_f32_e32 v190, v134, v113
	v_fmac_f32_e32 v191, v135, v113
	v_fmac_f32_e32 v192, v150, v113
	v_fmac_f32_e32 v193, v151, v113
	v_fmac_f32_e32 v190, v136, v114
	v_fmac_f32_e32 v191, v137, v114
	v_fmac_f32_e32 v192, v152, v114
	v_fmac_f32_e32 v193, v153, v114
	v_fmac_f32_e32 v190, v138, v115
	v_fmac_f32_e32 v191, v139, v115
	v_fmac_f32_e32 v192, v154, v115
	v_fmac_f32_e32 v193, v155, v115
	s_waitcnt vmcnt(16)
	v_cvt_f32_ubyte0_e32 v124, v56
	v_cvt_f32_ubyte1_e32 v126, v56
	v_cvt_f32_ubyte2_e32 v128, v56
	v_cvt_f32_ubyte3_e32 v130, v56
	v_cvt_f32_ubyte0_e32 v132, v57
	v_cvt_f32_ubyte1_e32 v134, v57
	v_cvt_f32_ubyte2_e32 v136, v57
	v_cvt_f32_ubyte3_e32 v138, v57
	s_waitcnt vmcnt(15)
	v_cvt_f32_ubyte0_e32 v125, v58
	v_cvt_f32_ubyte1_e32 v127, v58
	v_cvt_f32_ubyte2_e32 v129, v58
	v_cvt_f32_ubyte3_e32 v131, v58
	v_cvt_f32_ubyte0_e32 v133, v59
	v_cvt_f32_ubyte1_e32 v135, v59
	v_cvt_f32_ubyte2_e32 v137, v59
	v_cvt_f32_ubyte3_e32 v139, v59
	s_waitcnt vmcnt(14)
	v_cvt_f32_ubyte0_e32 v140, v60
	v_cvt_f32_ubyte1_e32 v142, v60
	v_cvt_f32_ubyte2_e32 v144, v60
	v_cvt_f32_ubyte3_e32 v146, v60
	v_cvt_f32_ubyte0_e32 v148, v61
	v_cvt_f32_ubyte1_e32 v150, v61
	v_cvt_f32_ubyte2_e32 v152, v61
	v_cvt_f32_ubyte3_e32 v154, v61
	s_waitcnt vmcnt(13)
	v_cvt_f32_ubyte0_e32 v141, v62
	v_cvt_f32_ubyte1_e32 v143, v62
	v_cvt_f32_ubyte2_e32 v145, v62
	v_cvt_f32_ubyte3_e32 v147, v62
	v_cvt_f32_ubyte0_e32 v149, v63
	v_cvt_f32_ubyte1_e32 v151, v63
	v_cvt_f32_ubyte2_e32 v153, v63
	v_cvt_f32_ubyte3_e32 v155, v63
	v_mul_f32_e32 v194, v124, v108
	v_mul_f32_e32 v195, v125, v108
	v_mul_f32_e32 v196, v140, v108
	v_mul_f32_e32 v197, v141, v108
	v_fmac_f32_e32 v194, v126, v109
	v_fmac_f32_e32 v195, v127, v109
	v_fmac_f32_e32 v196, v142, v109
	v_fmac_f32_e32 v197, v143, v109
	v_fmac_f32_e32 v194, v128, v110
	v_fmac_f32_e32 v195, v129, v110
	v_fmac_f32_e32 v196, v144, v110
	v_fmac_f32_e32 v197, v145, v110
	v_fmac_f32_e32 v194, v130, v111
	v_fmac_f32_e32 v195, v131, v111
	v_fmac_f32_e32 v196, v146, v111
	v_fmac_f32_e32 v197, v147, v111
	v_fmac_f32_e32 v194, v132, v112
	v_fmac_f32_e32 v195, v133, v112
	v_fmac_f32_e32 v196, v148, v112
	v_fmac_f32_e32 v197, v149, v112
	v_fmac_f32_e32 v194, v134, v113
	v_fmac_f32_e32 v195, v135, v113
	v_fmac_f32_e32 v196, v150, v113
	v_fmac_f32_e32 v197, v151, v113
	v_fmac_f32_e32 v194, v136, v114
	v_fmac_f32_e32 v195, v137, v114
	v_fmac_f32_e32 v196, v152, v114
	v_fmac_f32_e32 v197, v153, v114
	v_fmac_f32_e32 v194, v138, v115
	v_fmac_f32_e32 v195, v139, v115
	v_fmac_f32_e32 v196, v154, v115
	v_fmac_f32_e32 v197, v155, v115
	s_waitcnt vmcnt(12)
	v_cvt_f32_ubyte0_e32 v124, v64
	v_cvt_f32_ubyte1_e32 v126, v64
	v_cvt_f32_ubyte2_e32 v128, v64
	v_cvt_f32_ubyte3_e32 v130, v64
	v_cvt_f32_ubyte0_e32 v132, v65
	v_cvt_f32_ubyte1_e32 v134, v65
	v_cvt_f32_ubyte2_e32 v136, v65
	v_cvt_f32_ubyte3_e32 v138, v65
	s_waitcnt vmcnt(11)
	v_cvt_f32_ubyte0_e32 v125, v66
	v_cvt_f32_ubyte1_e32 v127, v66
	v_cvt_f32_ubyte2_e32 v129, v66
	v_cvt_f32_ubyte3_e32 v131, v66
	v_cvt_f32_ubyte0_e32 v133, v67
	v_cvt_f32_ubyte1_e32 v135, v67
	v_cvt_f32_ubyte2_e32 v137, v67
	v_cvt_f32_ubyte3_e32 v139, v67
	s_waitcnt vmcnt(10)
	v_cvt_f32_ubyte0_e32 v140, v68
	v_cvt_f32_ubyte1_e32 v142, v68
	v_cvt_f32_ubyte2_e32 v144, v68
	v_cvt_f32_ubyte3_e32 v146, v68
	v_cvt_f32_ubyte0_e32 v148, v69
	v_cvt_f32_ubyte1_e32 v150, v69
	v_cvt_f32_ubyte2_e32 v152, v69
	v_cvt_f32_ubyte3_e32 v154, v69
	s_waitcnt vmcnt(9)
	v_cvt_f32_ubyte0_e32 v141, v70
	v_cvt_f32_ubyte1_e32 v143, v70
	v_cvt_f32_ubyte2_e32 v145, v70
	v_cvt_f32_ubyte3_e32 v147, v70
	v_cvt_f32_ubyte0_e32 v149, v71
	v_cvt_f32_ubyte1_e32 v151, v71
	v_cvt_f32_ubyte2_e32 v153, v71
	v_cvt_f32_ubyte3_e32 v155, v71
	v_mul_f32_e32 v198, v124, v108
	v_mul_f32_e32 v199, v125, v108
	v_mul_f32_e32 v200, v140, v108
	v_mul_f32_e32 v201, v141, v108
	v_fmac_f32_e32 v198, v126, v109
	v_fmac_f32_e32 v199, v127, v109
	v_fmac_f32_e32 v200, v142, v109
	v_fmac_f32_e32 v201, v143, v109
	v_fmac_f32_e32 v198, v128, v110
	v_fmac_f32_e32 v199, v129, v110
	v_fmac_f32_e32 v200, v144, v110
	v_fmac_f32_e32 v201, v145, v110
	v_fmac_f32_e32 v198, v130, v111
	v_fmac_f32_e32 v199, v131, v111
	v_fmac_f32_e32 v200, v146, v111
	v_fmac_f32_e32 v201, v147, v111
	v_fmac_f32_e32 v198, v132, v112
	v_fmac_f32_e32 v199, v133, v112
	v_fmac_f32_e32 v200, v148, v112
	v_fmac_f32_e32 v201, v149, v112
	v_fmac_f32_e32 v198, v134, v113
	v_fmac_f32_e32 v199, v135, v113
	v_fmac_f32_e32 v200, v150, v113
	v_fmac_f32_e32 v201, v151, v113
	v_fmac_f32_e32 v198, v136, v114
	v_fmac_f32_e32 v199, v137, v114
	v_fmac_f32_e32 v200, v152, v114
	v_fmac_f32_e32 v201, v153, v114
	v_fmac_f32_e32 v198, v138, v115
	v_fmac_f32_e32 v199, v139, v115
	v_fmac_f32_e32 v200, v154, v115
	v_fmac_f32_e32 v201, v155, v115
	s_waitcnt vmcnt(8)
	v_cvt_f32_ubyte0_e32 v124, v72
	v_cvt_f32_ubyte1_e32 v126, v72
	v_cvt_f32_ubyte2_e32 v128, v72
	v_cvt_f32_ubyte3_e32 v130, v72
	v_cvt_f32_ubyte0_e32 v132, v73
	v_cvt_f32_ubyte1_e32 v134, v73
	v_cvt_f32_ubyte2_e32 v136, v73
	v_cvt_f32_ubyte3_e32 v138, v73
	s_waitcnt vmcnt(7)
	v_cvt_f32_ubyte0_e32 v125, v74
	v_cvt_f32_ubyte1_e32 v127, v74
	v_cvt_f32_ubyte2_e32 v129, v74
	v_cvt_f32_ubyte3_e32 v131, v74
	v_cvt_f32_ubyte0_e32 v133, v75
	v_cvt_f32_ubyte1_e32 v135, v75
	v_cvt_f32_ubyte2_e32 v137, v75
	v_cvt_f32_ubyte3_e32 v139, v75
	s_waitcnt vmcnt(6)
	v_cvt_f32_ubyte0_e32 v140, v76
	v_cvt_f32_ubyte1_e32 v142, v76
	v_cvt_f32_ubyte2_e32 v144, v76
	v_cvt_f32_ubyte3_e32 v146, v76
	v_cvt_f32_ubyte0_e32 v148, v77
	v_cvt_f32_ubyte1_e32 v150, v77
	v_cvt_f32_ubyte2_e32 v152, v77
	v_cvt_f32_ubyte3_e32 v154, v77
	s_waitcnt vmcnt(5)
	v_cvt_f32_ubyte0_e32 v141, v78
	v_cvt_f32_ubyte1_e32 v143, v78
	v_cvt_f32_ubyte2_e32 v145, v78
	v_cvt_f32_ubyte3_e32 v147, v78
	v_cvt_f32_ubyte0_e32 v149, v79
	v_cvt_f32_ubyte1_e32 v151, v79
	v_cvt_f32_ubyte2_e32 v153, v79
	v_cvt_f32_ubyte3_e32 v155, v79
	v_mul_f32_e32 v202, v124, v108
	v_mul_f32_e32 v203, v125, v108
	v_mul_f32_e32 v204, v140, v108
	v_mul_f32_e32 v205, v141, v108
	v_fmac_f32_e32 v202, v126, v109
	v_fmac_f32_e32 v203, v127, v109
	v_fmac_f32_e32 v204, v142, v109
	v_fmac_f32_e32 v205, v143, v109
	v_fmac_f32_e32 v202, v128, v110
	v_fmac_f32_e32 v203, v129, v110
	v_fmac_f32_e32 v204, v144, v110
	v_fmac_f32_e32 v205, v145, v110
	v_fmac_f32_e32 v202, v130, v111
	v_fmac_f32_e32 v203, v131, v111
	v_fmac_f32_e32 v204, v146, v111
	v_fmac_f32_e32 v205, v147, v111
	v_fmac_f32_e32 v202, v132, v112
	v_fmac_f32_e32 v203, v133, v112
	v_fmac_f32_e32 v204, v148, v112
	v_fmac_f32_e32 v205, v149, v112
	v_fmac_f32_e32 v202, v134, v113
	v_fmac_f32_e32 v203, v135, v113
	v_fmac_f32_e32 v204, v150, v113
	v_fmac_f32_e32 v205, v151, v113
	v_fmac_f32_e32 v202, v136, v114
	v_fmac_f32_e32 v203, v137, v114
	v_fmac_f32_e32 v204, v152, v114
	v_fmac_f32_e32 v205, v153, v114
	v_fmac_f32_e32 v202, v138, v115
	v_fmac_f32_e32 v203, v139, v115
	v_fmac_f32_e32 v204, v154, v115
	v_fmac_f32_e32 v205, v155, v115
	s_waitcnt vmcnt(4)
	v_cvt_f32_ubyte0_e32 v124, v80
	v_cvt_f32_ubyte1_e32 v126, v80
	v_cvt_f32_ubyte2_e32 v128, v80
	v_cvt_f32_ubyte3_e32 v130, v80
	v_cvt_f32_ubyte0_e32 v132, v81
	v_cvt_f32_ubyte1_e32 v134, v81
	v_cvt_f32_ubyte2_e32 v136, v81
	v_cvt_f32_ubyte3_e32 v138, v81
	s_waitcnt vmcnt(3)
	v_cvt_f32_ubyte0_e32 v125, v82
	v_cvt_f32_ubyte1_e32 v127, v82
	v_cvt_f32_ubyte2_e32 v129, v82
	v_cvt_f32_ubyte3_e32 v131, v82
	v_cvt_f32_ubyte0_e32 v133, v83
	v_cvt_f32_ubyte1_e32 v135, v83
	v_cvt_f32_ubyte2_e32 v137, v83
	v_cvt_f32_ubyte3_e32 v139, v83
	s_waitcnt vmcnt(2)
	v_cvt_f32_ubyte0_e32 v140, v84
	v_cvt_f32_ubyte1_e32 v142, v84
	v_cvt_f32_ubyte2_e32 v144, v84
	v_cvt_f32_ubyte3_e32 v146, v84
	v_cvt_f32_ubyte0_e32 v148, v85
	v_cvt_f32_ubyte1_e32 v150, v85
	v_cvt_f32_ubyte2_e32 v152, v85
	v_cvt_f32_ubyte3_e32 v154, v85
	s_waitcnt vmcnt(1)
	v_cvt_f32_ubyte0_e32 v141, v86
	v_cvt_f32_ubyte1_e32 v143, v86
	v_cvt_f32_ubyte2_e32 v145, v86
	v_cvt_f32_ubyte3_e32 v147, v86
	v_cvt_f32_ubyte0_e32 v149, v87
	v_cvt_f32_ubyte1_e32 v151, v87
	v_cvt_f32_ubyte2_e32 v153, v87
	v_cvt_f32_ubyte3_e32 v155, v87
	v_mul_f32_e32 v206, v124, v108
	v_mul_f32_e32 v207, v125, v108
	v_mul_f32_e32 v208, v140, v108
	v_mul_f32_e32 v209, v141, v108
	v_fmac_f32_e32 v206, v126, v109
	v_fmac_f32_e32 v207, v127, v109
	v_fmac_f32_e32 v208, v142, v109
	v_fmac_f32_e32 v209, v143, v109
	v_fmac_f32_e32 v206, v128, v110
	v_fmac_f32_e32 v207, v129, v110
	v_fmac_f32_e32 v208, v144, v110
	v_fmac_f32_e32 v209, v145, v110
	v_fmac_f32_e32 v206, v130, v111
	v_fmac_f32_e32 v207, v131, v111
	v_fmac_f32_e32 v208, v146, v111
	v_fmac_f32_e32 v209, v147, v111
	v_fmac_f32_e32 v206, v132, v112
	v_fmac_f32_e32 v207, v133, v112
	v_fmac_f32_e32 v208, v148, v112
	v_fmac_f32_e32 v209, v149, v112
	v_fmac_f32_e32 v206, v134, v113
	v_fmac_f32_e32 v207, v135, v113
	v_fmac_f32_e32 v208, v150, v113
	v_fmac_f32_e32 v209, v151, v113
	v_fmac_f32_e32 v206, v136, v114
	v_fmac_f32_e32 v207, v137, v114
	v_fmac_f32_e32 v208, v152, v114
	v_fmac_f32_e32 v209, v153, v114
	v_fmac_f32_e32 v206, v138, v115
	v_fmac_f32_e32 v207, v139, v115
	v_fmac_f32_e32 v208, v154, v115
	v_fmac_f32_e32 v209, v155, v115
	s_waitcnt lgkmcnt(0)
	s_load_dwordx16 s[84:99], s[38:39], 0x40
	s_lshl_b32 s30, s68, 12
	s_add_u32 s28, s26, s30
	s_addc_u32 s29, s27, 0
	global_load_dwordx2 v[24:25], v162, s[28:29]
	s_lshl_b32 s30, s69, 12
	s_add_u32 s28, s26, s30
	s_addc_u32 s29, s27, 0
	global_load_dwordx2 v[26:27], v162, s[28:29]
	s_lshl_b32 s30, s70, 12
	s_add_u32 s28, s26, s30
	s_addc_u32 s29, s27, 0
	global_load_dwordx2 v[28:29], v162, s[28:29]
	s_lshl_b32 s30, s71, 12
	s_add_u32 s28, s26, s30
	s_addc_u32 s29, s27, 0
	global_load_dwordx2 v[30:31], v162, s[28:29]
	s_lshl_b32 s30, s72, 12
	s_add_u32 s28, s26, s30
	s_addc_u32 s29, s27, 0
	global_load_dwordx2 v[32:33], v162, s[28:29]
	s_lshl_b32 s30, s73, 12
	s_add_u32 s28, s26, s30
	s_addc_u32 s29, s27, 0
	global_load_dwordx2 v[34:35], v162, s[28:29]
	s_lshl_b32 s30, s74, 12
	s_add_u32 s28, s26, s30
	s_addc_u32 s29, s27, 0
	global_load_dwordx2 v[36:37], v162, s[28:29]
	s_lshl_b32 s30, s75, 12
	s_add_u32 s28, s26, s30
	s_addc_u32 s29, s27, 0
	global_load_dwordx2 v[38:39], v162, s[28:29]
	s_lshl_b32 s30, s76, 12
	s_add_u32 s28, s26, s30
	s_addc_u32 s29, s27, 0
	global_load_dwordx2 v[40:41], v162, s[28:29]
	s_lshl_b32 s30, s77, 12
	s_add_u32 s28, s26, s30
	s_addc_u32 s29, s27, 0
	global_load_dwordx2 v[42:43], v162, s[28:29]
	s_lshl_b32 s30, s78, 12
	s_add_u32 s28, s26, s30
	s_addc_u32 s29, s27, 0
	global_load_dwordx2 v[44:45], v162, s[28:29]
	s_lshl_b32 s30, s79, 12
	s_add_u32 s28, s26, s30
	s_addc_u32 s29, s27, 0
	global_load_dwordx2 v[46:47], v162, s[28:29]
	s_lshl_b32 s30, s80, 12
	s_add_u32 s28, s26, s30
	s_addc_u32 s29, s27, 0
	global_load_dwordx2 v[48:49], v162, s[28:29]
	s_lshl_b32 s30, s81, 12
	s_add_u32 s28, s26, s30
	s_addc_u32 s29, s27, 0
	global_load_dwordx2 v[50:51], v162, s[28:29]
	s_lshl_b32 s30, s82, 12
	s_add_u32 s28, s26, s30
	s_addc_u32 s29, s27, 0
	global_load_dwordx2 v[52:53], v162, s[28:29]
	s_lshl_b32 s30, s83, 12
	s_add_u32 s28, s26, s30
	s_addc_u32 s29, s27, 0
	global_load_dwordx2 v[54:55], v162, s[28:29]
	s_waitcnt lgkmcnt(0)
	s_load_dwordx16 s[68:83], s[38:39], 0x80
	s_lshl_b32 s30, s84, 12
	s_add_u32 s28, s26, s30
	s_addc_u32 s29, s27, 0
	global_load_dwordx2 v[56:57], v162, s[28:29]
	s_lshl_b32 s30, s85, 12
	s_add_u32 s28, s26, s30
	s_addc_u32 s29, s27, 0
	global_load_dwordx2 v[58:59], v162, s[28:29]
	s_lshl_b32 s30, s86, 12
	s_add_u32 s28, s26, s30
	s_addc_u32 s29, s27, 0
	global_load_dwordx2 v[60:61], v162, s[28:29]
	s_lshl_b32 s30, s87, 12
	s_add_u32 s28, s26, s30
	s_addc_u32 s29, s27, 0
	global_load_dwordx2 v[62:63], v162, s[28:29]
	s_lshl_b32 s30, s88, 12
	s_add_u32 s28, s26, s30
	s_addc_u32 s29, s27, 0
	global_load_dwordx2 v[64:65], v162, s[28:29]
	s_lshl_b32 s30, s89, 12
	s_add_u32 s28, s26, s30
	s_addc_u32 s29, s27, 0
	global_load_dwordx2 v[66:67], v162, s[28:29]
	s_lshl_b32 s30, s90, 12
	s_add_u32 s28, s26, s30
	s_addc_u32 s29, s27, 0
	global_load_dwordx2 v[68:69], v162, s[28:29]
	s_lshl_b32 s30, s91, 12
	s_add_u32 s28, s26, s30
	s_addc_u32 s29, s27, 0
	global_load_dwordx2 v[70:71], v162, s[28:29]
	s_lshl_b32 s30, s92, 12
	s_add_u32 s28, s26, s30
	s_addc_u32 s29, s27, 0
	global_load_dwordx2 v[72:73], v162, s[28:29]
	s_lshl_b32 s30, s93, 12
	s_add_u32 s28, s26, s30
	s_addc_u32 s29, s27, 0
	global_load_dwordx2 v[74:75], v162, s[28:29]
	s_lshl_b32 s30, s94, 12
	s_add_u32 s28, s26, s30
	s_addc_u32 s29, s27, 0
	global_load_dwordx2 v[76:77], v162, s[28:29]
	s_lshl_b32 s30, s95, 12
	s_add_u32 s28, s26, s30
	s_addc_u32 s29, s27, 0
	global_load_dwordx2 v[78:79], v162, s[28:29]
	s_lshl_b32 s30, s96, 12
	s_add_u32 s28, s26, s30
	s_addc_u32 s29, s27, 0
	global_load_dwordx2 v[80:81], v162, s[28:29]
	s_lshl_b32 s30, s97, 12
	s_add_u32 s28, s26, s30
	s_addc_u32 s29, s27, 0
	global_load_dwordx2 v[82:83], v162, s[28:29]
	s_lshl_b32 s30, s98, 12
	s_add_u32 s28, s26, s30
	s_addc_u32 s29, s27, 0
	global_load_dwordx2 v[84:85], v162, s[28:29]
	s_lshl_b32 s30, s99, 12
	s_add_u32 s28, s26, s30
	s_addc_u32 s29, s27, 0
	global_load_dwordx2 v[86:87], v162, s[28:29]
	v_permlane32_swap_b32_e32 v178, v194
	v_permlane32_swap_b32_e32 v179, v195
	v_permlane32_swap_b32_e32 v180, v196
	v_permlane32_swap_b32_e32 v181, v197
	v_permlane32_swap_b32_e32 v182, v198
	v_permlane32_swap_b32_e32 v183, v199
	v_permlane32_swap_b32_e32 v184, v200
	v_permlane32_swap_b32_e32 v185, v201
	v_permlane32_swap_b32_e32 v186, v202
	v_permlane32_swap_b32_e32 v187, v203
	v_permlane32_swap_b32_e32 v188, v204
	v_permlane32_swap_b32_e32 v189, v205
	v_permlane32_swap_b32_e32 v190, v206
	v_permlane32_swap_b32_e32 v191, v207
	v_permlane32_swap_b32_e32 v192, v208
	v_permlane32_swap_b32_e32 v193, v209
	v_add_f32_e32 v178, v178, v194
	v_add_f32_e32 v179, v179, v195
	v_add_f32_e32 v180, v180, v196
	v_add_f32_e32 v181, v181, v197
	v_add_f32_e32 v182, v182, v198
	v_add_f32_e32 v183, v183, v199
	v_add_f32_e32 v184, v184, v200
	v_add_f32_e32 v185, v185, v201
	v_add_f32_e32 v186, v186, v202
	v_add_f32_e32 v187, v187, v203
	v_add_f32_e32 v188, v188, v204
	v_add_f32_e32 v189, v189, v205
	v_add_f32_e32 v190, v190, v206
	v_add_f32_e32 v191, v191, v207
	v_add_f32_e32 v192, v192, v208
	v_add_f32_e32 v193, v193, v209
	v_permlane16_swap_b32_e32 v178, v186
	v_permlane16_swap_b32_e32 v179, v187
	v_permlane16_swap_b32_e32 v180, v188
	v_permlane16_swap_b32_e32 v181, v189
	v_permlane16_swap_b32_e32 v182, v190
	v_permlane16_swap_b32_e32 v183, v191
	v_permlane16_swap_b32_e32 v184, v192
	v_permlane16_swap_b32_e32 v185, v193
	v_add_f32_e32 v178, v178, v186
	v_add_f32_e32 v179, v179, v187
	v_add_f32_e32 v180, v180, v188
	v_add_f32_e32 v181, v181, v189
	v_add_f32_e32 v182, v182, v190
	v_add_f32_e32 v183, v183, v191
	v_add_f32_e32 v184, v184, v192
	v_add_f32_e32 v185, v185, v193
	v_cndmask_b32_e64 v2, v178, v182, s[8:9]
	v_cndmask_b32_e64 v3, v179, v183, s[8:9]
	v_cndmask_b32_e64 v4, v180, v184, s[8:9]
	v_cndmask_b32_e64 v5, v181, v185, s[8:9]
	v_cndmask_b32_e64 v6, v182, v178, s[8:9]
	v_cndmask_b32_e64 v7, v183, v179, s[8:9]
	v_cndmask_b32_e64 v8, v184, v180, s[8:9]
	v_cndmask_b32_e64 v9, v185, v181, s[8:9]
	v_add_f32_dpp v6, v2, v6 row_ror:8 row_mask:0xf bank_mask:0xf
	v_add_f32_dpp v7, v3, v7 row_ror:8 row_mask:0xf bank_mask:0xf
	v_add_f32_dpp v8, v4, v8 row_ror:8 row_mask:0xf bank_mask:0xf
	v_add_f32_dpp v9, v5, v9 row_ror:8 row_mask:0xf bank_mask:0xf
	v_cndmask_b32_e64 v2, v6, v8, s[10:11]
	v_cndmask_b32_e64 v3, v7, v9, s[10:11]
	v_cndmask_b32_e64 v4, v8, v6, s[10:11]
	v_cndmask_b32_e64 v5, v9, v7, s[10:11]
	v_add_f32_dpp v4, v2, v4 row_half_mirror row_mask:0xf bank_mask:0xf
	v_add_f32_dpp v5, v3, v5 row_half_mirror row_mask:0xf bank_mask:0xf
	v_cndmask_b32_e64 v2, v4, v5, s[14:15]
	v_cndmask_b32_e64 v3, v5, v4, s[14:15]
	s_nop 0
	v_add_f32_dpp v3, v2, v3 quad_perm:[2,3,0,1] row_mask:0xf bank_mask:0xf
	s_nop 1
	v_add_f32_dpp v11, v3, v3 quad_perm:[1,0,3,2] row_mask:0xf bank_mask:0xf
	s_mov_b64 exec, s[2:3]
	global_store_dword v[22:23], v11, off offset:384
	s_mov_b64 exec, -1
	s_add_i32 s16, s16, 1
	s_cmp_lt_i32 s16, s17
	s_cbranch_scc1 .Lpa_tok
	s_waitcnt vmcnt(0)
	s_waitcnt vmcnt(0)
	v_cmp_eq_u32_e32 vcc, 0, v0
	s_waitcnt vmcnt(0) lgkmcnt(0)
	s_barrier
	s_and_saveexec_b64 s[2:3], vcc
	s_cbranch_execz .Lgbb_1444
	v_readlane_b32 s4, v237, 5
	s_waitcnt vmcnt(0) expcnt(0) lgkmcnt(0)
	s_nop 0
	v_mov_b32_e32 v1, s4
	ds_read_b32 v3, v1
	ds_read_b32 v1, v1 offset:4
	s_waitcnt lgkmcnt(1)
	v_cmp_ne_u32_e32 vcc, 0, v3
	s_branch .Lgbb_1412
	v_readlane_b32 s4, v237, 2
	v_readlane_b32 s5, v237, 3
	s_load_dwordx2 s[8:9], s[6:7], 0x4
	s_lshl_b64 s[4:5], s[4:5], 2
	v_readlane_b32 s6, v237, 0
	s_add_u32 s4, s6, s4
	v_readlane_b32 s6, v237, 1
	s_addc_u32 s5, s6, s5
	s_add_u32 s6, s4, 0x1000
	s_addc_u32 s7, s5, 0
	s_waitcnt lgkmcnt(0)
	s_mul_i32 s20, s8, s38
	s_add_u32 s8, s4, 0x1100
	s_mul_i32 s20, s20, s9
	s_addc_u32 s9, s5, 0
	s_add_u32 s10, s4, 0x1200
	s_addc_u32 s11, s5, 0
	s_add_u32 s12, s4, 0x1300
	s_addc_u32 s13, s5, 0
	s_mov_b32 s21, 1
	v_mov_b32_e32 v17, 0
	s_branch .Lgbb_1400

.Lgbb_1444:
	s_or_b64 exec, exec, s[2:3]
	s_waitcnt lgkmcnt(0)
	s_barrier
	s_mov_b64 exec, -1
	v_and_b32_e32 v1, 63, v0
	v_readfirstlane_b32 s16, v0
	s_load_dwordx2 s[12:13], s[0:1], 0xc0
	s_lshr_b32 s16, s16, 6
	s_and_b32 s18, s33, 7
	s_lshr_b32 s19, s33, 3
	s_lshl_b32 s19, s19, 8
	s_lshl_b32 s16, s16, 5
	s_add_i32 s16, s16, s19
	s_add_i32 s17, s16, 32
	s_add_i32 s24, s17, -1
	s_lshl_b32 s19, s18, 9
	v_lshl_add_u32 v162, v1, 3, s19
	v_mov_b32_e32 v163, 0
	s_mov_b32 s31, 0
	v_mov_b32_e32 v4, v1
	v_mov_b32_e32 v5, 0
	s_mov_b32 s101, 0
	s_mov_b32 s100, 0x400000
	s_mov_b32 s41, 0x378e98ab
	s_mov_b32 s42, 0x3b7cd369
	s_mov_b32 s43, 0xbcc618b2
	s_mov_b32 s44, 0x3dda74e4
	s_mov_b32 s45, 0x3f228afd
	s_mov_b32 s46, 0x3e03c728
	s_mov_b32 s47, 0xbfb8aa3b
	s_mov_b32 s48, 0x42ce8ed0
	s_mov_b32 s49, 0xc2b17218
	s_mov_b32 s50, 0x7fffffff
	v_mov_b32_e32 v97, 0x43000000
	v_mov_b32_e32 v250, 0x3ba10414
	v_mov_b32_e32 v251, 0xb9c68948
	v_mov_b32_e32 v252, 0x7f800000
	s_load_dwordx2 s[4:5], s[0:1], 0xb8
	s_waitcnt lgkmcnt(0)
	s_add_u32 s26, s12, 0x17c00000
	s_addc_u32 s27, s13, 0
	s_add_u32 s20, s12, 0x100000
	s_addc_u32 s21, s13, 0
	v_lshl_add_u64 v[172:173], v[162:163], 1, s[20:21]
	s_add_u32 s20, s12, 0x4da00000
	s_addc_u32 s21, s13, 0
	v_lshl_add_u64 v[174:175], v[4:5], 2, s[20:21]
	s_add_u32 s20, s12, 0x4de00000
	s_addc_u32 s21, s13, 0
	v_lshl_add_u64 v[176:177], v[4:5], 2, s[20:21]
	s_add_u32 s20, s12, 0x23c00000
	s_addc_u32 s21, s13, 0
	v_lshl_add_u64 v[210:211], v[4:5], 2, s[20:21]
	s_add_u32 s20, s12, 0x25c00000
	s_addc_u32 s21, s13, 0
	v_and_b32_e32 v6, 7, v1
	v_mov_b32_e32 v7, 0
	v_lshlrev_b32_e32 v6, 20, v6
	v_lshl_add_u64 v[212:213], v[6:7], 0, s[20:21]
	v_lshl_add_u64 v[214:215], v[162:163], 2, s[4:5]
	s_add_u32 s66, s12, 0x1fe00000
	s_addc_u32 s67, s13, 0
	s_add_u32 s64, s12, 0x38d80000
	s_addc_u32 s65, s13, 0
	s_add_u32 s60, s12, 0x38d90000
	s_addc_u32 s61, s13, 0
	s_lshl_b32 s19, s18, 20
	s_add_u32 s62, s12, 0x26c00000
	s_addc_u32 s63, s13, 0
	s_add_u32 s62, s62, s19
	s_addc_u32 s63, s63, 0
	v_mov_b32_e32 v19, 0
	s_mov_b32 s2, 0x55555555
	s_mov_b32 s3, 0x55555555
	s_lshl_b32 s30, s16, 13
	v_lshl_add_u64 v[160:161], v[172:173], 0, s[30:31]
	global_load_dwordx4 v[116:119], v[160:161], off
	s_lshl_b32 s30, s16, 9
	v_lshl_add_u64 v[160:161], v[174:175], 0, s[30:31]
	global_load_dword v122, v[160:161], off
	global_load_dword v123, v[160:161], off offset:256
	v_lshl_add_u64 v[160:161], v[176:177], 0, s[30:31]
	global_load_dword v216, v[160:161], off
	global_load_dword v217, v[160:161], off offset:256
	v_lshl_add_u64 v[160:161], v[210:211], 0, s[30:31]
	global_load_dword v218, v[160:161], off
	global_load_dword v226, v[160:161], off offset:256
	v_lshl_add_u64 v[160:161], v[160:161], 0, s[100:101]
	global_load_dword v219, v[160:161], off
	global_load_dword v227, v[160:161], off offset:256
	v_lshl_add_u64 v[160:161], v[160:161], 0, s[100:101]
	global_load_dword v220, v[160:161], off
	global_load_dword v228, v[160:161], off offset:256
	v_lshl_add_u64 v[160:161], v[160:161], 0, s[100:101]
	global_load_dword v221, v[160:161], off
	global_load_dword v229, v[160:161], off offset:256
	v_lshl_add_u64 v[160:161], v[160:161], 0, s[100:101]
	global_load_dword v222, v[160:161], off
	global_load_dword v230, v[160:161], off offset:256
	v_lshl_add_u64 v[160:161], v[160:161], 0, s[100:101]
	global_load_dword v223, v[160:161], off
	global_load_dword v231, v[160:161], off offset:256
	v_lshl_add_u64 v[160:161], v[160:161], 0, s[100:101]
	global_load_dword v224, v[160:161], off
	global_load_dword v232, v[160:161], off offset:256
	v_lshl_add_u64 v[160:161], v[160:161], 0, s[100:101]
	global_load_dword v225, v[160:161], off
	global_load_dword v233, v[160:161], off offset:256
	s_lshl_b32 s30, s16, 7
	v_lshl_add_u64 v[160:161], v[212:213], 0, s[30:31]
	global_load_dword v234, v[160:161], off
	s_lshl_b32 s30, s16, 2
	s_add_u32 s28, s66, s30
	s_addc_u32 s29, s67, 0
	global_load_dword v235, v19, s[28:29]
	s_waitcnt vmcnt(0)
	v_lshlrev_b32_e32 v16, 2, v122
	v_lshlrev_b32_e32 v17, 2, v123
	global_load_dword v238, v16, s[64:65]
	global_load_dword v240, v16, s[60:61]
	global_load_dword v239, v17, s[64:65]
	global_load_dword v241, v17, s[60:61]
	s_waitcnt vmcnt(0)
	s_add_u32 s22, s12, 0x4da00000
	s_addc_u32 s23, s13, 0
	s_lshl_b32 s30, s16, 9
	s_add_u32 s36, s22, s30
	s_addc_u32 s37, s23, 0
	s_load_dwordx16 s[68:83], s[36:37], 0x0
	s_load_dwordx16 s[84:99], s[36:37], 0x40
	s_waitcnt lgkmcnt(0)
	s_lshl_b32 s30, s68, 12
	s_add_u32 s28, s26, s30
	s_addc_u32 s29, s27, 0
	global_load_dwordx2 v[24:25], v162, s[28:29]
	s_lshl_b32 s30, s69, 12
	s_add_u32 s28, s26, s30
	s_addc_u32 s29, s27, 0
	global_load_dwordx2 v[26:27], v162, s[28:29]
	s_lshl_b32 s30, s70, 12
	s_add_u32 s28, s26, s30
	s_addc_u32 s29, s27, 0
	global_load_dwordx2 v[28:29], v162, s[28:29]
	s_lshl_b32 s30, s71, 12
	s_add_u32 s28, s26, s30
	s_addc_u32 s29, s27, 0
	global_load_dwordx2 v[30:31], v162, s[28:29]
	s_lshl_b32 s30, s72, 12
	s_add_u32 s28, s26, s30
	s_addc_u32 s29, s27, 0
	global_load_dwordx2 v[32:33], v162, s[28:29]
	s_lshl_b32 s30, s73, 12
	s_add_u32 s28, s26, s30
	s_addc_u32 s29, s27, 0
	global_load_dwordx2 v[34:35], v162, s[28:29]
	s_lshl_b32 s30, s74, 12
	s_add_u32 s28, s26, s30
	s_addc_u32 s29, s27, 0
	global_load_dwordx2 v[36:37], v162, s[28:29]
	s_lshl_b32 s30, s75, 12
	s_add_u32 s28, s26, s30
	s_addc_u32 s29, s27, 0
	global_load_dwordx2 v[38:39], v162, s[28:29]
	s_lshl_b32 s30, s76, 12
	s_add_u32 s28, s26, s30
	s_addc_u32 s29, s27, 0
	global_load_dwordx2 v[40:41], v162, s[28:29]
	s_lshl_b32 s30, s77, 12
	s_add_u32 s28, s26, s30
	s_addc_u32 s29, s27, 0
	global_load_dwordx2 v[42:43], v162, s[28:29]
	s_lshl_b32 s30, s78, 12
	s_add_u32 s28, s26, s30
	s_addc_u32 s29, s27, 0
	global_load_dwordx2 v[44:45], v162, s[28:29]
	s_lshl_b32 s30, s79, 12
	s_add_u32 s28, s26, s30
	s_addc_u32 s29, s27, 0
	global_load_dwordx2 v[46:47], v162, s[28:29]
	s_lshl_b32 s30, s80, 12
	s_add_u32 s28, s26, s30
	s_addc_u32 s29, s27, 0
	global_load_dwordx2 v[48:49], v162, s[28:29]
	s_lshl_b32 s30, s81, 12
	s_add_u32 s28, s26, s30
	s_addc_u32 s29, s27, 0
	global_load_dwordx2 v[50:51], v162, s[28:29]
	s_lshl_b32 s30, s82, 12
	s_add_u32 s28, s26, s30
	s_addc_u32 s29, s27, 0
	global_load_dwordx2 v[52:53], v162, s[28:29]
	s_lshl_b32 s30, s83, 12
	s_add_u32 s28, s26, s30
	s_addc_u32 s29, s27, 0
	global_load_dwordx2 v[54:55], v162, s[28:29]
	s_lshl_b32 s30, s84, 12
	s_add_u32 s28, s26, s30
	s_addc_u32 s29, s27, 0
	global_load_dwordx2 v[56:57], v162, s[28:29]
	s_lshl_b32 s30, s85, 12
	s_add_u32 s28, s26, s30
	s_addc_u32 s29, s27, 0
	global_load_dwordx2 v[58:59], v162, s[28:29]
	s_lshl_b32 s30, s86, 12
	s_add_u32 s28, s26, s30
	s_addc_u32 s29, s27, 0
	global_load_dwordx2 v[60:61], v162, s[28:29]
	s_lshl_b32 s30, s87, 12
	s_add_u32 s28, s26, s30
	s_addc_u32 s29, s27, 0
	global_load_dwordx2 v[62:63], v162, s[28:29]
	s_lshl_b32 s30, s88, 12
	s_add_u32 s28, s26, s30
	s_addc_u32 s29, s27, 0
	global_load_dwordx2 v[64:65], v162, s[28:29]
	s_lshl_b32 s30, s89, 12
	s_add_u32 s28, s26, s30
	s_addc_u32 s29, s27, 0
	global_load_dwordx2 v[66:67], v162, s[28:29]
	s_lshl_b32 s30, s90, 12
	s_add_u32 s28, s26, s30
	s_addc_u32 s29, s27, 0
	global_load_dwordx2 v[68:69], v162, s[28:29]
	s_lshl_b32 s30, s91, 12
	s_add_u32 s28, s26, s30
	s_addc_u32 s29, s27, 0
	global_load_dwordx2 v[70:71], v162, s[28:29]
	s_lshl_b32 s30, s92, 12
	s_add_u32 s28, s26, s30
	s_addc_u32 s29, s27, 0
	global_load_dwordx2 v[72:73], v162, s[28:29]
	s_lshl_b32 s30, s93, 12
	s_add_u32 s28, s26, s30
	s_addc_u32 s29, s27, 0
	global_load_dwordx2 v[74:75], v162, s[28:29]
	s_lshl_b32 s30, s94, 12
	s_add_u32 s28, s26, s30
	s_addc_u32 s29, s27, 0
	global_load_dwordx2 v[76:77], v162, s[28:29]
	s_lshl_b32 s30, s95, 12
	s_add_u32 s28, s26, s30
	s_addc_u32 s29, s27, 0
	global_load_dwordx2 v[78:79], v162, s[28:29]
	s_lshl_b32 s30, s96, 12
	s_add_u32 s28, s26, s30
	s_addc_u32 s29, s27, 0
	global_load_dwordx2 v[80:81], v162, s[28:29]
	s_lshl_b32 s30, s97, 12
	s_add_u32 s28, s26, s30
	s_addc_u32 s29, s27, 0
	global_load_dwordx2 v[82:83], v162, s[28:29]
	s_lshl_b32 s30, s98, 12
	s_add_u32 s28, s26, s30
	s_addc_u32 s29, s27, 0
	global_load_dwordx2 v[84:85], v162, s[28:29]
	s_lshl_b32 s30, s99, 12
	s_add_u32 s28, s26, s30
	s_addc_u32 s29, s27, 0
	global_load_dwordx2 v[86:87], v162, s[28:29]
	s_load_dwordx16 s[68:83], s[36:37], 0x80

.Lerfa1_1476:
	s_andn2_saveexec_b64 s[34:35], s[34:35]
	v_mul_f32_e32 v12, v11, v11
	v_fmamk_f32 v13, v12, 0xba1345e1, v250
	v_fmaak_f32 v13, v12, v13, 0xbcdac9b8
	v_fmaak_f32 v13, v12, v13, 0x3de703be
	v_fmaak_f32 v13, v12, v13, 0xbec09330
	v_fmaak_f32 v12, v12, v13, 0x3e0375d0
	v_fma_f32 v12, |v11|, v12, |v11|
	s_or_b64 exec, exec, s[34:35]
	v_bfi_b32 v11, s50, v12, v11
	v_mul_f32_e32 v10, 0.5, v10
	v_add_f32_e32 v11, 1.0, v11
	v_mul_f32_e32 v10, v10, v11
	v_mul_f32_e32 v10, v164, v10
	v_mul_f32_e32 v10, v249, v10
	v_mov_b32_e32 v247, v10
	v_add_f32_e32 v16, v246, v247
	s_nop 1
	v_add_f32_dpp v17, v16, v16 quad_perm:[1,0,3,2] row_mask:0xf bank_mask:0xf
	s_nop 1
	v_add_f32_dpp v16, v17, v17 quad_perm:[2,3,0,1] row_mask:0xf bank_mask:0xf
	s_nop 1
	v_add_f32_dpp v17, v16, v16 row_half_mirror row_mask:0xf bank_mask:0xf
	s_nop 1
	v_add_f32_dpp v16, v17, v17 row_ror:8 row_mask:0xf bank_mask:0xf
	v_mov_b32_e32 v17, v16
	s_nop 1
	v_permlane16_swap_b32_e32 v16, v17
	v_add_f32_e32 v16, v16, v17
	v_mov_b32_e32 v17, v16
	s_nop 1
	v_permlane32_swap_b32_e32 v16, v17
	v_add_f32_e32 v16, v16, v17
	v_mul_f32_e32 v248, 0xc3000000, v16
	v_mov_b32_e32 v242, v116
	v_mov_b32_e32 v243, v117
	v_mov_b32_e32 v244, v118
	v_mov_b32_e32 v245, v119
	v_mov_b32_e32 v120, v122
	v_mov_b32_e32 v121, v123
	s_lshl_b32 s30, s16, 14
	v_lshl_add_u64 v[20:21], v[214:215], 0, s[30:31]
	s_add_i32 s18, s16, 1
	s_min_i32 s18, s18, s24
	s_lshl_b32 s30, s16, 9
	s_add_u32 s36, s22, s30
	s_addc_u32 s37, s23, 0
	s_lshl_b32 s30, s18, 9
	s_add_u32 s38, s22, s30
	s_addc_u32 s39, s23, 0
	s_lshl_b32 s30, s18, 13
	v_lshl_add_u64 v[160:161], v[172:173], 0, s[30:31]
	global_load_dwordx4 v[116:119], v[160:161], off
	s_lshl_b32 s30, s18, 9
	v_lshl_add_u64 v[160:161], v[174:175], 0, s[30:31]
	global_load_dword v122, v[160:161], off
	global_load_dword v123, v[160:161], off offset:256
	v_lshl_add_u64 v[160:161], v[176:177], 0, s[30:31]
	global_load_dword v216, v[160:161], off
	global_load_dword v217, v[160:161], off offset:256
	v_lshl_add_u64 v[160:161], v[210:211], 0, s[30:31]
	global_load_dword v218, v[160:161], off
	global_load_dword v226, v[160:161], off offset:256
	v_lshl_add_u64 v[160:161], v[160:161], 0, s[100:101]
	global_load_dword v219, v[160:161], off
	global_load_dword v227, v[160:161], off offset:256
	v_lshl_add_u64 v[160:161], v[160:161], 0, s[100:101]
	global_load_dword v220, v[160:161], off
	global_load_dword v228, v[160:161], off offset:256
	v_lshl_add_u64 v[160:161], v[160:161], 0, s[100:101]
	global_load_dword v221, v[160:161], off
	global_load_dword v229, v[160:161], off offset:256
	v_lshl_add_u64 v[160:161], v[160:161], 0, s[100:101]
	global_load_dword v222, v[160:161], off
	global_load_dword v230, v[160:161], off offset:256
	v_lshl_add_u64 v[160:161], v[160:161], 0, s[100:101]
	global_load_dword v223, v[160:161], off
	global_load_dword v231, v[160:161], off offset:256
	v_lshl_add_u64 v[160:161], v[160:161], 0, s[100:101]
	global_load_dword v224, v[160:161], off
	global_load_dword v232, v[160:161], off offset:256
	v_lshl_add_u64 v[160:161], v[160:161], 0, s[100:101]
	global_load_dword v225, v[160:161], off
	global_load_dword v233, v[160:161], off offset:256
	s_lshl_b32 s30, s18, 7
	v_lshl_add_u64 v[160:161], v[212:213], 0, s[30:31]
	global_load_dword v234, v[160:161], off
	s_lshl_b32 s30, s18, 2
	s_add_u32 s28, s66, s30
	s_addc_u32 s29, s67, 0
	global_load_dword v235, v19, s[28:29]
	v_mov_b32_e32 v178, 0
	v_mov_b32_e32 v179, 0
	v_mov_b32_e32 v180, 0
	v_mov_b32_e32 v181, 0
	v_mov_b32_e32 v182, 0
	v_mov_b32_e32 v183, 0
	v_mov_b32_e32 v184, 0
	v_mov_b32_e32 v185, 0
	s_waitcnt vmcnt(54)
	v_readlane_b32 s25, v246, 0
	v_cvt_f32_ubyte0_e32 v124, v24
	v_cvt_f32_ubyte1_e32 v125, v24
	v_cvt_f32_ubyte2_e32 v126, v24
	v_cvt_f32_ubyte3_e32 v127, v24
	v_cvt_f32_ubyte0_e32 v128, v25
	v_cvt_f32_ubyte1_e32 v129, v25
	v_cvt_f32_ubyte2_e32 v130, v25
	v_cvt_f32_ubyte3_e32 v131, v25
	s_waitcnt lgkmcnt(0)
	s_load_dwordx16 s[84:99], s[36:37], 0xc0
	s_lshl_b32 s30, s68, 12
	s_add_u32 s28, s26, s30
	s_addc_u32 s29, s27, 0
	global_load_dwordx2 v[24:25], v162, s[28:29]
	v_fmac_f32_e32 v178, s25, v124
	v_fmac_f32_e32 v179, s25, v125
	v_fmac_f32_e32 v180, s25, v126
	v_fmac_f32_e32 v181, s25, v127
	v_fmac_f32_e32 v182, s25, v128
	v_fmac_f32_e32 v183, s25, v129
	v_fmac_f32_e32 v184, s25, v130
	v_fmac_f32_e32 v185, s25, v131
	s_waitcnt vmcnt(54)
	v_readlane_b32 s25, v246, 1
	v_cvt_f32_ubyte0_e32 v132, v26
	v_cvt_f32_ubyte1_e32 v133, v26
	v_cvt_f32_ubyte2_e32 v134, v26
	v_cvt_f32_ubyte3_e32 v135, v26
	v_cvt_f32_ubyte0_e32 v136, v27
	v_cvt_f32_ubyte1_e32 v137, v27
	v_cvt_f32_ubyte2_e32 v138, v27
	v_cvt_f32_ubyte3_e32 v139, v27
	s_lshl_b32 s30, s69, 12
	s_add_u32 s28, s26, s30
	s_addc_u32 s29, s27, 0
	global_load_dwordx2 v[26:27], v162, s[28:29]
	v_fmac_f32_e32 v178, s25, v132
	v_fmac_f32_e32 v179, s25, v133
	v_fmac_f32_e32 v180, s25, v134
	v_fmac_f32_e32 v181, s25, v135
	v_fmac_f32_e32 v182, s25, v136
	v_fmac_f32_e32 v183, s25, v137
	v_fmac_f32_e32 v184, s25, v138
	v_fmac_f32_e32 v185, s25, v139
	s_waitcnt vmcnt(54)
	v_readlane_b32 s25, v246, 2
	v_cvt_f32_ubyte0_e32 v124, v28
	v_cvt_f32_ubyte1_e32 v125, v28
	v_cvt_f32_ubyte2_e32 v126, v28
	v_cvt_f32_ubyte3_e32 v127, v28
	v_cvt_f32_ubyte0_e32 v128, v29
	v_cvt_f32_ubyte1_e32 v129, v29
	v_cvt_f32_ubyte2_e32 v130, v29
	v_cvt_f32_ubyte3_e32 v131, v29
	s_lshl_b32 s30, s70, 12
	s_add_u32 s28, s26, s30
	s_addc_u32 s29, s27, 0
	global_load_dwordx2 v[28:29], v162, s[28:29]
	v_fmac_f32_e32 v178, s25, v124
	v_fmac_f32_e32 v179, s25, v125
	v_fmac_f32_e32 v180, s25, v126
	v_fmac_f32_e32 v181, s25, v127
	v_fmac_f32_e32 v182, s25, v128
	v_fmac_f32_e32 v183, s25, v129
	v_fmac_f32_e32 v184, s25, v130
	v_fmac_f32_e32 v185, s25, v131
	s_waitcnt vmcnt(54)
	v_readlane_b32 s25, v246, 3
	v_cvt_f32_ubyte0_e32 v132, v30
	v_cvt_f32_ubyte1_e32 v133, v30
	v_cvt_f32_ubyte2_e32 v134, v30
	v_cvt_f32_ubyte3_e32 v135, v30
	v_cvt_f32_ubyte0_e32 v136, v31
	v_cvt_f32_ubyte1_e32 v137, v31
	v_cvt_f32_ubyte2_e32 v138, v31
	v_cvt_f32_ubyte3_e32 v139, v31
	s_lshl_b32 s30, s71, 12
	s_add_u32 s28, s26, s30
	s_addc_u32 s29, s27, 0
	global_load_dwordx2 v[30:31], v162, s[28:29]
	v_fmac_f32_e32 v178, s25, v132
	v_fmac_f32_e32 v179, s25, v133
	v_fmac_f32_e32 v180, s25, v134
	v_fmac_f32_e32 v181, s25, v135
	v_fmac_f32_e32 v182, s25, v136
	v_fmac_f32_e32 v183, s25, v137
	v_fmac_f32_e32 v184, s25, v138
	v_fmac_f32_e32 v185, s25, v139
	s_waitcnt vmcnt(54)
	v_readlane_b32 s25, v246, 4
	v_cvt_f32_ubyte0_e32 v124, v32
	v_cvt_f32_ubyte1_e32 v125, v32
	v_cvt_f32_ubyte2_e32 v126, v32
	v_cvt_f32_ubyte3_e32 v127, v32
	v_cvt_f32_ubyte0_e32 v128, v33
	v_cvt_f32_ubyte1_e32 v129, v33
	v_cvt_f32_ubyte2_e32 v130, v33
	v_cvt_f32_ubyte3_e32 v131, v33
	s_lshl_b32 s30, s72, 12
	s_add_u32 s28, s26, s30
	s_addc_u32 s29, s27, 0
	global_load_dwordx2 v[32:33], v162, s[28:29]
	v_fmac_f32_e32 v178, s25, v124
	v_fmac_f32_e32 v179, s25, v125
	v_fmac_f32_e32 v180, s25, v126
	v_fmac_f32_e32 v181, s25, v127
	v_fmac_f32_e32 v182, s25, v128
	v_fmac_f32_e32 v183, s25, v129
	v_fmac_f32_e32 v184, s25, v130
	v_fmac_f32_e32 v185, s25, v131
	s_waitcnt vmcnt(54)
	v_readlane_b32 s25, v246, 5
	v_cvt_f32_ubyte0_e32 v132, v34
	v_cvt_f32_ubyte1_e32 v133, v34
	v_cvt_f32_ubyte2_e32 v134, v34
	v_cvt_f32_ubyte3_e32 v135, v34
	v_cvt_f32_ubyte0_e32 v136, v35
	v_cvt_f32_ubyte1_e32 v137, v35
	v_cvt_f32_ubyte2_e32 v138, v35
	v_cvt_f32_ubyte3_e32 v139, v35
	s_lshl_b32 s30, s73, 12
	s_add_u32 s28, s26, s30
	s_addc_u32 s29, s27, 0
	global_load_dwordx2 v[34:35], v162, s[28:29]
	v_fmac_f32_e32 v178, s25, v132
	v_fmac_f32_e32 v179, s25, v133
	v_fmac_f32_e32 v180, s25, v134
	v_fmac_f32_e32 v181, s25, v135
	v_fmac_f32_e32 v182, s25, v136
	v_fmac_f32_e32 v183, s25, v137
	v_fmac_f32_e32 v184, s25, v138
	v_fmac_f32_e32 v185, s25, v139
	s_waitcnt vmcnt(54)
	v_readlane_b32 s25, v246, 6
	v_cvt_f32_ubyte0_e32 v124, v36
	v_cvt_f32_ubyte1_e32 v125, v36
	v_cvt_f32_ubyte2_e32 v126, v36
	v_cvt_f32_ubyte3_e32 v127, v36
	v_cvt_f32_ubyte0_e32 v128, v37
	v_cvt_f32_ubyte1_e32 v129, v37
	v_cvt_f32_ubyte2_e32 v130, v37
	v_cvt_f32_ubyte3_e32 v131, v37
	s_lshl_b32 s30, s74, 12
	s_add_u32 s28, s26, s30
	s_addc_u32 s29, s27, 0
	global_load_dwordx2 v[36:37], v162, s[28:29]
	v_fmac_f32_e32 v178, s25, v124
	v_fmac_f32_e32 v179, s25, v125
	v_fmac_f32_e32 v180, s25, v126
	v_fmac_f32_e32 v181, s25, v127
	v_fmac_f32_e32 v182, s25, v128
	v_fmac_f32_e32 v183, s25, v129
	v_fmac_f32_e32 v184, s25, v130
	v_fmac_f32_e32 v185, s25, v131
	s_waitcnt vmcnt(54)
	v_readlane_b32 s25, v246, 7
	v_cvt_f32_ubyte0_e32 v132, v38
	v_cvt_f32_ubyte1_e32 v133, v38
	v_cvt_f32_ubyte2_e32 v134, v38
	v_cvt_f32_ubyte3_e32 v135, v38
	v_cvt_f32_ubyte0_e32 v136, v39
	v_cvt_f32_ubyte1_e32 v137, v39
	v_cvt_f32_ubyte2_e32 v138, v39
	v_cvt_f32_ubyte3_e32 v139, v39
	s_lshl_b32 s30, s75, 12
	s_add_u32 s28, s26, s30
	s_addc_u32 s29, s27, 0
	global_load_dwordx2 v[38:39], v162, s[28:29]
	v_fmac_f32_e32 v178, s25, v132
	v_fmac_f32_e32 v179, s25, v133
	v_fmac_f32_e32 v180, s25, v134
	v_fmac_f32_e32 v181, s25, v135
	v_fmac_f32_e32 v182, s25, v136
	v_fmac_f32_e32 v183, s25, v137
	v_fmac_f32_e32 v184, s25, v138
	v_fmac_f32_e32 v185, s25, v139
	s_waitcnt vmcnt(54)
	v_readlane_b32 s25, v246, 8
	v_cvt_f32_ubyte0_e32 v124, v40
	v_cvt_f32_ubyte1_e32 v125, v40
	v_cvt_f32_ubyte2_e32 v126, v40
	v_cvt_f32_ubyte3_e32 v127, v40
	v_cvt_f32_ubyte0_e32 v128, v41
	v_cvt_f32_ubyte1_e32 v129, v41
	v_cvt_f32_ubyte2_e32 v130, v41
	v_cvt_f32_ubyte3_e32 v131, v41
	s_lshl_b32 s30, s76, 12
	s_add_u32 s28, s26, s30
	s_addc_u32 s29, s27, 0
	global_load_dwordx2 v[40:41], v162, s[28:29]
	v_fmac_f32_e32 v178, s25, v124
	v_fmac_f32_e32 v179, s25, v125
	v_fmac_f32_e32 v180, s25, v126
	v_fmac_f32_e32 v181, s25, v127
	v_fmac_f32_e32 v182, s25, v128
	v_fmac_f32_e32 v183, s25, v129
	v_fmac_f32_e32 v184, s25, v130
	v_fmac_f32_e32 v185, s25, v131
	s_waitcnt vmcnt(54)
	v_readlane_b32 s25, v246, 9
	v_cvt_f32_ubyte0_e32 v132, v42
	v_cvt_f32_ubyte1_e32 v133, v42
	v_cvt_f32_ubyte2_e32 v134, v42
	v_cvt_f32_ubyte3_e32 v135, v42
	v_cvt_f32_ubyte0_e32 v136, v43
	v_cvt_f32_ubyte1_e32 v137, v43
	v_cvt_f32_ubyte2_e32 v138, v43
	v_cvt_f32_ubyte3_e32 v139, v43
	s_lshl_b32 s30, s77, 12
	s_add_u32 s28, s26, s30
	s_addc_u32 s29, s27, 0
	global_load_dwordx2 v[42:43], v162, s[28:29]
	v_fmac_f32_e32 v178, s25, v132
	v_fmac_f32_e32 v179, s25, v133
	v_fmac_f32_e32 v180, s25, v134
	v_fmac_f32_e32 v181, s25, v135
	v_fmac_f32_e32 v182, s25, v136
	v_fmac_f32_e32 v183, s25, v137
	v_fmac_f32_e32 v184, s25, v138
	v_fmac_f32_e32 v185, s25, v139
	s_waitcnt vmcnt(54)
	v_readlane_b32 s25, v246, 10
	v_cvt_f32_ubyte0_e32 v124, v44
	v_cvt_f32_ubyte1_e32 v125, v44
	v_cvt_f32_ubyte2_e32 v126, v44
	v_cvt_f32_ubyte3_e32 v127, v44
	v_cvt_f32_ubyte0_e32 v128, v45
	v_cvt_f32_ubyte1_e32 v129, v45
	v_cvt_f32_ubyte2_e32 v130, v45
	v_cvt_f32_ubyte3_e32 v131, v45
	s_lshl_b32 s30, s78, 12
	s_add_u32 s28, s26, s30
	s_addc_u32 s29, s27, 0
	global_load_dwordx2 v[44:45], v162, s[28:29]
	v_fmac_f32_e32 v178, s25, v124
	v_fmac_f32_e32 v179, s25, v125
	v_fmac_f32_e32 v180, s25, v126
	v_fmac_f32_e32 v181, s25, v127
	v_fmac_f32_e32 v182, s25, v128
	v_fmac_f32_e32 v183, s25, v129
	v_fmac_f32_e32 v184, s25, v130
	v_fmac_f32_e32 v185, s25, v131
	s_waitcnt vmcnt(54)
	v_readlane_b32 s25, v246, 11
	v_cvt_f32_ubyte0_e32 v132, v46
	v_cvt_f32_ubyte1_e32 v133, v46
	v_cvt_f32_ubyte2_e32 v134, v46
	v_cvt_f32_ubyte3_e32 v135, v46
	v_cvt_f32_ubyte0_e32 v136, v47
	v_cvt_f32_ubyte1_e32 v137, v47
	v_cvt_f32_ubyte2_e32 v138, v47
	v_cvt_f32_ubyte3_e32 v139, v47
	s_lshl_b32 s30, s79, 12
	s_add_u32 s28, s26, s30
	s_addc_u32 s29, s27, 0
	global_load_dwordx2 v[46:47], v162, s[28:29]
	v_fmac_f32_e32 v178, s25, v132
	v_fmac_f32_e32 v179, s25, v133
	v_fmac_f32_e32 v180, s25, v134
	v_fmac_f32_e32 v181, s25, v135
	v_fmac_f32_e32 v182, s25, v136
	v_fmac_f32_e32 v183, s25, v137
	v_fmac_f32_e32 v184, s25, v138
	v_fmac_f32_e32 v185, s25, v139
	s_waitcnt vmcnt(54)
	v_readlane_b32 s25, v246, 12
	v_cvt_f32_ubyte0_e32 v124, v48
	v_cvt_f32_ubyte1_e32 v125, v48
	v_cvt_f32_ubyte2_e32 v126, v48
	v_cvt_f32_ubyte3_e32 v127, v48
	v_cvt_f32_ubyte0_e32 v128, v49
	v_cvt_f32_ubyte1_e32 v129, v49
	v_cvt_f32_ubyte2_e32 v130, v49
	v_cvt_f32_ubyte3_e32 v131, v49
	s_lshl_b32 s30, s80, 12
	s_add_u32 s28, s26, s30
	s_addc_u32 s29, s27, 0
	global_load_dwordx2 v[48:49], v162, s[28:29]
	v_fmac_f32_e32 v178, s25, v124
	v_fmac_f32_e32 v179, s25, v125
	v_fmac_f32_e32 v180, s25, v126
	v_fmac_f32_e32 v181, s25, v127
	v_fmac_f32_e32 v182, s25, v128
	v_fmac_f32_e32 v183, s25, v129
	v_fmac_f32_e32 v184, s25, v130
	v_fmac_f32_e32 v185, s25, v131
	s_waitcnt vmcnt(54)
	v_readlane_b32 s25, v246, 13
	v_cvt_f32_ubyte0_e32 v132, v50
	v_cvt_f32_ubyte1_e32 v133, v50
	v_cvt_f32_ubyte2_e32 v134, v50
	v_cvt_f32_ubyte3_e32 v135, v50
	v_cvt_f32_ubyte0_e32 v136, v51
	v_cvt_f32_ubyte1_e32 v137, v51
	v_cvt_f32_ubyte2_e32 v138, v51
	v_cvt_f32_ubyte3_e32 v139, v51
	s_lshl_b32 s30, s81, 12
	s_add_u32 s28, s26, s30
	s_addc_u32 s29, s27, 0
	global_load_dwordx2 v[50:51], v162, s[28:29]
	v_fmac_f32_e32 v178, s25, v132
	v_fmac_f32_e32 v179, s25, v133
	v_fmac_f32_e32 v180, s25, v134
	v_fmac_f32_e32 v181, s25, v135
	v_fmac_f32_e32 v182, s25, v136
	v_fmac_f32_e32 v183, s25, v137
	v_fmac_f32_e32 v184, s25, v138
	v_fmac_f32_e32 v185, s25, v139
	s_waitcnt vmcnt(54)
	v_readlane_b32 s25, v246, 14
	v_cvt_f32_ubyte0_e32 v124, v52
	v_cvt_f32_ubyte1_e32 v125, v52
	v_cvt_f32_ubyte2_e32 v126, v52
	v_cvt_f32_ubyte3_e32 v127, v52
	v_cvt_f32_ubyte0_e32 v128, v53
	v_cvt_f32_ubyte1_e32 v129, v53
	v_cvt_f32_ubyte2_e32 v130, v53
	v_cvt_f32_ubyte3_e32 v131, v53
	s_lshl_b32 s30, s82, 12
	s_add_u32 s28, s26, s30
	s_addc_u32 s29, s27, 0
	global_load_dwordx2 v[52:53], v162, s[28:29]
	v_fmac_f32_e32 v178, s25, v124
	v_fmac_f32_e32 v179, s25, v125
	v_fmac_f32_e32 v180, s25, v126
	v_fmac_f32_e32 v181, s25, v127
	v_fmac_f32_e32 v182, s25, v128
	v_fmac_f32_e32 v183, s25, v129
	v_fmac_f32_e32 v184, s25, v130
	v_fmac_f32_e32 v185, s25, v131
	s_waitcnt vmcnt(54)
	v_readlane_b32 s25, v246, 15
	v_cvt_f32_ubyte0_e32 v132, v54
	v_cvt_f32_ubyte1_e32 v133, v54
	v_cvt_f32_ubyte2_e32 v134, v54
	v_cvt_f32_ubyte3_e32 v135, v54
	v_cvt_f32_ubyte0_e32 v136, v55
	v_cvt_f32_ubyte1_e32 v137, v55
	v_cvt_f32_ubyte2_e32 v138, v55
	v_cvt_f32_ubyte3_e32 v139, v55
	s_lshl_b32 s30, s83, 12
	s_add_u32 s28, s26, s30
	s_addc_u32 s29, s27, 0
	global_load_dwordx2 v[54:55], v162, s[28:29]
	v_fmac_f32_e32 v178, s25, v132
	v_fmac_f32_e32 v179, s25, v133
	v_fmac_f32_e32 v180, s25, v134
	v_fmac_f32_e32 v181, s25, v135
	v_fmac_f32_e32 v182, s25, v136
	v_fmac_f32_e32 v183, s25, v137
	v_fmac_f32_e32 v184, s25, v138
	v_fmac_f32_e32 v185, s25, v139
	s_waitcnt vmcnt(54)
	v_readlane_b32 s25, v246, 16
	v_cvt_f32_ubyte0_e32 v124, v56
	v_cvt_f32_ubyte1_e32 v125, v56
	v_cvt_f32_ubyte2_e32 v126, v56
	v_cvt_f32_ubyte3_e32 v127, v56
	v_cvt_f32_ubyte0_e32 v128, v57
	v_cvt_f32_ubyte1_e32 v129, v57
	v_cvt_f32_ubyte2_e32 v130, v57
	v_cvt_f32_ubyte3_e32 v131, v57
	s_waitcnt lgkmcnt(0)
	s_load_dwordx16 s[68:83], s[36:37], 0x100
	s_lshl_b32 s30, s84, 12
	s_add_u32 s28, s26, s30
	s_addc_u32 s29, s27, 0
	global_load_dwordx2 v[56:57], v162, s[28:29]
	v_fmac_f32_e32 v178, s25, v124
	v_fmac_f32_e32 v179, s25, v125
	v_fmac_f32_e32 v180, s25, v126
	v_fmac_f32_e32 v181, s25, v127
	v_fmac_f32_e32 v182, s25, v128
	v_fmac_f32_e32 v183, s25, v129
	v_fmac_f32_e32 v184, s25, v130
	v_fmac_f32_e32 v185, s25, v131
	s_waitcnt vmcnt(54)
	v_readlane_b32 s25, v246, 17
	v_cvt_f32_ubyte0_e32 v132, v58
	v_cvt_f32_ubyte1_e32 v133, v58
	v_cvt_f32_ubyte2_e32 v134, v58
	v_cvt_f32_ubyte3_e32 v135, v58
	v_cvt_f32_ubyte0_e32 v136, v59
	v_cvt_f32_ubyte1_e32 v137, v59
	v_cvt_f32_ubyte2_e32 v138, v59
	v_cvt_f32_ubyte3_e32 v139, v59
	s_lshl_b32 s30, s85, 12
	s_add_u32 s28, s26, s30
	s_addc_u32 s29, s27, 0
	global_load_dwordx2 v[58:59], v162, s[28:29]
	v_fmac_f32_e32 v178, s25, v132
	v_fmac_f32_e32 v179, s25, v133
	v_fmac_f32_e32 v180, s25, v134
	v_fmac_f32_e32 v181, s25, v135
	v_fmac_f32_e32 v182, s25, v136
	v_fmac_f32_e32 v183, s25, v137
	v_fmac_f32_e32 v184, s25, v138
	v_fmac_f32_e32 v185, s25, v139
	s_waitcnt vmcnt(54)
	v_readlane_b32 s25, v246, 18
	v_cvt_f32_ubyte0_e32 v124, v60
	v_cvt_f32_ubyte1_e32 v125, v60
	v_cvt_f32_ubyte2_e32 v126, v60
	v_cvt_f32_ubyte3_e32 v127, v60
	v_cvt_f32_ubyte0_e32 v128, v61
	v_cvt_f32_ubyte1_e32 v129, v61
	v_cvt_f32_ubyte2_e32 v130, v61
	v_cvt_f32_ubyte3_e32 v131, v61
	s_lshl_b32 s30, s86, 12
	s_add_u32 s28, s26, s30
	s_addc_u32 s29, s27, 0
	global_load_dwordx2 v[60:61], v162, s[28:29]
	v_fmac_f32_e32 v178, s25, v124
	v_fmac_f32_e32 v179, s25, v125
	v_fmac_f32_e32 v180, s25, v126
	v_fmac_f32_e32 v181, s25, v127
	v_fmac_f32_e32 v182, s25, v128
	v_fmac_f32_e32 v183, s25, v129
	v_fmac_f32_e32 v184, s25, v130
	v_fmac_f32_e32 v185, s25, v131
	s_waitcnt vmcnt(54)
	v_readlane_b32 s25, v246, 19
	v_cvt_f32_ubyte0_e32 v132, v62
	v_cvt_f32_ubyte1_e32 v133, v62
	v_cvt_f32_ubyte2_e32 v134, v62
	v_cvt_f32_ubyte3_e32 v135, v62
	v_cvt_f32_ubyte0_e32 v136, v63
	v_cvt_f32_ubyte1_e32 v137, v63
	v_cvt_f32_ubyte2_e32 v138, v63
	v_cvt_f32_ubyte3_e32 v139, v63
	s_lshl_b32 s30, s87, 12
	s_add_u32 s28, s26, s30
	s_addc_u32 s29, s27, 0
	global_load_dwordx2 v[62:63], v162, s[28:29]
	v_fmac_f32_e32 v178, s25, v132
	v_fmac_f32_e32 v179, s25, v133
	v_fmac_f32_e32 v180, s25, v134
	v_fmac_f32_e32 v181, s25, v135
	v_fmac_f32_e32 v182, s25, v136
	v_fmac_f32_e32 v183, s25, v137
	v_fmac_f32_e32 v184, s25, v138
	v_fmac_f32_e32 v185, s25, v139
	s_waitcnt vmcnt(54)
	v_readlane_b32 s25, v246, 20
	v_cvt_f32_ubyte0_e32 v124, v64
	v_cvt_f32_ubyte1_e32 v125, v64
	v_cvt_f32_ubyte2_e32 v126, v64
	v_cvt_f32_ubyte3_e32 v127, v64
	v_cvt_f32_ubyte0_e32 v128, v65
	v_cvt_f32_ubyte1_e32 v129, v65
	v_cvt_f32_ubyte2_e32 v130, v65
	v_cvt_f32_ubyte3_e32 v131, v65
	s_lshl_b32 s30, s88, 12
	s_add_u32 s28, s26, s30
	s_addc_u32 s29, s27, 0
	global_load_dwordx2 v[64:65], v162, s[28:29]
	v_fmac_f32_e32 v178, s25, v124
	v_fmac_f32_e32 v179, s25, v125
	v_fmac_f32_e32 v180, s25, v126
	v_fmac_f32_e32 v181, s25, v127
	v_fmac_f32_e32 v182, s25, v128
	v_fmac_f32_e32 v183, s25, v129
	v_fmac_f32_e32 v184, s25, v130
	v_fmac_f32_e32 v185, s25, v131
	s_waitcnt vmcnt(54)
	v_readlane_b32 s25, v246, 21
	v_cvt_f32_ubyte0_e32 v132, v66
	v_cvt_f32_ubyte1_e32 v133, v66
	v_cvt_f32_ubyte2_e32 v134, v66
	v_cvt_f32_ubyte3_e32 v135, v66
	v_cvt_f32_ubyte0_e32 v136, v67
	v_cvt_f32_ubyte1_e32 v137, v67
	v_cvt_f32_ubyte2_e32 v138, v67
	v_cvt_f32_ubyte3_e32 v139, v67
	s_lshl_b32 s30, s89, 12
	s_add_u32 s28, s26, s30
	s_addc_u32 s29, s27, 0
	global_load_dwordx2 v[66:67], v162, s[28:29]
	v_fmac_f32_e32 v178, s25, v132
	v_fmac_f32_e32 v179, s25, v133
	v_fmac_f32_e32 v180, s25, v134
	v_fmac_f32_e32 v181, s25, v135
	v_fmac_f32_e32 v182, s25, v136
	v_fmac_f32_e32 v183, s25, v137
	v_fmac_f32_e32 v184, s25, v138
	v_fmac_f32_e32 v185, s25, v139
	s_waitcnt vmcnt(54)
	v_readlane_b32 s25, v246, 22
	v_cvt_f32_ubyte0_e32 v124, v68
	v_cvt_f32_ubyte1_e32 v125, v68
	v_cvt_f32_ubyte2_e32 v126, v68
	v_cvt_f32_ubyte3_e32 v127, v68
	v_cvt_f32_ubyte0_e32 v128, v69
	v_cvt_f32_ubyte1_e32 v129, v69
	v_cvt_f32_ubyte2_e32 v130, v69
	v_cvt_f32_ubyte3_e32 v131, v69
	s_lshl_b32 s30, s90, 12
	s_add_u32 s28, s26, s30
	s_addc_u32 s29, s27, 0
	global_load_dwordx2 v[68:69], v162, s[28:29]
	v_fmac_f32_e32 v178, s25, v124
	v_fmac_f32_e32 v179, s25, v125
	v_fmac_f32_e32 v180, s25, v126
	v_fmac_f32_e32 v181, s25, v127
	v_fmac_f32_e32 v182, s25, v128
	v_fmac_f32_e32 v183, s25, v129
	v_fmac_f32_e32 v184, s25, v130
	v_fmac_f32_e32 v185, s25, v131
	s_waitcnt vmcnt(54)
	v_readlane_b32 s25, v246, 23
	v_cvt_f32_ubyte0_e32 v132, v70
	v_cvt_f32_ubyte1_e32 v133, v70
	v_cvt_f32_ubyte2_e32 v134, v70
	v_cvt_f32_ubyte3_e32 v135, v70
	v_cvt_f32_ubyte0_e32 v136, v71
	v_cvt_f32_ubyte1_e32 v137, v71
	v_cvt_f32_ubyte2_e32 v138, v71
	v_cvt_f32_ubyte3_e32 v139, v71
	s_lshl_b32 s30, s91, 12
	s_add_u32 s28, s26, s30
	s_addc_u32 s29, s27, 0
	global_load_dwordx2 v[70:71], v162, s[28:29]
	v_fmac_f32_e32 v178, s25, v132
	v_fmac_f32_e32 v179, s25, v133
	v_fmac_f32_e32 v180, s25, v134
	v_fmac_f32_e32 v181, s25, v135
	v_fmac_f32_e32 v182, s25, v136
	v_fmac_f32_e32 v183, s25, v137
	v_fmac_f32_e32 v184, s25, v138
	v_fmac_f32_e32 v185, s25, v139
	s_waitcnt vmcnt(54)
	v_readlane_b32 s25, v246, 24
	v_cvt_f32_ubyte0_e32 v124, v72
	v_cvt_f32_ubyte1_e32 v125, v72
	v_cvt_f32_ubyte2_e32 v126, v72
	v_cvt_f32_ubyte3_e32 v127, v72
	v_cvt_f32_ubyte0_e32 v128, v73
	v_cvt_f32_ubyte1_e32 v129, v73
	v_cvt_f32_ubyte2_e32 v130, v73
	v_cvt_f32_ubyte3_e32 v131, v73
	s_lshl_b32 s30, s92, 12
	s_add_u32 s28, s26, s30
	s_addc_u32 s29, s27, 0
	global_load_dwordx2 v[72:73], v162, s[28:29]
	v_fmac_f32_e32 v178, s25, v124
	v_fmac_f32_e32 v179, s25, v125
	v_fmac_f32_e32 v180, s25, v126
	v_fmac_f32_e32 v181, s25, v127
	v_fmac_f32_e32 v182, s25, v128
	v_fmac_f32_e32 v183, s25, v129
	v_fmac_f32_e32 v184, s25, v130
	v_fmac_f32_e32 v185, s25, v131
	s_waitcnt vmcnt(54)
	v_readlane_b32 s25, v246, 25
	v_cvt_f32_ubyte0_e32 v132, v74
	v_cvt_f32_ubyte1_e32 v133, v74
	v_cvt_f32_ubyte2_e32 v134, v74
	v_cvt_f32_ubyte3_e32 v135, v74
	v_cvt_f32_ubyte0_e32 v136, v75
	v_cvt_f32_ubyte1_e32 v137, v75
	v_cvt_f32_ubyte2_e32 v138, v75
	v_cvt_f32_ubyte3_e32 v139, v75
	s_lshl_b32 s30, s93, 12
	s_add_u32 s28, s26, s30
	s_addc_u32 s29, s27, 0
	global_load_dwordx2 v[74:75], v162, s[28:29]
	v_fmac_f32_e32 v178, s25, v132
	v_fmac_f32_e32 v179, s25, v133
	v_fmac_f32_e32 v180, s25, v134
	v_fmac_f32_e32 v181, s25, v135
	v_fmac_f32_e32 v182, s25, v136
	v_fmac_f32_e32 v183, s25, v137
	v_fmac_f32_e32 v184, s25, v138
	v_fmac_f32_e32 v185, s25, v139
	s_waitcnt vmcnt(54)
	v_readlane_b32 s25, v246, 26
	v_cvt_f32_ubyte0_e32 v124, v76
	v_cvt_f32_ubyte1_e32 v125, v76
	v_cvt_f32_ubyte2_e32 v126, v76
	v_cvt_f32_ubyte3_e32 v127, v76
	v_cvt_f32_ubyte0_e32 v128, v77
	v_cvt_f32_ubyte1_e32 v129, v77
	v_cvt_f32_ubyte2_e32 v130, v77
	v_cvt_f32_ubyte3_e32 v131, v77
	s_lshl_b32 s30, s94, 12
	s_add_u32 s28, s26, s30
	s_addc_u32 s29, s27, 0
	global_load_dwordx2 v[76:77], v162, s[28:29]
	v_fmac_f32_e32 v178, s25, v124
	v_fmac_f32_e32 v179, s25, v125
	v_fmac_f32_e32 v180, s25, v126
	v_fmac_f32_e32 v181, s25, v127
	v_fmac_f32_e32 v182, s25, v128
	v_fmac_f32_e32 v183, s25, v129
	v_fmac_f32_e32 v184, s25, v130
	v_fmac_f32_e32 v185, s25, v131
	s_waitcnt vmcnt(54)
	v_readlane_b32 s25, v246, 27
	v_cvt_f32_ubyte0_e32 v132, v78
	v_cvt_f32_ubyte1_e32 v133, v78
	v_cvt_f32_ubyte2_e32 v134, v78
	v_cvt_f32_ubyte3_e32 v135, v78
	v_cvt_f32_ubyte0_e32 v136, v79
	v_cvt_f32_ubyte1_e32 v137, v79
	v_cvt_f32_ubyte2_e32 v138, v79
	v_cvt_f32_ubyte3_e32 v139, v79
	s_lshl_b32 s30, s95, 12
	s_add_u32 s28, s26, s30
	s_addc_u32 s29, s27, 0
	global_load_dwordx2 v[78:79], v162, s[28:29]
	v_fmac_f32_e32 v178, s25, v132
	v_fmac_f32_e32 v179, s25, v133
	v_fmac_f32_e32 v180, s25, v134
	v_fmac_f32_e32 v181, s25, v135
	v_fmac_f32_e32 v182, s25, v136
	v_fmac_f32_e32 v183, s25, v137
	v_fmac_f32_e32 v184, s25, v138
	v_fmac_f32_e32 v185, s25, v139
	s_waitcnt vmcnt(54)
	v_readlane_b32 s25, v246, 28
	v_cvt_f32_ubyte0_e32 v124, v80
	v_cvt_f32_ubyte1_e32 v125, v80
	v_cvt_f32_ubyte2_e32 v126, v80
	v_cvt_f32_ubyte3_e32 v127, v80
	v_cvt_f32_ubyte0_e32 v128, v81
	v_cvt_f32_ubyte1_e32 v129, v81
	v_cvt_f32_ubyte2_e32 v130, v81
	v_cvt_f32_ubyte3_e32 v131, v81
	s_lshl_b32 s30, s96, 12
	s_add_u32 s28, s26, s30
	s_addc_u32 s29, s27, 0
	global_load_dwordx2 v[80:81], v162, s[28:29]
	v_fmac_f32_e32 v178, s25, v124
	v_fmac_f32_e32 v179, s25, v125
	v_fmac_f32_e32 v180, s25, v126
	v_fmac_f32_e32 v181, s25, v127
	v_fmac_f32_e32 v182, s25, v128
	v_fmac_f32_e32 v183, s25, v129
	v_fmac_f32_e32 v184, s25, v130
	v_fmac_f32_e32 v185, s25, v131
	s_waitcnt vmcnt(54)
	v_readlane_b32 s25, v246, 29
	v_cvt_f32_ubyte0_e32 v132, v82
	v_cvt_f32_ubyte1_e32 v133, v82
	v_cvt_f32_ubyte2_e32 v134, v82
	v_cvt_f32_ubyte3_e32 v135, v82
	v_cvt_f32_ubyte0_e32 v136, v83
	v_cvt_f32_ubyte1_e32 v137, v83
	v_cvt_f32_ubyte2_e32 v138, v83
	v_cvt_f32_ubyte3_e32 v139, v83
	s_lshl_b32 s30, s97, 12
	s_add_u32 s28, s26, s30
	s_addc_u32 s29, s27, 0
	global_load_dwordx2 v[82:83], v162, s[28:29]
	v_fmac_f32_e32 v178, s25, v132
	v_fmac_f32_e32 v179, s25, v133
	v_fmac_f32_e32 v180, s25, v134
	v_fmac_f32_e32 v181, s25, v135
	v_fmac_f32_e32 v182, s25, v136
	v_fmac_f32_e32 v183, s25, v137
	v_fmac_f32_e32 v184, s25, v138
	v_fmac_f32_e32 v185, s25, v139
	s_waitcnt vmcnt(54)
	v_readlane_b32 s25, v246, 30
	v_cvt_f32_ubyte0_e32 v124, v84
	v_cvt_f32_ubyte1_e32 v125, v84
	v_cvt_f32_ubyte2_e32 v126, v84
	v_cvt_f32_ubyte3_e32 v127, v84
	v_cvt_f32_ubyte0_e32 v128, v85
	v_cvt_f32_ubyte1_e32 v129, v85
	v_cvt_f32_ubyte2_e32 v130, v85
	v_cvt_f32_ubyte3_e32 v131, v85
	s_lshl_b32 s30, s98, 12
	s_add_u32 s28, s26, s30
	s_addc_u32 s29, s27, 0
	global_load_dwordx2 v[84:85], v162, s[28:29]
	v_fmac_f32_e32 v178, s25, v124
	v_fmac_f32_e32 v179, s25, v125
	v_fmac_f32_e32 v180, s25, v126
	v_fmac_f32_e32 v181, s25, v127
	v_fmac_f32_e32 v182, s25, v128
	v_fmac_f32_e32 v183, s25, v129
	v_fmac_f32_e32 v184, s25, v130
	v_fmac_f32_e32 v185, s25, v131
	s_waitcnt vmcnt(54)
	v_readlane_b32 s25, v246, 31
	v_cvt_f32_ubyte0_e32 v132, v86
	v_cvt_f32_ubyte1_e32 v133, v86
	v_cvt_f32_ubyte2_e32 v134, v86
	v_cvt_f32_ubyte3_e32 v135, v86
	v_cvt_f32_ubyte0_e32 v136, v87
	v_cvt_f32_ubyte1_e32 v137, v87
	v_cvt_f32_ubyte2_e32 v138, v87
	v_cvt_f32_ubyte3_e32 v139, v87
	s_lshl_b32 s30, s99, 12
	s_add_u32 s28, s26, s30
	s_addc_u32 s29, s27, 0
	global_load_dwordx2 v[86:87], v162, s[28:29]
	v_fmac_f32_e32 v178, s25, v132
	v_fmac_f32_e32 v179, s25, v133
	v_fmac_f32_e32 v180, s25, v134
	v_fmac_f32_e32 v181, s25, v135
	v_fmac_f32_e32 v182, s25, v136
	v_fmac_f32_e32 v183, s25, v137
	v_fmac_f32_e32 v184, s25, v138
	v_fmac_f32_e32 v185, s25, v139
	s_waitcnt vmcnt(31)
	v_readlane_b32 s25, v246, 32
	v_cvt_f32_ubyte0_e32 v124, v24
	v_cvt_f32_ubyte1_e32 v125, v24
	v_cvt_f32_ubyte2_e32 v126, v24
	v_cvt_f32_ubyte3_e32 v127, v24
	v_cvt_f32_ubyte0_e32 v128, v25
	v_cvt_f32_ubyte1_e32 v129, v25
	v_cvt_f32_ubyte2_e32 v130, v25
	v_cvt_f32_ubyte3_e32 v131, v25
	s_waitcnt lgkmcnt(0)
	s_load_dwordx16 s[84:99], s[36:37], 0x140
	s_lshl_b32 s30, s68, 12
	s_add_u32 s28, s26, s30
	s_addc_u32 s29, s27, 0
	global_load_dwordx2 v[24:25], v162, s[28:29]
	v_fmac_f32_e32 v178, s25, v124
	v_fmac_f32_e32 v179, s25, v125
	v_fmac_f32_e32 v180, s25, v126
	v_fmac_f32_e32 v181, s25, v127
	v_fmac_f32_e32 v182, s25, v128
	v_fmac_f32_e32 v183, s25, v129
	v_fmac_f32_e32 v184, s25, v130
	v_fmac_f32_e32 v185, s25, v131
	s_waitcnt vmcnt(31)
	v_readlane_b32 s25, v246, 33
	v_cvt_f32_ubyte0_e32 v132, v26
	v_cvt_f32_ubyte1_e32 v133, v26
	v_cvt_f32_ubyte2_e32 v134, v26
	v_cvt_f32_ubyte3_e32 v135, v26
	v_cvt_f32_ubyte0_e32 v136, v27
	v_cvt_f32_ubyte1_e32 v137, v27
	v_cvt_f32_ubyte2_e32 v138, v27
	v_cvt_f32_ubyte3_e32 v139, v27
	s_lshl_b32 s30, s69, 12
	s_add_u32 s28, s26, s30
	s_addc_u32 s29, s27, 0
	global_load_dwordx2 v[26:27], v162, s[28:29]
	v_fmac_f32_e32 v178, s25, v132
	v_fmac_f32_e32 v179, s25, v133
	v_fmac_f32_e32 v180, s25, v134
	v_fmac_f32_e32 v181, s25, v135
	v_fmac_f32_e32 v182, s25, v136
	v_fmac_f32_e32 v183, s25, v137
	v_fmac_f32_e32 v184, s25, v138
	v_fmac_f32_e32 v185, s25, v139
	s_waitcnt vmcnt(31)
	v_readlane_b32 s25, v246, 34
	v_cvt_f32_ubyte0_e32 v124, v28
	v_cvt_f32_ubyte1_e32 v125, v28
	v_cvt_f32_ubyte2_e32 v126, v28
	v_cvt_f32_ubyte3_e32 v127, v28
	v_cvt_f32_ubyte0_e32 v128, v29
	v_cvt_f32_ubyte1_e32 v129, v29
	v_cvt_f32_ubyte2_e32 v130, v29
	v_cvt_f32_ubyte3_e32 v131, v29
	s_lshl_b32 s30, s70, 12
	s_add_u32 s28, s26, s30
	s_addc_u32 s29, s27, 0
	global_load_dwordx2 v[28:29], v162, s[28:29]
	v_fmac_f32_e32 v178, s25, v124
	v_fmac_f32_e32 v179, s25, v125
	v_fmac_f32_e32 v180, s25, v126
	v_fmac_f32_e32 v181, s25, v127
	v_fmac_f32_e32 v182, s25, v128
	v_fmac_f32_e32 v183, s25, v129
	v_fmac_f32_e32 v184, s25, v130
	v_fmac_f32_e32 v185, s25, v131
	s_waitcnt vmcnt(31)
	v_readlane_b32 s25, v246, 35
	v_cvt_f32_ubyte0_e32 v132, v30
	v_cvt_f32_ubyte1_e32 v133, v30
	v_cvt_f32_ubyte2_e32 v134, v30
	v_cvt_f32_ubyte3_e32 v135, v30
	v_cvt_f32_ubyte0_e32 v136, v31
	v_cvt_f32_ubyte1_e32 v137, v31
	v_cvt_f32_ubyte2_e32 v138, v31
	v_cvt_f32_ubyte3_e32 v139, v31
	s_lshl_b32 s30, s71, 12
	s_add_u32 s28, s26, s30
	s_addc_u32 s29, s27, 0
	global_load_dwordx2 v[30:31], v162, s[28:29]
	v_fmac_f32_e32 v178, s25, v132
	v_fmac_f32_e32 v179, s25, v133
	v_fmac_f32_e32 v180, s25, v134
	v_fmac_f32_e32 v181, s25, v135
	v_fmac_f32_e32 v182, s25, v136
	v_fmac_f32_e32 v183, s25, v137
	v_fmac_f32_e32 v184, s25, v138
	v_fmac_f32_e32 v185, s25, v139
	s_waitcnt vmcnt(31)
	v_readlane_b32 s25, v246, 36
	v_cvt_f32_ubyte0_e32 v124, v32
	v_cvt_f32_ubyte1_e32 v125, v32
	v_cvt_f32_ubyte2_e32 v126, v32
	v_cvt_f32_ubyte3_e32 v127, v32
	v_cvt_f32_ubyte0_e32 v128, v33
	v_cvt_f32_ubyte1_e32 v129, v33
	v_cvt_f32_ubyte2_e32 v130, v33
	v_cvt_f32_ubyte3_e32 v131, v33
	s_lshl_b32 s30, s72, 12
	s_add_u32 s28, s26, s30
	s_addc_u32 s29, s27, 0
	global_load_dwordx2 v[32:33], v162, s[28:29]
	v_fmac_f32_e32 v178, s25, v124
	v_fmac_f32_e32 v179, s25, v125
	v_fmac_f32_e32 v180, s25, v126
	v_fmac_f32_e32 v181, s25, v127
	v_fmac_f32_e32 v182, s25, v128
	v_fmac_f32_e32 v183, s25, v129
	v_fmac_f32_e32 v184, s25, v130
	v_fmac_f32_e32 v185, s25, v131
	s_waitcnt vmcnt(31)
	v_readlane_b32 s25, v246, 37
	v_cvt_f32_ubyte0_e32 v132, v34
	v_cvt_f32_ubyte1_e32 v133, v34
	v_cvt_f32_ubyte2_e32 v134, v34
	v_cvt_f32_ubyte3_e32 v135, v34
	v_cvt_f32_ubyte0_e32 v136, v35
	v_cvt_f32_ubyte1_e32 v137, v35
	v_cvt_f32_ubyte2_e32 v138, v35
	v_cvt_f32_ubyte3_e32 v139, v35
	s_lshl_b32 s30, s73, 12
	s_add_u32 s28, s26, s30
	s_addc_u32 s29, s27, 0
	global_load_dwordx2 v[34:35], v162, s[28:29]
	v_fmac_f32_e32 v178, s25, v132
	v_fmac_f32_e32 v179, s25, v133
	v_fmac_f32_e32 v180, s25, v134
	v_fmac_f32_e32 v181, s25, v135
	v_fmac_f32_e32 v182, s25, v136
	v_fmac_f32_e32 v183, s25, v137
	v_fmac_f32_e32 v184, s25, v138
	v_fmac_f32_e32 v185, s25, v139
	s_waitcnt vmcnt(31)
	v_readlane_b32 s25, v246, 38
	v_cvt_f32_ubyte0_e32 v124, v36
	v_cvt_f32_ubyte1_e32 v125, v36
	v_cvt_f32_ubyte2_e32 v126, v36
	v_cvt_f32_ubyte3_e32 v127, v36
	v_cvt_f32_ubyte0_e32 v128, v37
	v_cvt_f32_ubyte1_e32 v129, v37
	v_cvt_f32_ubyte2_e32 v130, v37
	v_cvt_f32_ubyte3_e32 v131, v37
	s_lshl_b32 s30, s74, 12
	s_add_u32 s28, s26, s30
	s_addc_u32 s29, s27, 0
	global_load_dwordx2 v[36:37], v162, s[28:29]
	v_fmac_f32_e32 v178, s25, v124
	v_fmac_f32_e32 v179, s25, v125
	v_fmac_f32_e32 v180, s25, v126
	v_fmac_f32_e32 v181, s25, v127
	v_fmac_f32_e32 v182, s25, v128
	v_fmac_f32_e32 v183, s25, v129
	v_fmac_f32_e32 v184, s25, v130
	v_fmac_f32_e32 v185, s25, v131
	s_waitcnt vmcnt(31)
	v_readlane_b32 s25, v246, 39
	v_cvt_f32_ubyte0_e32 v132, v38
	v_cvt_f32_ubyte1_e32 v133, v38
	v_cvt_f32_ubyte2_e32 v134, v38
	v_cvt_f32_ubyte3_e32 v135, v38
	v_cvt_f32_ubyte0_e32 v136, v39
	v_cvt_f32_ubyte1_e32 v137, v39
	v_cvt_f32_ubyte2_e32 v138, v39
	v_cvt_f32_ubyte3_e32 v139, v39
	s_lshl_b32 s30, s75, 12
	s_add_u32 s28, s26, s30
	s_addc_u32 s29, s27, 0
	global_load_dwordx2 v[38:39], v162, s[28:29]
	v_fmac_f32_e32 v178, s25, v132
	v_fmac_f32_e32 v179, s25, v133
	v_fmac_f32_e32 v180, s25, v134
	v_fmac_f32_e32 v181, s25, v135
	v_fmac_f32_e32 v182, s25, v136
	v_fmac_f32_e32 v183, s25, v137
	v_fmac_f32_e32 v184, s25, v138
	v_fmac_f32_e32 v185, s25, v139
	s_waitcnt vmcnt(31)
	v_readlane_b32 s25, v246, 40
	v_cvt_f32_ubyte0_e32 v124, v40
	v_cvt_f32_ubyte1_e32 v125, v40
	v_cvt_f32_ubyte2_e32 v126, v40
	v_cvt_f32_ubyte3_e32 v127, v40
	v_cvt_f32_ubyte0_e32 v128, v41
	v_cvt_f32_ubyte1_e32 v129, v41
	v_cvt_f32_ubyte2_e32 v130, v41
	v_cvt_f32_ubyte3_e32 v131, v41
	s_lshl_b32 s30, s76, 12
	s_add_u32 s28, s26, s30
	s_addc_u32 s29, s27, 0
	global_load_dwordx2 v[40:41], v162, s[28:29]
	v_fmac_f32_e32 v178, s25, v124
	v_fmac_f32_e32 v179, s25, v125
	v_fmac_f32_e32 v180, s25, v126
	v_fmac_f32_e32 v181, s25, v127
	v_fmac_f32_e32 v182, s25, v128
	v_fmac_f32_e32 v183, s25, v129
	v_fmac_f32_e32 v184, s25, v130
	v_fmac_f32_e32 v185, s25, v131
	s_waitcnt vmcnt(31)
	v_readlane_b32 s25, v246, 41
	v_cvt_f32_ubyte0_e32 v132, v42
	v_cvt_f32_ubyte1_e32 v133, v42
	v_cvt_f32_ubyte2_e32 v134, v42
	v_cvt_f32_ubyte3_e32 v135, v42
	v_cvt_f32_ubyte0_e32 v136, v43
	v_cvt_f32_ubyte1_e32 v137, v43
	v_cvt_f32_ubyte2_e32 v138, v43
	v_cvt_f32_ubyte3_e32 v139, v43
	s_lshl_b32 s30, s77, 12
	s_add_u32 s28, s26, s30
	s_addc_u32 s29, s27, 0
	global_load_dwordx2 v[42:43], v162, s[28:29]
	v_fmac_f32_e32 v178, s25, v132
	v_fmac_f32_e32 v179, s25, v133
	v_fmac_f32_e32 v180, s25, v134
	v_fmac_f32_e32 v181, s25, v135
	v_fmac_f32_e32 v182, s25, v136
	v_fmac_f32_e32 v183, s25, v137
	v_fmac_f32_e32 v184, s25, v138
	v_fmac_f32_e32 v185, s25, v139
	s_waitcnt vmcnt(31)
	v_readlane_b32 s25, v246, 42
	v_cvt_f32_ubyte0_e32 v124, v44
	v_cvt_f32_ubyte1_e32 v125, v44
	v_cvt_f32_ubyte2_e32 v126, v44
	v_cvt_f32_ubyte3_e32 v127, v44
	v_cvt_f32_ubyte0_e32 v128, v45
	v_cvt_f32_ubyte1_e32 v129, v45
	v_cvt_f32_ubyte2_e32 v130, v45
	v_cvt_f32_ubyte3_e32 v131, v45
	s_lshl_b32 s30, s78, 12
	s_add_u32 s28, s26, s30
	s_addc_u32 s29, s27, 0
	global_load_dwordx2 v[44:45], v162, s[28:29]
	v_fmac_f32_e32 v178, s25, v124
	v_fmac_f32_e32 v179, s25, v125
	v_fmac_f32_e32 v180, s25, v126
	v_fmac_f32_e32 v181, s25, v127
	v_fmac_f32_e32 v182, s25, v128
	v_fmac_f32_e32 v183, s25, v129
	v_fmac_f32_e32 v184, s25, v130
	v_fmac_f32_e32 v185, s25, v131
	s_waitcnt vmcnt(31)
	v_readlane_b32 s25, v246, 43
	v_cvt_f32_ubyte0_e32 v132, v46
	v_cvt_f32_ubyte1_e32 v133, v46
	v_cvt_f32_ubyte2_e32 v134, v46
	v_cvt_f32_ubyte3_e32 v135, v46
	v_cvt_f32_ubyte0_e32 v136, v47
	v_cvt_f32_ubyte1_e32 v137, v47
	v_cvt_f32_ubyte2_e32 v138, v47
	v_cvt_f32_ubyte3_e32 v139, v47
	s_lshl_b32 s30, s79, 12
	s_add_u32 s28, s26, s30
	s_addc_u32 s29, s27, 0
	global_load_dwordx2 v[46:47], v162, s[28:29]
	v_fmac_f32_e32 v178, s25, v132
	v_fmac_f32_e32 v179, s25, v133
	v_fmac_f32_e32 v180, s25, v134
	v_fmac_f32_e32 v181, s25, v135
	v_fmac_f32_e32 v182, s25, v136
	v_fmac_f32_e32 v183, s25, v137
	v_fmac_f32_e32 v184, s25, v138
	v_fmac_f32_e32 v185, s25, v139
	s_waitcnt vmcnt(31)
	v_readlane_b32 s25, v246, 44
	v_cvt_f32_ubyte0_e32 v124, v48
	v_cvt_f32_ubyte1_e32 v125, v48
	v_cvt_f32_ubyte2_e32 v126, v48
	v_cvt_f32_ubyte3_e32 v127, v48
	v_cvt_f32_ubyte0_e32 v128, v49
	v_cvt_f32_ubyte1_e32 v129, v49
	v_cvt_f32_ubyte2_e32 v130, v49
	v_cvt_f32_ubyte3_e32 v131, v49
	s_lshl_b32 s30, s80, 12
	s_add_u32 s28, s26, s30
	s_addc_u32 s29, s27, 0
	global_load_dwordx2 v[48:49], v162, s[28:29]
	v_fmac_f32_e32 v178, s25, v124
	v_fmac_f32_e32 v179, s25, v125
	v_fmac_f32_e32 v180, s25, v126
	v_fmac_f32_e32 v181, s25, v127
	v_fmac_f32_e32 v182, s25, v128
	v_fmac_f32_e32 v183, s25, v129
	v_fmac_f32_e32 v184, s25, v130
	v_fmac_f32_e32 v185, s25, v131
	s_waitcnt vmcnt(31)
	v_readlane_b32 s25, v246, 45
	v_cvt_f32_ubyte0_e32 v132, v50
	v_cvt_f32_ubyte1_e32 v133, v50
	v_cvt_f32_ubyte2_e32 v134, v50
	v_cvt_f32_ubyte3_e32 v135, v50
	v_cvt_f32_ubyte0_e32 v136, v51
	v_cvt_f32_ubyte1_e32 v137, v51
	v_cvt_f32_ubyte2_e32 v138, v51
	v_cvt_f32_ubyte3_e32 v139, v51
	s_lshl_b32 s30, s81, 12
	s_add_u32 s28, s26, s30
	s_addc_u32 s29, s27, 0
	global_load_dwordx2 v[50:51], v162, s[28:29]
	v_fmac_f32_e32 v178, s25, v132
	v_fmac_f32_e32 v179, s25, v133
	v_fmac_f32_e32 v180, s25, v134
	v_fmac_f32_e32 v181, s25, v135
	v_fmac_f32_e32 v182, s25, v136
	v_fmac_f32_e32 v183, s25, v137
	v_fmac_f32_e32 v184, s25, v138
	v_fmac_f32_e32 v185, s25, v139
	s_waitcnt vmcnt(31)
	v_readlane_b32 s25, v246, 46
	v_cvt_f32_ubyte0_e32 v124, v52
	v_cvt_f32_ubyte1_e32 v125, v52
	v_cvt_f32_ubyte2_e32 v126, v52
	v_cvt_f32_ubyte3_e32 v127, v52
	v_cvt_f32_ubyte0_e32 v128, v53
	v_cvt_f32_ubyte1_e32 v129, v53
	v_cvt_f32_ubyte2_e32 v130, v53
	v_cvt_f32_ubyte3_e32 v131, v53
	s_lshl_b32 s30, s82, 12
	s_add_u32 s28, s26, s30
	s_addc_u32 s29, s27, 0
	global_load_dwordx2 v[52:53], v162, s[28:29]
	v_fmac_f32_e32 v178, s25, v124
	v_fmac_f32_e32 v179, s25, v125
	v_fmac_f32_e32 v180, s25, v126
	v_fmac_f32_e32 v181, s25, v127
	v_fmac_f32_e32 v182, s25, v128
	v_fmac_f32_e32 v183, s25, v129
	v_fmac_f32_e32 v184, s25, v130
	v_fmac_f32_e32 v185, s25, v131
	s_waitcnt vmcnt(31)
	v_readlane_b32 s25, v246, 47
	v_cvt_f32_ubyte0_e32 v132, v54
	v_cvt_f32_ubyte1_e32 v133, v54
	v_cvt_f32_ubyte2_e32 v134, v54
	v_cvt_f32_ubyte3_e32 v135, v54
	v_cvt_f32_ubyte0_e32 v136, v55
	v_cvt_f32_ubyte1_e32 v137, v55
	v_cvt_f32_ubyte2_e32 v138, v55
	v_cvt_f32_ubyte3_e32 v139, v55
	s_lshl_b32 s30, s83, 12
	s_add_u32 s28, s26, s30
	s_addc_u32 s29, s27, 0
	global_load_dwordx2 v[54:55], v162, s[28:29]
	v_fmac_f32_e32 v178, s25, v132
	v_fmac_f32_e32 v179, s25, v133
	v_fmac_f32_e32 v180, s25, v134
	v_fmac_f32_e32 v181, s25, v135
	v_fmac_f32_e32 v182, s25, v136
	v_fmac_f32_e32 v183, s25, v137
	v_fmac_f32_e32 v184, s25, v138
	v_fmac_f32_e32 v185, s25, v139
	s_waitcnt vmcnt(31)
	v_readlane_b32 s25, v246, 48
	v_cvt_f32_ubyte0_e32 v124, v56
	v_cvt_f32_ubyte1_e32 v125, v56
	v_cvt_f32_ubyte2_e32 v126, v56
	v_cvt_f32_ubyte3_e32 v127, v56
	v_cvt_f32_ubyte0_e32 v128, v57
	v_cvt_f32_ubyte1_e32 v129, v57
	v_cvt_f32_ubyte2_e32 v130, v57
	v_cvt_f32_ubyte3_e32 v131, v57
	s_waitcnt lgkmcnt(0)
	s_load_dwordx16 s[68:83], s[36:37], 0x180
	s_lshl_b32 s30, s84, 12
	s_add_u32 s28, s26, s30
	s_addc_u32 s29, s27, 0
	global_load_dwordx2 v[56:57], v162, s[28:29]
	v_fmac_f32_e32 v178, s25, v124
	v_fmac_f32_e32 v179, s25, v125
	v_fmac_f32_e32 v180, s25, v126
	v_fmac_f32_e32 v181, s25, v127
	v_fmac_f32_e32 v182, s25, v128
	v_fmac_f32_e32 v183, s25, v129
	v_fmac_f32_e32 v184, s25, v130
	v_fmac_f32_e32 v185, s25, v131
	s_waitcnt vmcnt(31)
	v_readlane_b32 s25, v246, 49
	v_cvt_f32_ubyte0_e32 v132, v58
	v_cvt_f32_ubyte1_e32 v133, v58
	v_cvt_f32_ubyte2_e32 v134, v58
	v_cvt_f32_ubyte3_e32 v135, v58
	v_cvt_f32_ubyte0_e32 v136, v59
	v_cvt_f32_ubyte1_e32 v137, v59
	v_cvt_f32_ubyte2_e32 v138, v59
	v_cvt_f32_ubyte3_e32 v139, v59
	s_lshl_b32 s30, s85, 12
	s_add_u32 s28, s26, s30
	s_addc_u32 s29, s27, 0
	global_load_dwordx2 v[58:59], v162, s[28:29]
	v_fmac_f32_e32 v178, s25, v132
	v_fmac_f32_e32 v179, s25, v133
	v_fmac_f32_e32 v180, s25, v134
	v_fmac_f32_e32 v181, s25, v135
	v_fmac_f32_e32 v182, s25, v136
	v_fmac_f32_e32 v183, s25, v137
	v_fmac_f32_e32 v184, s25, v138
	v_fmac_f32_e32 v185, s25, v139
	s_waitcnt vmcnt(31)
	v_readlane_b32 s25, v246, 50
	v_cvt_f32_ubyte0_e32 v124, v60
	v_cvt_f32_ubyte1_e32 v125, v60
	v_cvt_f32_ubyte2_e32 v126, v60
	v_cvt_f32_ubyte3_e32 v127, v60
	v_cvt_f32_ubyte0_e32 v128, v61
	v_cvt_f32_ubyte1_e32 v129, v61
	v_cvt_f32_ubyte2_e32 v130, v61
	v_cvt_f32_ubyte3_e32 v131, v61
	s_lshl_b32 s30, s86, 12
	s_add_u32 s28, s26, s30
	s_addc_u32 s29, s27, 0
	global_load_dwordx2 v[60:61], v162, s[28:29]
	v_fmac_f32_e32 v178, s25, v124
	v_fmac_f32_e32 v179, s25, v125
	v_fmac_f32_e32 v180, s25, v126
	v_fmac_f32_e32 v181, s25, v127
	v_fmac_f32_e32 v182, s25, v128
	v_fmac_f32_e32 v183, s25, v129
	v_fmac_f32_e32 v184, s25, v130
	v_fmac_f32_e32 v185, s25, v131
	s_waitcnt vmcnt(31)
	v_readlane_b32 s25, v246, 51
	v_cvt_f32_ubyte0_e32 v132, v62
	v_cvt_f32_ubyte1_e32 v133, v62
	v_cvt_f32_ubyte2_e32 v134, v62
	v_cvt_f32_ubyte3_e32 v135, v62
	v_cvt_f32_ubyte0_e32 v136, v63
	v_cvt_f32_ubyte1_e32 v137, v63
	v_cvt_f32_ubyte2_e32 v138, v63
	v_cvt_f32_ubyte3_e32 v139, v63
	s_lshl_b32 s30, s87, 12
	s_add_u32 s28, s26, s30
	s_addc_u32 s29, s27, 0
	global_load_dwordx2 v[62:63], v162, s[28:29]
	v_fmac_f32_e32 v178, s25, v132
	v_fmac_f32_e32 v179, s25, v133
	v_fmac_f32_e32 v180, s25, v134
	v_fmac_f32_e32 v181, s25, v135
	v_fmac_f32_e32 v182, s25, v136
	v_fmac_f32_e32 v183, s25, v137
	v_fmac_f32_e32 v184, s25, v138
	v_fmac_f32_e32 v185, s25, v139
	s_waitcnt vmcnt(31)
	v_readlane_b32 s25, v246, 52
	v_cvt_f32_ubyte0_e32 v124, v64
	v_cvt_f32_ubyte1_e32 v125, v64
	v_cvt_f32_ubyte2_e32 v126, v64
	v_cvt_f32_ubyte3_e32 v127, v64
	v_cvt_f32_ubyte0_e32 v128, v65
	v_cvt_f32_ubyte1_e32 v129, v65
	v_cvt_f32_ubyte2_e32 v130, v65
	v_cvt_f32_ubyte3_e32 v131, v65
	s_lshl_b32 s30, s88, 12
	s_add_u32 s28, s26, s30
	s_addc_u32 s29, s27, 0
	global_load_dwordx2 v[64:65], v162, s[28:29]
	v_fmac_f32_e32 v178, s25, v124
	v_fmac_f32_e32 v179, s25, v125
	v_fmac_f32_e32 v180, s25, v126
	v_fmac_f32_e32 v181, s25, v127
	v_fmac_f32_e32 v182, s25, v128
	v_fmac_f32_e32 v183, s25, v129
	v_fmac_f32_e32 v184, s25, v130
	v_fmac_f32_e32 v185, s25, v131
	s_waitcnt vmcnt(31)
	v_readlane_b32 s25, v246, 53
	v_cvt_f32_ubyte0_e32 v132, v66
	v_cvt_f32_ubyte1_e32 v133, v66
	v_cvt_f32_ubyte2_e32 v134, v66
	v_cvt_f32_ubyte3_e32 v135, v66
	v_cvt_f32_ubyte0_e32 v136, v67
	v_cvt_f32_ubyte1_e32 v137, v67
	v_cvt_f32_ubyte2_e32 v138, v67
	v_cvt_f32_ubyte3_e32 v139, v67
	s_lshl_b32 s30, s89, 12
	s_add_u32 s28, s26, s30
	s_addc_u32 s29, s27, 0
	global_load_dwordx2 v[66:67], v162, s[28:29]
	v_fmac_f32_e32 v178, s25, v132
	v_fmac_f32_e32 v179, s25, v133
	v_fmac_f32_e32 v180, s25, v134
	v_fmac_f32_e32 v181, s25, v135
	v_fmac_f32_e32 v182, s25, v136
	v_fmac_f32_e32 v183, s25, v137
	v_fmac_f32_e32 v184, s25, v138
	v_fmac_f32_e32 v185, s25, v139
	s_waitcnt vmcnt(31)
	v_readlane_b32 s25, v246, 54
	v_cvt_f32_ubyte0_e32 v124, v68
	v_cvt_f32_ubyte1_e32 v125, v68
	v_cvt_f32_ubyte2_e32 v126, v68
	v_cvt_f32_ubyte3_e32 v127, v68
	v_cvt_f32_ubyte0_e32 v128, v69
	v_cvt_f32_ubyte1_e32 v129, v69
	v_cvt_f32_ubyte2_e32 v130, v69
	v_cvt_f32_ubyte3_e32 v131, v69
	s_lshl_b32 s30, s90, 12
	s_add_u32 s28, s26, s30
	s_addc_u32 s29, s27, 0
	global_load_dwordx2 v[68:69], v162, s[28:29]
	v_fmac_f32_e32 v178, s25, v124
	v_fmac_f32_e32 v179, s25, v125
	v_fmac_f32_e32 v180, s25, v126
	v_fmac_f32_e32 v181, s25, v127
	v_fmac_f32_e32 v182, s25, v128
	v_fmac_f32_e32 v183, s25, v129
	v_fmac_f32_e32 v184, s25, v130
	v_fmac_f32_e32 v185, s25, v131
	s_waitcnt vmcnt(31)
	v_readlane_b32 s25, v246, 55
	v_cvt_f32_ubyte0_e32 v132, v70
	v_cvt_f32_ubyte1_e32 v133, v70
	v_cvt_f32_ubyte2_e32 v134, v70
	v_cvt_f32_ubyte3_e32 v135, v70
	v_cvt_f32_ubyte0_e32 v136, v71
	v_cvt_f32_ubyte1_e32 v137, v71
	v_cvt_f32_ubyte2_e32 v138, v71
	v_cvt_f32_ubyte3_e32 v139, v71
	s_lshl_b32 s30, s91, 12
	s_add_u32 s28, s26, s30
	s_addc_u32 s29, s27, 0
	global_load_dwordx2 v[70:71], v162, s[28:29]
	v_fmac_f32_e32 v178, s25, v132
	v_fmac_f32_e32 v179, s25, v133
	v_fmac_f32_e32 v180, s25, v134
	v_fmac_f32_e32 v181, s25, v135
	v_fmac_f32_e32 v182, s25, v136
	v_fmac_f32_e32 v183, s25, v137
	v_fmac_f32_e32 v184, s25, v138
	v_fmac_f32_e32 v185, s25, v139
	s_waitcnt vmcnt(31)
	v_readlane_b32 s25, v246, 56
	v_cvt_f32_ubyte0_e32 v124, v72
	v_cvt_f32_ubyte1_e32 v125, v72
	v_cvt_f32_ubyte2_e32 v126, v72
	v_cvt_f32_ubyte3_e32 v127, v72
	v_cvt_f32_ubyte0_e32 v128, v73
	v_cvt_f32_ubyte1_e32 v129, v73
	v_cvt_f32_ubyte2_e32 v130, v73
	v_cvt_f32_ubyte3_e32 v131, v73
	s_lshl_b32 s30, s92, 12
	s_add_u32 s28, s26, s30
	s_addc_u32 s29, s27, 0
	global_load_dwordx2 v[72:73], v162, s[28:29]
	v_fmac_f32_e32 v178, s25, v124
	v_fmac_f32_e32 v179, s25, v125
	v_fmac_f32_e32 v180, s25, v126
	v_fmac_f32_e32 v181, s25, v127
	v_fmac_f32_e32 v182, s25, v128
	v_fmac_f32_e32 v183, s25, v129
	v_fmac_f32_e32 v184, s25, v130
	v_fmac_f32_e32 v185, s25, v131
	s_waitcnt vmcnt(31)
	v_readlane_b32 s25, v246, 57
	v_cvt_f32_ubyte0_e32 v132, v74
	v_cvt_f32_ubyte1_e32 v133, v74
	v_cvt_f32_ubyte2_e32 v134, v74
	v_cvt_f32_ubyte3_e32 v135, v74
	v_cvt_f32_ubyte0_e32 v136, v75
	v_cvt_f32_ubyte1_e32 v137, v75
	v_cvt_f32_ubyte2_e32 v138, v75
	v_cvt_f32_ubyte3_e32 v139, v75
	s_lshl_b32 s30, s93, 12
	s_add_u32 s28, s26, s30
	s_addc_u32 s29, s27, 0
	global_load_dwordx2 v[74:75], v162, s[28:29]
	v_fmac_f32_e32 v178, s25, v132
	v_fmac_f32_e32 v179, s25, v133
	v_fmac_f32_e32 v180, s25, v134
	v_fmac_f32_e32 v181, s25, v135
	v_fmac_f32_e32 v182, s25, v136
	v_fmac_f32_e32 v183, s25, v137
	v_fmac_f32_e32 v184, s25, v138
	v_fmac_f32_e32 v185, s25, v139
	s_waitcnt vmcnt(31)
	v_readlane_b32 s25, v246, 58
	v_cvt_f32_ubyte0_e32 v124, v76
	v_cvt_f32_ubyte1_e32 v125, v76
	v_cvt_f32_ubyte2_e32 v126, v76
	v_cvt_f32_ubyte3_e32 v127, v76
	v_cvt_f32_ubyte0_e32 v128, v77
	v_cvt_f32_ubyte1_e32 v129, v77
	v_cvt_f32_ubyte2_e32 v130, v77
	v_cvt_f32_ubyte3_e32 v131, v77
	s_lshl_b32 s30, s94, 12
	s_add_u32 s28, s26, s30
	s_addc_u32 s29, s27, 0
	global_load_dwordx2 v[76:77], v162, s[28:29]
	v_fmac_f32_e32 v178, s25, v124
	v_fmac_f32_e32 v179, s25, v125
	v_fmac_f32_e32 v180, s25, v126
	v_fmac_f32_e32 v181, s25, v127
	v_fmac_f32_e32 v182, s25, v128
	v_fmac_f32_e32 v183, s25, v129
	v_fmac_f32_e32 v184, s25, v130
	v_fmac_f32_e32 v185, s25, v131
	s_waitcnt vmcnt(31)
	v_readlane_b32 s25, v246, 59
	v_cvt_f32_ubyte0_e32 v132, v78
	v_cvt_f32_ubyte1_e32 v133, v78
	v_cvt_f32_ubyte2_e32 v134, v78
	v_cvt_f32_ubyte3_e32 v135, v78
	v_cvt_f32_ubyte0_e32 v136, v79
	v_cvt_f32_ubyte1_e32 v137, v79
	v_cvt_f32_ubyte2_e32 v138, v79
	v_cvt_f32_ubyte3_e32 v139, v79
	s_lshl_b32 s30, s95, 12
	s_add_u32 s28, s26, s30
	s_addc_u32 s29, s27, 0
	global_load_dwordx2 v[78:79], v162, s[28:29]
	v_fmac_f32_e32 v178, s25, v132
	v_fmac_f32_e32 v179, s25, v133
	v_fmac_f32_e32 v180, s25, v134
	v_fmac_f32_e32 v181, s25, v135
	v_fmac_f32_e32 v182, s25, v136
	v_fmac_f32_e32 v183, s25, v137
	v_fmac_f32_e32 v184, s25, v138
	v_fmac_f32_e32 v185, s25, v139
	s_waitcnt vmcnt(31)
	v_readlane_b32 s25, v246, 60
	v_cvt_f32_ubyte0_e32 v124, v80
	v_cvt_f32_ubyte1_e32 v125, v80
	v_cvt_f32_ubyte2_e32 v126, v80
	v_cvt_f32_ubyte3_e32 v127, v80
	v_cvt_f32_ubyte0_e32 v128, v81
	v_cvt_f32_ubyte1_e32 v129, v81
	v_cvt_f32_ubyte2_e32 v130, v81
	v_cvt_f32_ubyte3_e32 v131, v81
	s_lshl_b32 s30, s96, 12
	s_add_u32 s28, s26, s30
	s_addc_u32 s29, s27, 0
	global_load_dwordx2 v[80:81], v162, s[28:29]
	v_fmac_f32_e32 v178, s25, v124
	v_fmac_f32_e32 v179, s25, v125
	v_fmac_f32_e32 v180, s25, v126
	v_fmac_f32_e32 v181, s25, v127
	v_fmac_f32_e32 v182, s25, v128
	v_fmac_f32_e32 v183, s25, v129
	v_fmac_f32_e32 v184, s25, v130
	v_fmac_f32_e32 v185, s25, v131
	s_waitcnt vmcnt(31)
	v_readlane_b32 s25, v246, 61
	v_cvt_f32_ubyte0_e32 v132, v82
	v_cvt_f32_ubyte1_e32 v133, v82
	v_cvt_f32_ubyte2_e32 v134, v82
	v_cvt_f32_ubyte3_e32 v135, v82
	v_cvt_f32_ubyte0_e32 v136, v83
	v_cvt_f32_ubyte1_e32 v137, v83
	v_cvt_f32_ubyte2_e32 v138, v83
	v_cvt_f32_ubyte3_e32 v139, v83
	s_lshl_b32 s30, s97, 12
	s_add_u32 s28, s26, s30
	s_addc_u32 s29, s27, 0
	global_load_dwordx2 v[82:83], v162, s[28:29]
	v_fmac_f32_e32 v178, s25, v132
	v_fmac_f32_e32 v179, s25, v133
	v_fmac_f32_e32 v180, s25, v134
	v_fmac_f32_e32 v181, s25, v135
	v_fmac_f32_e32 v182, s25, v136
	v_fmac_f32_e32 v183, s25, v137
	v_fmac_f32_e32 v184, s25, v138
	v_fmac_f32_e32 v185, s25, v139
	s_waitcnt vmcnt(31)
	v_readlane_b32 s25, v246, 62
	v_cvt_f32_ubyte0_e32 v124, v84
	v_cvt_f32_ubyte1_e32 v125, v84
	v_cvt_f32_ubyte2_e32 v126, v84
	v_cvt_f32_ubyte3_e32 v127, v84
	v_cvt_f32_ubyte0_e32 v128, v85
	v_cvt_f32_ubyte1_e32 v129, v85
	v_cvt_f32_ubyte2_e32 v130, v85
	v_cvt_f32_ubyte3_e32 v131, v85
	s_lshl_b32 s30, s98, 12
	s_add_u32 s28, s26, s30
	s_addc_u32 s29, s27, 0
	global_load_dwordx2 v[84:85], v162, s[28:29]
	v_fmac_f32_e32 v178, s25, v124
	v_fmac_f32_e32 v179, s25, v125
	v_fmac_f32_e32 v180, s25, v126
	v_fmac_f32_e32 v181, s25, v127
	v_fmac_f32_e32 v182, s25, v128
	v_fmac_f32_e32 v183, s25, v129
	v_fmac_f32_e32 v184, s25, v130
	v_fmac_f32_e32 v185, s25, v131
	s_waitcnt vmcnt(31)
	v_readlane_b32 s25, v246, 63
	v_cvt_f32_ubyte0_e32 v132, v86
	v_cvt_f32_ubyte1_e32 v133, v86
	v_cvt_f32_ubyte2_e32 v134, v86
	v_cvt_f32_ubyte3_e32 v135, v86
	v_cvt_f32_ubyte0_e32 v136, v87
	v_cvt_f32_ubyte1_e32 v137, v87
	v_cvt_f32_ubyte2_e32 v138, v87
	v_cvt_f32_ubyte3_e32 v139, v87
	s_lshl_b32 s30, s99, 12
	s_add_u32 s28, s26, s30
	s_addc_u32 s29, s27, 0
	global_load_dwordx2 v[86:87], v162, s[28:29]
	v_fmac_f32_e32 v178, s25, v132
	v_fmac_f32_e32 v179, s25, v133
	v_fmac_f32_e32 v180, s25, v134
	v_fmac_f32_e32 v181, s25, v135
	v_fmac_f32_e32 v182, s25, v136
	v_fmac_f32_e32 v183, s25, v137
	v_fmac_f32_e32 v184, s25, v138
	v_fmac_f32_e32 v185, s25, v139
	s_waitcnt vmcnt(31)
	v_readlane_b32 s25, v247, 0
	v_cvt_f32_ubyte0_e32 v124, v24
	v_cvt_f32_ubyte1_e32 v125, v24
	v_cvt_f32_ubyte2_e32 v126, v24
	v_cvt_f32_ubyte3_e32 v127, v24
	v_cvt_f32_ubyte0_e32 v128, v25
	v_cvt_f32_ubyte1_e32 v129, v25
	v_cvt_f32_ubyte2_e32 v130, v25
	v_cvt_f32_ubyte3_e32 v131, v25
	s_waitcnt lgkmcnt(0)
	s_load_dwordx16 s[84:99], s[36:37], 0x1c0
	s_lshl_b32 s30, s68, 12
	s_add_u32 s28, s26, s30
	s_addc_u32 s29, s27, 0
	global_load_dwordx2 v[24:25], v162, s[28:29]
	v_lshlrev_b32_e32 v16, 2, v122
	v_lshlrev_b32_e32 v17, 2, v123
	global_load_dword v238, v16, s[64:65]
	global_load_dword v240, v16, s[60:61]
	global_load_dword v239, v17, s[64:65]
	global_load_dword v241, v17, s[60:61]
	v_fmac_f32_e32 v178, s25, v124
	v_fmac_f32_e32 v179, s25, v125
	v_fmac_f32_e32 v180, s25, v126
	v_fmac_f32_e32 v181, s25, v127
	v_fmac_f32_e32 v182, s25, v128
	v_fmac_f32_e32 v183, s25, v129
	v_fmac_f32_e32 v184, s25, v130
	v_fmac_f32_e32 v185, s25, v131
	s_waitcnt vmcnt(35)
	v_readlane_b32 s25, v247, 1
	v_cvt_f32_ubyte0_e32 v132, v26
	v_cvt_f32_ubyte1_e32 v133, v26
	v_cvt_f32_ubyte2_e32 v134, v26
	v_cvt_f32_ubyte3_e32 v135, v26
	v_cvt_f32_ubyte0_e32 v136, v27
	v_cvt_f32_ubyte1_e32 v137, v27
	v_cvt_f32_ubyte2_e32 v138, v27
	v_cvt_f32_ubyte3_e32 v139, v27
	s_lshl_b32 s30, s69, 12
	s_add_u32 s28, s26, s30
	s_addc_u32 s29, s27, 0
	global_load_dwordx2 v[26:27], v162, s[28:29]
	v_fmac_f32_e32 v178, s25, v132
	v_fmac_f32_e32 v179, s25, v133
	v_fmac_f32_e32 v180, s25, v134
	v_fmac_f32_e32 v181, s25, v135
	v_fmac_f32_e32 v182, s25, v136
	v_fmac_f32_e32 v183, s25, v137
	v_fmac_f32_e32 v184, s25, v138
	v_fmac_f32_e32 v185, s25, v139
	s_waitcnt vmcnt(35)
	v_readlane_b32 s25, v247, 2
	v_cvt_f32_ubyte0_e32 v124, v28
	v_cvt_f32_ubyte1_e32 v125, v28
	v_cvt_f32_ubyte2_e32 v126, v28
	v_cvt_f32_ubyte3_e32 v127, v28
	v_cvt_f32_ubyte0_e32 v128, v29
	v_cvt_f32_ubyte1_e32 v129, v29
	v_cvt_f32_ubyte2_e32 v130, v29
	v_cvt_f32_ubyte3_e32 v131, v29
	s_lshl_b32 s30, s70, 12
	s_add_u32 s28, s26, s30
	s_addc_u32 s29, s27, 0
	global_load_dwordx2 v[28:29], v162, s[28:29]
	v_fmac_f32_e32 v178, s25, v124
	v_fmac_f32_e32 v179, s25, v125
	v_fmac_f32_e32 v180, s25, v126
	v_fmac_f32_e32 v181, s25, v127
	v_fmac_f32_e32 v182, s25, v128
	v_fmac_f32_e32 v183, s25, v129
	v_fmac_f32_e32 v184, s25, v130
	v_fmac_f32_e32 v185, s25, v131
	s_waitcnt vmcnt(35)
	v_readlane_b32 s25, v247, 3
	v_cvt_f32_ubyte0_e32 v132, v30
	v_cvt_f32_ubyte1_e32 v133, v30
	v_cvt_f32_ubyte2_e32 v134, v30
	v_cvt_f32_ubyte3_e32 v135, v30
	v_cvt_f32_ubyte0_e32 v136, v31
	v_cvt_f32_ubyte1_e32 v137, v31
	v_cvt_f32_ubyte2_e32 v138, v31
	v_cvt_f32_ubyte3_e32 v139, v31
	s_lshl_b32 s30, s71, 12
	s_add_u32 s28, s26, s30
	s_addc_u32 s29, s27, 0
	global_load_dwordx2 v[30:31], v162, s[28:29]
	v_fmac_f32_e32 v178, s25, v132
	v_fmac_f32_e32 v179, s25, v133
	v_fmac_f32_e32 v180, s25, v134
	v_fmac_f32_e32 v181, s25, v135
	v_fmac_f32_e32 v182, s25, v136
	v_fmac_f32_e32 v183, s25, v137
	v_fmac_f32_e32 v184, s25, v138
	v_fmac_f32_e32 v185, s25, v139
	s_waitcnt vmcnt(35)
	v_readlane_b32 s25, v247, 4
	v_cvt_f32_ubyte0_e32 v124, v32
	v_cvt_f32_ubyte1_e32 v125, v32
	v_cvt_f32_ubyte2_e32 v126, v32
	v_cvt_f32_ubyte3_e32 v127, v32
	v_cvt_f32_ubyte0_e32 v128, v33
	v_cvt_f32_ubyte1_e32 v129, v33
	v_cvt_f32_ubyte2_e32 v130, v33
	v_cvt_f32_ubyte3_e32 v131, v33
	s_lshl_b32 s30, s72, 12
	s_add_u32 s28, s26, s30
	s_addc_u32 s29, s27, 0
	global_load_dwordx2 v[32:33], v162, s[28:29]
	v_fmac_f32_e32 v178, s25, v124
	v_fmac_f32_e32 v179, s25, v125
	v_fmac_f32_e32 v180, s25, v126
	v_fmac_f32_e32 v181, s25, v127
	v_fmac_f32_e32 v182, s25, v128
	v_fmac_f32_e32 v183, s25, v129
	v_fmac_f32_e32 v184, s25, v130
	v_fmac_f32_e32 v185, s25, v131
	s_waitcnt vmcnt(35)
	v_readlane_b32 s25, v247, 5
	v_cvt_f32_ubyte0_e32 v132, v34
	v_cvt_f32_ubyte1_e32 v133, v34
	v_cvt_f32_ubyte2_e32 v134, v34
	v_cvt_f32_ubyte3_e32 v135, v34
	v_cvt_f32_ubyte0_e32 v136, v35
	v_cvt_f32_ubyte1_e32 v137, v35
	v_cvt_f32_ubyte2_e32 v138, v35
	v_cvt_f32_ubyte3_e32 v139, v35
	s_lshl_b32 s30, s73, 12
	s_add_u32 s28, s26, s30
	s_addc_u32 s29, s27, 0
	global_load_dwordx2 v[34:35], v162, s[28:29]
	v_fmac_f32_e32 v178, s25, v132
	v_fmac_f32_e32 v179, s25, v133
	v_fmac_f32_e32 v180, s25, v134
	v_fmac_f32_e32 v181, s25, v135
	v_fmac_f32_e32 v182, s25, v136
	v_fmac_f32_e32 v183, s25, v137
	v_fmac_f32_e32 v184, s25, v138
	v_fmac_f32_e32 v185, s25, v139
	s_waitcnt vmcnt(35)
	v_readlane_b32 s25, v247, 6
	v_cvt_f32_ubyte0_e32 v124, v36
	v_cvt_f32_ubyte1_e32 v125, v36
	v_cvt_f32_ubyte2_e32 v126, v36
	v_cvt_f32_ubyte3_e32 v127, v36
	v_cvt_f32_ubyte0_e32 v128, v37
	v_cvt_f32_ubyte1_e32 v129, v37
	v_cvt_f32_ubyte2_e32 v130, v37
	v_cvt_f32_ubyte3_e32 v131, v37
	s_lshl_b32 s30, s74, 12
	s_add_u32 s28, s26, s30
	s_addc_u32 s29, s27, 0
	global_load_dwordx2 v[36:37], v162, s[28:29]
	v_fmac_f32_e32 v178, s25, v124
	v_fmac_f32_e32 v179, s25, v125
	v_fmac_f32_e32 v180, s25, v126
	v_fmac_f32_e32 v181, s25, v127
	v_fmac_f32_e32 v182, s25, v128
	v_fmac_f32_e32 v183, s25, v129
	v_fmac_f32_e32 v184, s25, v130
	v_fmac_f32_e32 v185, s25, v131
	s_waitcnt vmcnt(35)
	v_readlane_b32 s25, v247, 7
	v_cvt_f32_ubyte0_e32 v132, v38
	v_cvt_f32_ubyte1_e32 v133, v38
	v_cvt_f32_ubyte2_e32 v134, v38
	v_cvt_f32_ubyte3_e32 v135, v38
	v_cvt_f32_ubyte0_e32 v136, v39
	v_cvt_f32_ubyte1_e32 v137, v39
	v_cvt_f32_ubyte2_e32 v138, v39
	v_cvt_f32_ubyte3_e32 v139, v39
	s_lshl_b32 s30, s75, 12
	s_add_u32 s28, s26, s30
	s_addc_u32 s29, s27, 0
	global_load_dwordx2 v[38:39], v162, s[28:29]
	v_fmac_f32_e32 v178, s25, v132
	v_fmac_f32_e32 v179, s25, v133
	v_fmac_f32_e32 v180, s25, v134
	v_fmac_f32_e32 v181, s25, v135
	v_fmac_f32_e32 v182, s25, v136
	v_fmac_f32_e32 v183, s25, v137
	v_fmac_f32_e32 v184, s25, v138
	v_fmac_f32_e32 v185, s25, v139
	s_waitcnt vmcnt(35)
	v_readlane_b32 s25, v247, 8
	v_cvt_f32_ubyte0_e32 v124, v40
	v_cvt_f32_ubyte1_e32 v125, v40
	v_cvt_f32_ubyte2_e32 v126, v40
	v_cvt_f32_ubyte3_e32 v127, v40
	v_cvt_f32_ubyte0_e32 v128, v41
	v_cvt_f32_ubyte1_e32 v129, v41
	v_cvt_f32_ubyte2_e32 v130, v41
	v_cvt_f32_ubyte3_e32 v131, v41
	s_lshl_b32 s30, s76, 12
	s_add_u32 s28, s26, s30
	s_addc_u32 s29, s27, 0
	global_load_dwordx2 v[40:41], v162, s[28:29]
	v_fmac_f32_e32 v178, s25, v124
	v_fmac_f32_e32 v179, s25, v125
	v_fmac_f32_e32 v180, s25, v126
	v_fmac_f32_e32 v181, s25, v127
	v_fmac_f32_e32 v182, s25, v128
	v_fmac_f32_e32 v183, s25, v129
	v_fmac_f32_e32 v184, s25, v130
	v_fmac_f32_e32 v185, s25, v131
	s_waitcnt vmcnt(35)
	v_readlane_b32 s25, v247, 9
	v_cvt_f32_ubyte0_e32 v132, v42
	v_cvt_f32_ubyte1_e32 v133, v42
	v_cvt_f32_ubyte2_e32 v134, v42
	v_cvt_f32_ubyte3_e32 v135, v42
	v_cvt_f32_ubyte0_e32 v136, v43
	v_cvt_f32_ubyte1_e32 v137, v43
	v_cvt_f32_ubyte2_e32 v138, v43
	v_cvt_f32_ubyte3_e32 v139, v43
	s_lshl_b32 s30, s77, 12
	s_add_u32 s28, s26, s30
	s_addc_u32 s29, s27, 0
	global_load_dwordx2 v[42:43], v162, s[28:29]
	v_fmac_f32_e32 v178, s25, v132
	v_fmac_f32_e32 v179, s25, v133
	v_fmac_f32_e32 v180, s25, v134
	v_fmac_f32_e32 v181, s25, v135
	v_fmac_f32_e32 v182, s25, v136
	v_fmac_f32_e32 v183, s25, v137
	v_fmac_f32_e32 v184, s25, v138
	v_fmac_f32_e32 v185, s25, v139
	s_waitcnt vmcnt(35)
	v_readlane_b32 s25, v247, 10
	v_cvt_f32_ubyte0_e32 v124, v44
	v_cvt_f32_ubyte1_e32 v125, v44
	v_cvt_f32_ubyte2_e32 v126, v44
	v_cvt_f32_ubyte3_e32 v127, v44
	v_cvt_f32_ubyte0_e32 v128, v45
	v_cvt_f32_ubyte1_e32 v129, v45
	v_cvt_f32_ubyte2_e32 v130, v45
	v_cvt_f32_ubyte3_e32 v131, v45
	s_lshl_b32 s30, s78, 12
	s_add_u32 s28, s26, s30
	s_addc_u32 s29, s27, 0
	global_load_dwordx2 v[44:45], v162, s[28:29]
	v_fmac_f32_e32 v178, s25, v124
	v_fmac_f32_e32 v179, s25, v125
	v_fmac_f32_e32 v180, s25, v126
	v_fmac_f32_e32 v181, s25, v127
	v_fmac_f32_e32 v182, s25, v128
	v_fmac_f32_e32 v183, s25, v129
	v_fmac_f32_e32 v184, s25, v130
	v_fmac_f32_e32 v185, s25, v131
	s_waitcnt vmcnt(35)
	v_readlane_b32 s25, v247, 11
	v_cvt_f32_ubyte0_e32 v132, v46
	v_cvt_f32_ubyte1_e32 v133, v46
	v_cvt_f32_ubyte2_e32 v134, v46
	v_cvt_f32_ubyte3_e32 v135, v46
	v_cvt_f32_ubyte0_e32 v136, v47
	v_cvt_f32_ubyte1_e32 v137, v47
	v_cvt_f32_ubyte2_e32 v138, v47
	v_cvt_f32_ubyte3_e32 v139, v47
	s_lshl_b32 s30, s79, 12
	s_add_u32 s28, s26, s30
	s_addc_u32 s29, s27, 0
	global_load_dwordx2 v[46:47], v162, s[28:29]
	v_fmac_f32_e32 v178, s25, v132
	v_fmac_f32_e32 v179, s25, v133
	v_fmac_f32_e32 v180, s25, v134
	v_fmac_f32_e32 v181, s25, v135
	v_fmac_f32_e32 v182, s25, v136
	v_fmac_f32_e32 v183, s25, v137
	v_fmac_f32_e32 v184, s25, v138
	v_fmac_f32_e32 v185, s25, v139
	s_waitcnt vmcnt(35)
	v_readlane_b32 s25, v247, 12
	v_cvt_f32_ubyte0_e32 v124, v48
	v_cvt_f32_ubyte1_e32 v125, v48
	v_cvt_f32_ubyte2_e32 v126, v48
	v_cvt_f32_ubyte3_e32 v127, v48
	v_cvt_f32_ubyte0_e32 v128, v49
	v_cvt_f32_ubyte1_e32 v129, v49
	v_cvt_f32_ubyte2_e32 v130, v49
	v_cvt_f32_ubyte3_e32 v131, v49
	s_lshl_b32 s30, s80, 12
	s_add_u32 s28, s26, s30
	s_addc_u32 s29, s27, 0
	global_load_dwordx2 v[48:49], v162, s[28:29]
	v_fmac_f32_e32 v178, s25, v124
	v_fmac_f32_e32 v179, s25, v125
	v_fmac_f32_e32 v180, s25, v126
	v_fmac_f32_e32 v181, s25, v127
	v_fmac_f32_e32 v182, s25, v128
	v_fmac_f32_e32 v183, s25, v129
	v_fmac_f32_e32 v184, s25, v130
	v_fmac_f32_e32 v185, s25, v131
	s_waitcnt vmcnt(35)
	v_readlane_b32 s25, v247, 13
	v_cvt_f32_ubyte0_e32 v132, v50
	v_cvt_f32_ubyte1_e32 v133, v50
	v_cvt_f32_ubyte2_e32 v134, v50
	v_cvt_f32_ubyte3_e32 v135, v50
	v_cvt_f32_ubyte0_e32 v136, v51
	v_cvt_f32_ubyte1_e32 v137, v51
	v_cvt_f32_ubyte2_e32 v138, v51
	v_cvt_f32_ubyte3_e32 v139, v51
	s_lshl_b32 s30, s81, 12
	s_add_u32 s28, s26, s30
	s_addc_u32 s29, s27, 0
	global_load_dwordx2 v[50:51], v162, s[28:29]
	v_fmac_f32_e32 v178, s25, v132
	v_fmac_f32_e32 v179, s25, v133
	v_fmac_f32_e32 v180, s25, v134
	v_fmac_f32_e32 v181, s25, v135
	v_fmac_f32_e32 v182, s25, v136
	v_fmac_f32_e32 v183, s25, v137
	v_fmac_f32_e32 v184, s25, v138
	v_fmac_f32_e32 v185, s25, v139
	s_waitcnt vmcnt(35)
	v_readlane_b32 s25, v247, 14
	v_cvt_f32_ubyte0_e32 v124, v52
	v_cvt_f32_ubyte1_e32 v125, v52
	v_cvt_f32_ubyte2_e32 v126, v52
	v_cvt_f32_ubyte3_e32 v127, v52
	v_cvt_f32_ubyte0_e32 v128, v53
	v_cvt_f32_ubyte1_e32 v129, v53
	v_cvt_f32_ubyte2_e32 v130, v53
	v_cvt_f32_ubyte3_e32 v131, v53
	s_lshl_b32 s30, s82, 12
	s_add_u32 s28, s26, s30
	s_addc_u32 s29, s27, 0
	global_load_dwordx2 v[52:53], v162, s[28:29]
	v_fmac_f32_e32 v178, s25, v124
	v_fmac_f32_e32 v179, s25, v125
	v_fmac_f32_e32 v180, s25, v126
	v_fmac_f32_e32 v181, s25, v127
	v_fmac_f32_e32 v182, s25, v128
	v_fmac_f32_e32 v183, s25, v129
	v_fmac_f32_e32 v184, s25, v130
	v_fmac_f32_e32 v185, s25, v131
	s_waitcnt vmcnt(35)
	v_readlane_b32 s25, v247, 15
	v_cvt_f32_ubyte0_e32 v132, v54
	v_cvt_f32_ubyte1_e32 v133, v54
	v_cvt_f32_ubyte2_e32 v134, v54
	v_cvt_f32_ubyte3_e32 v135, v54
	v_cvt_f32_ubyte0_e32 v136, v55
	v_cvt_f32_ubyte1_e32 v137, v55
	v_cvt_f32_ubyte2_e32 v138, v55
	v_cvt_f32_ubyte3_e32 v139, v55
	s_lshl_b32 s30, s83, 12
	s_add_u32 s28, s26, s30
	s_addc_u32 s29, s27, 0
	global_load_dwordx2 v[54:55], v162, s[28:29]
	v_fmac_f32_e32 v178, s25, v132
	v_fmac_f32_e32 v179, s25, v133
	v_fmac_f32_e32 v180, s25, v134
	v_fmac_f32_e32 v181, s25, v135
	v_fmac_f32_e32 v182, s25, v136
	v_fmac_f32_e32 v183, s25, v137
	v_fmac_f32_e32 v184, s25, v138
	v_fmac_f32_e32 v185, s25, v139
	s_waitcnt vmcnt(35)
	v_readlane_b32 s25, v247, 16
	v_cvt_f32_ubyte0_e32 v124, v56
	v_cvt_f32_ubyte1_e32 v125, v56
	v_cvt_f32_ubyte2_e32 v126, v56
	v_cvt_f32_ubyte3_e32 v127, v56
	v_cvt_f32_ubyte0_e32 v128, v57
	v_cvt_f32_ubyte1_e32 v129, v57
	v_cvt_f32_ubyte2_e32 v130, v57
	v_cvt_f32_ubyte3_e32 v131, v57
	s_waitcnt lgkmcnt(0)
	s_load_dwordx16 s[68:83], s[38:39], 0x0
	s_lshl_b32 s30, s84, 12
	s_add_u32 s28, s26, s30
	s_addc_u32 s29, s27, 0
	global_load_dwordx2 v[56:57], v162, s[28:29]
	v_fmac_f32_e32 v178, s25, v124
	v_fmac_f32_e32 v179, s25, v125
	v_fmac_f32_e32 v180, s25, v126
	v_fmac_f32_e32 v181, s25, v127
	v_fmac_f32_e32 v182, s25, v128
	v_fmac_f32_e32 v183, s25, v129
	v_fmac_f32_e32 v184, s25, v130
	v_fmac_f32_e32 v185, s25, v131
	s_waitcnt vmcnt(35)
	v_readlane_b32 s25, v247, 17
	v_cvt_f32_ubyte0_e32 v132, v58
	v_cvt_f32_ubyte1_e32 v133, v58
	v_cvt_f32_ubyte2_e32 v134, v58
	v_cvt_f32_ubyte3_e32 v135, v58
	v_cvt_f32_ubyte0_e32 v136, v59
	v_cvt_f32_ubyte1_e32 v137, v59
	v_cvt_f32_ubyte2_e32 v138, v59
	v_cvt_f32_ubyte3_e32 v139, v59
	s_lshl_b32 s30, s85, 12
	s_add_u32 s28, s26, s30
	s_addc_u32 s29, s27, 0
	global_load_dwordx2 v[58:59], v162, s[28:29]
	v_fmac_f32_e32 v178, s25, v132
	v_fmac_f32_e32 v179, s25, v133
	v_fmac_f32_e32 v180, s25, v134
	v_fmac_f32_e32 v181, s25, v135
	v_fmac_f32_e32 v182, s25, v136
	v_fmac_f32_e32 v183, s25, v137
	v_fmac_f32_e32 v184, s25, v138
	v_fmac_f32_e32 v185, s25, v139
	s_waitcnt vmcnt(35)
	v_readlane_b32 s25, v247, 18
	v_cvt_f32_ubyte0_e32 v124, v60
	v_cvt_f32_ubyte1_e32 v125, v60
	v_cvt_f32_ubyte2_e32 v126, v60
	v_cvt_f32_ubyte3_e32 v127, v60
	v_cvt_f32_ubyte0_e32 v128, v61
	v_cvt_f32_ubyte1_e32 v129, v61
	v_cvt_f32_ubyte2_e32 v130, v61
	v_cvt_f32_ubyte3_e32 v131, v61
	s_lshl_b32 s30, s86, 12
	s_add_u32 s28, s26, s30
	s_addc_u32 s29, s27, 0
	global_load_dwordx2 v[60:61], v162, s[28:29]
	v_fmac_f32_e32 v178, s25, v124
	v_fmac_f32_e32 v179, s25, v125
	v_fmac_f32_e32 v180, s25, v126
	v_fmac_f32_e32 v181, s25, v127
	v_fmac_f32_e32 v182, s25, v128
	v_fmac_f32_e32 v183, s25, v129
	v_fmac_f32_e32 v184, s25, v130
	v_fmac_f32_e32 v185, s25, v131
	s_waitcnt vmcnt(35)
	v_readlane_b32 s25, v247, 19
	v_cvt_f32_ubyte0_e32 v132, v62
	v_cvt_f32_ubyte1_e32 v133, v62
	v_cvt_f32_ubyte2_e32 v134, v62
	v_cvt_f32_ubyte3_e32 v135, v62
	v_cvt_f32_ubyte0_e32 v136, v63
	v_cvt_f32_ubyte1_e32 v137, v63
	v_cvt_f32_ubyte2_e32 v138, v63
	v_cvt_f32_ubyte3_e32 v139, v63
	s_lshl_b32 s30, s87, 12
	s_add_u32 s28, s26, s30
	s_addc_u32 s29, s27, 0
	global_load_dwordx2 v[62:63], v162, s[28:29]
	v_fmac_f32_e32 v178, s25, v132
	v_fmac_f32_e32 v179, s25, v133
	v_fmac_f32_e32 v180, s25, v134
	v_fmac_f32_e32 v181, s25, v135
	v_fmac_f32_e32 v182, s25, v136
	v_fmac_f32_e32 v183, s25, v137
	v_fmac_f32_e32 v184, s25, v138
	v_fmac_f32_e32 v185, s25, v139
	s_waitcnt vmcnt(35)
	v_readlane_b32 s25, v247, 20
	v_cvt_f32_ubyte0_e32 v124, v64
	v_cvt_f32_ubyte1_e32 v125, v64
	v_cvt_f32_ubyte2_e32 v126, v64
	v_cvt_f32_ubyte3_e32 v127, v64
	v_cvt_f32_ubyte0_e32 v128, v65
	v_cvt_f32_ubyte1_e32 v129, v65
	v_cvt_f32_ubyte2_e32 v130, v65
	v_cvt_f32_ubyte3_e32 v131, v65
	s_lshl_b32 s30, s88, 12
	s_add_u32 s28, s26, s30
	s_addc_u32 s29, s27, 0
	global_load_dwordx2 v[64:65], v162, s[28:29]
	v_fmac_f32_e32 v178, s25, v124
	v_fmac_f32_e32 v179, s25, v125
	v_fmac_f32_e32 v180, s25, v126
	v_fmac_f32_e32 v181, s25, v127
	v_fmac_f32_e32 v182, s25, v128
	v_fmac_f32_e32 v183, s25, v129
	v_fmac_f32_e32 v184, s25, v130
	v_fmac_f32_e32 v185, s25, v131
	s_waitcnt vmcnt(35)
	v_readlane_b32 s25, v247, 21
	v_cvt_f32_ubyte0_e32 v132, v66
	v_cvt_f32_ubyte1_e32 v133, v66
	v_cvt_f32_ubyte2_e32 v134, v66
	v_cvt_f32_ubyte3_e32 v135, v66
	v_cvt_f32_ubyte0_e32 v136, v67
	v_cvt_f32_ubyte1_e32 v137, v67
	v_cvt_f32_ubyte2_e32 v138, v67
	v_cvt_f32_ubyte3_e32 v139, v67
	s_lshl_b32 s30, s89, 12
	s_add_u32 s28, s26, s30
	s_addc_u32 s29, s27, 0
	global_load_dwordx2 v[66:67], v162, s[28:29]
	v_fmac_f32_e32 v178, s25, v132
	v_fmac_f32_e32 v179, s25, v133
	v_fmac_f32_e32 v180, s25, v134
	v_fmac_f32_e32 v181, s25, v135
	v_fmac_f32_e32 v182, s25, v136
	v_fmac_f32_e32 v183, s25, v137
	v_fmac_f32_e32 v184, s25, v138
	v_fmac_f32_e32 v185, s25, v139
	s_waitcnt vmcnt(35)
	v_readlane_b32 s25, v247, 22
	v_cvt_f32_ubyte0_e32 v124, v68
	v_cvt_f32_ubyte1_e32 v125, v68
	v_cvt_f32_ubyte2_e32 v126, v68
	v_cvt_f32_ubyte3_e32 v127, v68
	v_cvt_f32_ubyte0_e32 v128, v69
	v_cvt_f32_ubyte1_e32 v129, v69
	v_cvt_f32_ubyte2_e32 v130, v69
	v_cvt_f32_ubyte3_e32 v131, v69
	s_lshl_b32 s30, s90, 12
	s_add_u32 s28, s26, s30
	s_addc_u32 s29, s27, 0
	global_load_dwordx2 v[68:69], v162, s[28:29]
	v_fmac_f32_e32 v178, s25, v124
	v_fmac_f32_e32 v179, s25, v125
	v_fmac_f32_e32 v180, s25, v126
	v_fmac_f32_e32 v181, s25, v127
	v_fmac_f32_e32 v182, s25, v128
	v_fmac_f32_e32 v183, s25, v129
	v_fmac_f32_e32 v184, s25, v130
	v_fmac_f32_e32 v185, s25, v131
	s_waitcnt vmcnt(35)
	v_readlane_b32 s25, v247, 23
	v_cvt_f32_ubyte0_e32 v132, v70
	v_cvt_f32_ubyte1_e32 v133, v70
	v_cvt_f32_ubyte2_e32 v134, v70
	v_cvt_f32_ubyte3_e32 v135, v70
	v_cvt_f32_ubyte0_e32 v136, v71
	v_cvt_f32_ubyte1_e32 v137, v71
	v_cvt_f32_ubyte2_e32 v138, v71
	v_cvt_f32_ubyte3_e32 v139, v71
	s_lshl_b32 s30, s91, 12
	s_add_u32 s28, s26, s30
	s_addc_u32 s29, s27, 0
	global_load_dwordx2 v[70:71], v162, s[28:29]
	v_fmac_f32_e32 v178, s25, v132
	v_fmac_f32_e32 v179, s25, v133
	v_fmac_f32_e32 v180, s25, v134
	v_fmac_f32_e32 v181, s25, v135
	v_fmac_f32_e32 v182, s25, v136
	v_fmac_f32_e32 v183, s25, v137
	v_fmac_f32_e32 v184, s25, v138
	v_fmac_f32_e32 v185, s25, v139
	s_waitcnt vmcnt(35)
	v_readlane_b32 s25, v247, 24
	v_cvt_f32_ubyte0_e32 v124, v72
	v_cvt_f32_ubyte1_e32 v125, v72
	v_cvt_f32_ubyte2_e32 v126, v72
	v_cvt_f32_ubyte3_e32 v127, v72
	v_cvt_f32_ubyte0_e32 v128, v73
	v_cvt_f32_ubyte1_e32 v129, v73
	v_cvt_f32_ubyte2_e32 v130, v73
	v_cvt_f32_ubyte3_e32 v131, v73
	s_lshl_b32 s30, s92, 12
	s_add_u32 s28, s26, s30
	s_addc_u32 s29, s27, 0
	global_load_dwordx2 v[72:73], v162, s[28:29]
	v_fmac_f32_e32 v178, s25, v124
	v_fmac_f32_e32 v179, s25, v125
	v_fmac_f32_e32 v180, s25, v126
	v_fmac_f32_e32 v181, s25, v127
	v_fmac_f32_e32 v182, s25, v128
	v_fmac_f32_e32 v183, s25, v129
	v_fmac_f32_e32 v184, s25, v130
	v_fmac_f32_e32 v185, s25, v131
	s_waitcnt vmcnt(35)
	v_readlane_b32 s25, v247, 25
	v_cvt_f32_ubyte0_e32 v132, v74
	v_cvt_f32_ubyte1_e32 v133, v74
	v_cvt_f32_ubyte2_e32 v134, v74
	v_cvt_f32_ubyte3_e32 v135, v74
	v_cvt_f32_ubyte0_e32 v136, v75
	v_cvt_f32_ubyte1_e32 v137, v75
	v_cvt_f32_ubyte2_e32 v138, v75
	v_cvt_f32_ubyte3_e32 v139, v75
	s_lshl_b32 s30, s93, 12
	s_add_u32 s28, s26, s30
	s_addc_u32 s29, s27, 0
	global_load_dwordx2 v[74:75], v162, s[28:29]
	v_fmac_f32_e32 v178, s25, v132
	v_fmac_f32_e32 v179, s25, v133
	v_fmac_f32_e32 v180, s25, v134
	v_fmac_f32_e32 v181, s25, v135
	v_fmac_f32_e32 v182, s25, v136
	v_fmac_f32_e32 v183, s25, v137
	v_fmac_f32_e32 v184, s25, v138
	v_fmac_f32_e32 v185, s25, v139
	s_waitcnt vmcnt(35)
	v_readlane_b32 s25, v247, 26
	v_cvt_f32_ubyte0_e32 v124, v76
	v_cvt_f32_ubyte1_e32 v125, v76
	v_cvt_f32_ubyte2_e32 v126, v76
	v_cvt_f32_ubyte3_e32 v127, v76
	v_cvt_f32_ubyte0_e32 v128, v77
	v_cvt_f32_ubyte1_e32 v129, v77
	v_cvt_f32_ubyte2_e32 v130, v77
	v_cvt_f32_ubyte3_e32 v131, v77
	s_lshl_b32 s30, s94, 12
	s_add_u32 s28, s26, s30
	s_addc_u32 s29, s27, 0
	global_load_dwordx2 v[76:77], v162, s[28:29]
	v_fmac_f32_e32 v178, s25, v124
	v_fmac_f32_e32 v179, s25, v125
	v_fmac_f32_e32 v180, s25, v126
	v_fmac_f32_e32 v181, s25, v127
	v_fmac_f32_e32 v182, s25, v128
	v_fmac_f32_e32 v183, s25, v129
	v_fmac_f32_e32 v184, s25, v130
	v_fmac_f32_e32 v185, s25, v131
	s_waitcnt vmcnt(35)
	v_readlane_b32 s25, v247, 27
	v_cvt_f32_ubyte0_e32 v132, v78
	v_cvt_f32_ubyte1_e32 v133, v78
	v_cvt_f32_ubyte2_e32 v134, v78
	v_cvt_f32_ubyte3_e32 v135, v78
	v_cvt_f32_ubyte0_e32 v136, v79
	v_cvt_f32_ubyte1_e32 v137, v79
	v_cvt_f32_ubyte2_e32 v138, v79
	v_cvt_f32_ubyte3_e32 v139, v79
	s_lshl_b32 s30, s95, 12
	s_add_u32 s28, s26, s30
	s_addc_u32 s29, s27, 0
	global_load_dwordx2 v[78:79], v162, s[28:29]
	v_fmac_f32_e32 v178, s25, v132
	v_fmac_f32_e32 v179, s25, v133
	v_fmac_f32_e32 v180, s25, v134
	v_fmac_f32_e32 v181, s25, v135
	v_fmac_f32_e32 v182, s25, v136
	v_fmac_f32_e32 v183, s25, v137
	v_fmac_f32_e32 v184, s25, v138
	v_fmac_f32_e32 v185, s25, v139
	s_waitcnt vmcnt(35)
	v_readlane_b32 s25, v247, 28
	v_cvt_f32_ubyte0_e32 v124, v80
	v_cvt_f32_ubyte1_e32 v125, v80
	v_cvt_f32_ubyte2_e32 v126, v80
	v_cvt_f32_ubyte3_e32 v127, v80
	v_cvt_f32_ubyte0_e32 v128, v81
	v_cvt_f32_ubyte1_e32 v129, v81
	v_cvt_f32_ubyte2_e32 v130, v81
	v_cvt_f32_ubyte3_e32 v131, v81
	s_lshl_b32 s30, s96, 12
	s_add_u32 s28, s26, s30
	s_addc_u32 s29, s27, 0
	global_load_dwordx2 v[80:81], v162, s[28:29]
	v_fmac_f32_e32 v178, s25, v124
	v_fmac_f32_e32 v179, s25, v125
	v_fmac_f32_e32 v180, s25, v126
	v_fmac_f32_e32 v181, s25, v127
	v_fmac_f32_e32 v182, s25, v128
	v_fmac_f32_e32 v183, s25, v129
	v_fmac_f32_e32 v184, s25, v130
	v_fmac_f32_e32 v185, s25, v131
	s_waitcnt vmcnt(35)
	v_readlane_b32 s25, v247, 29
	v_cvt_f32_ubyte0_e32 v132, v82
	v_cvt_f32_ubyte1_e32 v133, v82
	v_cvt_f32_ubyte2_e32 v134, v82
	v_cvt_f32_ubyte3_e32 v135, v82
	v_cvt_f32_ubyte0_e32 v136, v83
	v_cvt_f32_ubyte1_e32 v137, v83
	v_cvt_f32_ubyte2_e32 v138, v83
	v_cvt_f32_ubyte3_e32 v139, v83
	s_lshl_b32 s30, s97, 12
	s_add_u32 s28, s26, s30
	s_addc_u32 s29, s27, 0
	global_load_dwordx2 v[82:83], v162, s[28:29]
	v_fmac_f32_e32 v178, s25, v132
	v_fmac_f32_e32 v179, s25, v133
	v_fmac_f32_e32 v180, s25, v134
	v_fmac_f32_e32 v181, s25, v135
	v_fmac_f32_e32 v182, s25, v136
	v_fmac_f32_e32 v183, s25, v137
	v_fmac_f32_e32 v184, s25, v138
	v_fmac_f32_e32 v185, s25, v139
	s_waitcnt vmcnt(35)
	v_readlane_b32 s25, v247, 30
	v_cvt_f32_ubyte0_e32 v124, v84
	v_cvt_f32_ubyte1_e32 v125, v84
	v_cvt_f32_ubyte2_e32 v126, v84
	v_cvt_f32_ubyte3_e32 v127, v84
	v_cvt_f32_ubyte0_e32 v128, v85
	v_cvt_f32_ubyte1_e32 v129, v85
	v_cvt_f32_ubyte2_e32 v130, v85
	v_cvt_f32_ubyte3_e32 v131, v85
	s_lshl_b32 s30, s98, 12
	s_add_u32 s28, s26, s30
	s_addc_u32 s29, s27, 0
	global_load_dwordx2 v[84:85], v162, s[28:29]
	v_fmac_f32_e32 v178, s25, v124
	v_fmac_f32_e32 v179, s25, v125
	v_fmac_f32_e32 v180, s25, v126
	v_fmac_f32_e32 v181, s25, v127
	v_fmac_f32_e32 v182, s25, v128
	v_fmac_f32_e32 v183, s25, v129
	v_fmac_f32_e32 v184, s25, v130
	v_fmac_f32_e32 v185, s25, v131
	s_waitcnt vmcnt(35)
	v_readlane_b32 s25, v247, 31
	v_cvt_f32_ubyte0_e32 v132, v86
	v_cvt_f32_ubyte1_e32 v133, v86
	v_cvt_f32_ubyte2_e32 v134, v86
	v_cvt_f32_ubyte3_e32 v135, v86
	v_cvt_f32_ubyte0_e32 v136, v87
	v_cvt_f32_ubyte1_e32 v137, v87
	v_cvt_f32_ubyte2_e32 v138, v87
	v_cvt_f32_ubyte3_e32 v139, v87
	s_lshl_b32 s30, s99, 12
	s_add_u32 s28, s26, s30
	s_addc_u32 s29, s27, 0
	global_load_dwordx2 v[86:87], v162, s[28:29]
	v_fmac_f32_e32 v178, s25, v132
	v_fmac_f32_e32 v179, s25, v133
	v_fmac_f32_e32 v180, s25, v134
	v_fmac_f32_e32 v181, s25, v135
	v_fmac_f32_e32 v182, s25, v136
	v_fmac_f32_e32 v183, s25, v137
	v_fmac_f32_e32 v184, s25, v138
	v_fmac_f32_e32 v185, s25, v139
	s_waitcnt vmcnt(35)
	v_readlane_b32 s25, v247, 32
	v_cvt_f32_ubyte0_e32 v124, v24
	v_cvt_f32_ubyte1_e32 v125, v24
	v_cvt_f32_ubyte2_e32 v126, v24
	v_cvt_f32_ubyte3_e32 v127, v24
	v_cvt_f32_ubyte0_e32 v128, v25
	v_cvt_f32_ubyte1_e32 v129, v25
	v_cvt_f32_ubyte2_e32 v130, v25
	v_cvt_f32_ubyte3_e32 v131, v25
	v_fmac_f32_e32 v178, s25, v124
	v_fmac_f32_e32 v179, s25, v125
	v_fmac_f32_e32 v180, s25, v126
	v_fmac_f32_e32 v181, s25, v127
	v_fmac_f32_e32 v182, s25, v128
	v_fmac_f32_e32 v183, s25, v129
	v_fmac_f32_e32 v184, s25, v130
	v_fmac_f32_e32 v185, s25, v131
	s_waitcnt vmcnt(30)
	v_readlane_b32 s25, v247, 33
	v_cvt_f32_ubyte0_e32 v132, v26
	v_cvt_f32_ubyte1_e32 v133, v26
	v_cvt_f32_ubyte2_e32 v134, v26
	v_cvt_f32_ubyte3_e32 v135, v26
	v_cvt_f32_ubyte0_e32 v136, v27
	v_cvt_f32_ubyte1_e32 v137, v27
	v_cvt_f32_ubyte2_e32 v138, v27
	v_cvt_f32_ubyte3_e32 v139, v27
	v_fmac_f32_e32 v178, s25, v132
	v_fmac_f32_e32 v179, s25, v133
	v_fmac_f32_e32 v180, s25, v134
	v_fmac_f32_e32 v181, s25, v135
	v_fmac_f32_e32 v182, s25, v136
	v_fmac_f32_e32 v183, s25, v137
	v_fmac_f32_e32 v184, s25, v138
	v_fmac_f32_e32 v185, s25, v139
	s_waitcnt vmcnt(29)
	v_readlane_b32 s25, v247, 34
	v_cvt_f32_ubyte0_e32 v124, v28
	v_cvt_f32_ubyte1_e32 v125, v28
	v_cvt_f32_ubyte2_e32 v126, v28
	v_cvt_f32_ubyte3_e32 v127, v28
	v_cvt_f32_ubyte0_e32 v128, v29
	v_cvt_f32_ubyte1_e32 v129, v29
	v_cvt_f32_ubyte2_e32 v130, v29
	v_cvt_f32_ubyte3_e32 v131, v29
	v_fmac_f32_e32 v178, s25, v124
	v_fmac_f32_e32 v179, s25, v125
	v_fmac_f32_e32 v180, s25, v126
	v_fmac_f32_e32 v181, s25, v127
	v_fmac_f32_e32 v182, s25, v128
	v_fmac_f32_e32 v183, s25, v129
	v_fmac_f32_e32 v184, s25, v130
	v_fmac_f32_e32 v185, s25, v131
	s_waitcnt vmcnt(28)
	v_readlane_b32 s25, v247, 35
	v_cvt_f32_ubyte0_e32 v132, v30
	v_cvt_f32_ubyte1_e32 v133, v30
	v_cvt_f32_ubyte2_e32 v134, v30
	v_cvt_f32_ubyte3_e32 v135, v30
	v_cvt_f32_ubyte0_e32 v136, v31
	v_cvt_f32_ubyte1_e32 v137, v31
	v_cvt_f32_ubyte2_e32 v138, v31
	v_cvt_f32_ubyte3_e32 v139, v31
	v_fmac_f32_e32 v178, s25, v132
	v_fmac_f32_e32 v179, s25, v133
	v_fmac_f32_e32 v180, s25, v134
	v_fmac_f32_e32 v181, s25, v135
	v_fmac_f32_e32 v182, s25, v136
	v_fmac_f32_e32 v183, s25, v137
	v_fmac_f32_e32 v184, s25, v138
	v_fmac_f32_e32 v185, s25, v139
	s_waitcnt vmcnt(27)
	v_readlane_b32 s25, v247, 36
	v_cvt_f32_ubyte0_e32 v124, v32
	v_cvt_f32_ubyte1_e32 v125, v32
	v_cvt_f32_ubyte2_e32 v126, v32
	v_cvt_f32_ubyte3_e32 v127, v32
	v_cvt_f32_ubyte0_e32 v128, v33
	v_cvt_f32_ubyte1_e32 v129, v33
	v_cvt_f32_ubyte2_e32 v130, v33
	v_cvt_f32_ubyte3_e32 v131, v33
	v_fmac_f32_e32 v178, s25, v124
	v_fmac_f32_e32 v179, s25, v125
	v_fmac_f32_e32 v180, s25, v126
	v_fmac_f32_e32 v181, s25, v127
	v_fmac_f32_e32 v182, s25, v128
	v_fmac_f32_e32 v183, s25, v129
	v_fmac_f32_e32 v184, s25, v130
	v_fmac_f32_e32 v185, s25, v131
	s_waitcnt vmcnt(26)
	v_readlane_b32 s25, v247, 37
	v_cvt_f32_ubyte0_e32 v132, v34
	v_cvt_f32_ubyte1_e32 v133, v34
	v_cvt_f32_ubyte2_e32 v134, v34
	v_cvt_f32_ubyte3_e32 v135, v34
	v_cvt_f32_ubyte0_e32 v136, v35
	v_cvt_f32_ubyte1_e32 v137, v35
	v_cvt_f32_ubyte2_e32 v138, v35
	v_cvt_f32_ubyte3_e32 v139, v35
	v_fmac_f32_e32 v178, s25, v132
	v_fmac_f32_e32 v179, s25, v133
	v_fmac_f32_e32 v180, s25, v134
	v_fmac_f32_e32 v181, s25, v135
	v_fmac_f32_e32 v182, s25, v136
	v_fmac_f32_e32 v183, s25, v137
	v_fmac_f32_e32 v184, s25, v138
	v_fmac_f32_e32 v185, s25, v139
	s_waitcnt vmcnt(25)
	v_readlane_b32 s25, v247, 38
	v_cvt_f32_ubyte0_e32 v124, v36
	v_cvt_f32_ubyte1_e32 v125, v36
	v_cvt_f32_ubyte2_e32 v126, v36
	v_cvt_f32_ubyte3_e32 v127, v36
	v_cvt_f32_ubyte0_e32 v128, v37
	v_cvt_f32_ubyte1_e32 v129, v37
	v_cvt_f32_ubyte2_e32 v130, v37
	v_cvt_f32_ubyte3_e32 v131, v37
	v_fmac_f32_e32 v178, s25, v124
	v_fmac_f32_e32 v179, s25, v125
	v_fmac_f32_e32 v180, s25, v126
	v_fmac_f32_e32 v181, s25, v127
	v_fmac_f32_e32 v182, s25, v128
	v_fmac_f32_e32 v183, s25, v129
	v_fmac_f32_e32 v184, s25, v130
	v_fmac_f32_e32 v185, s25, v131
	s_waitcnt vmcnt(24)
	v_readlane_b32 s25, v247, 39
	v_cvt_f32_ubyte0_e32 v132, v38
	v_cvt_f32_ubyte1_e32 v133, v38
	v_cvt_f32_ubyte2_e32 v134, v38
	v_cvt_f32_ubyte3_e32 v135, v38
	v_cvt_f32_ubyte0_e32 v136, v39
	v_cvt_f32_ubyte1_e32 v137, v39
	v_cvt_f32_ubyte2_e32 v138, v39
	v_cvt_f32_ubyte3_e32 v139, v39
	v_fmac_f32_e32 v178, s25, v132
	v_fmac_f32_e32 v179, s25, v133
	v_fmac_f32_e32 v180, s25, v134
	v_fmac_f32_e32 v181, s25, v135
	v_fmac_f32_e32 v182, s25, v136
	v_fmac_f32_e32 v183, s25, v137
	v_fmac_f32_e32 v184, s25, v138
	v_fmac_f32_e32 v185, s25, v139
	s_waitcnt vmcnt(23)
	v_readlane_b32 s25, v247, 40
	v_cvt_f32_ubyte0_e32 v124, v40
	v_cvt_f32_ubyte1_e32 v125, v40
	v_cvt_f32_ubyte2_e32 v126, v40
	v_cvt_f32_ubyte3_e32 v127, v40
	v_cvt_f32_ubyte0_e32 v128, v41
	v_cvt_f32_ubyte1_e32 v129, v41
	v_cvt_f32_ubyte2_e32 v130, v41
	v_cvt_f32_ubyte3_e32 v131, v41
	v_fmac_f32_e32 v178, s25, v124
	v_fmac_f32_e32 v179, s25, v125
	v_fmac_f32_e32 v180, s25, v126
	v_fmac_f32_e32 v181, s25, v127
	v_fmac_f32_e32 v182, s25, v128
	v_fmac_f32_e32 v183, s25, v129
	v_fmac_f32_e32 v184, s25, v130
	v_fmac_f32_e32 v185, s25, v131
	s_waitcnt vmcnt(22)
	v_readlane_b32 s25, v247, 41
	v_cvt_f32_ubyte0_e32 v132, v42
	v_cvt_f32_ubyte1_e32 v133, v42
	v_cvt_f32_ubyte2_e32 v134, v42
	v_cvt_f32_ubyte3_e32 v135, v42
	v_cvt_f32_ubyte0_e32 v136, v43
	v_cvt_f32_ubyte1_e32 v137, v43
	v_cvt_f32_ubyte2_e32 v138, v43
	v_cvt_f32_ubyte3_e32 v139, v43
	v_fmac_f32_e32 v178, s25, v132
	v_fmac_f32_e32 v179, s25, v133
	v_fmac_f32_e32 v180, s25, v134
	v_fmac_f32_e32 v181, s25, v135
	v_fmac_f32_e32 v182, s25, v136
	v_fmac_f32_e32 v183, s25, v137
	v_fmac_f32_e32 v184, s25, v138
	v_fmac_f32_e32 v185, s25, v139
	s_waitcnt vmcnt(21)
	v_readlane_b32 s25, v247, 42
	v_cvt_f32_ubyte0_e32 v124, v44
	v_cvt_f32_ubyte1_e32 v125, v44
	v_cvt_f32_ubyte2_e32 v126, v44
	v_cvt_f32_ubyte3_e32 v127, v44
	v_cvt_f32_ubyte0_e32 v128, v45
	v_cvt_f32_ubyte1_e32 v129, v45
	v_cvt_f32_ubyte2_e32 v130, v45
	v_cvt_f32_ubyte3_e32 v131, v45
	v_fmac_f32_e32 v178, s25, v124
	v_fmac_f32_e32 v179, s25, v125
	v_fmac_f32_e32 v180, s25, v126
	v_fmac_f32_e32 v181, s25, v127
	v_fmac_f32_e32 v182, s25, v128
	v_fmac_f32_e32 v183, s25, v129
	v_fmac_f32_e32 v184, s25, v130
	v_fmac_f32_e32 v185, s25, v131
	s_waitcnt vmcnt(20)
	v_readlane_b32 s25, v247, 43
	v_cvt_f32_ubyte0_e32 v132, v46
	v_cvt_f32_ubyte1_e32 v133, v46
	v_cvt_f32_ubyte2_e32 v134, v46
	v_cvt_f32_ubyte3_e32 v135, v46
	v_cvt_f32_ubyte0_e32 v136, v47
	v_cvt_f32_ubyte1_e32 v137, v47
	v_cvt_f32_ubyte2_e32 v138, v47
	v_cvt_f32_ubyte3_e32 v139, v47
	v_fmac_f32_e32 v178, s25, v132
	v_fmac_f32_e32 v179, s25, v133
	v_fmac_f32_e32 v180, s25, v134
	v_fmac_f32_e32 v181, s25, v135
	v_fmac_f32_e32 v182, s25, v136
	v_fmac_f32_e32 v183, s25, v137
	v_fmac_f32_e32 v184, s25, v138
	v_fmac_f32_e32 v185, s25, v139
	s_waitcnt vmcnt(19)
	v_readlane_b32 s25, v247, 44
	v_cvt_f32_ubyte0_e32 v124, v48
	v_cvt_f32_ubyte1_e32 v125, v48
	v_cvt_f32_ubyte2_e32 v126, v48
	v_cvt_f32_ubyte3_e32 v127, v48
	v_cvt_f32_ubyte0_e32 v128, v49
	v_cvt_f32_ubyte1_e32 v129, v49
	v_cvt_f32_ubyte2_e32 v130, v49
	v_cvt_f32_ubyte3_e32 v131, v49
	v_fmac_f32_e32 v178, s25, v124
	v_fmac_f32_e32 v179, s25, v125
	v_fmac_f32_e32 v180, s25, v126
	v_fmac_f32_e32 v181, s25, v127
	v_fmac_f32_e32 v182, s25, v128
	v_fmac_f32_e32 v183, s25, v129
	v_fmac_f32_e32 v184, s25, v130
	v_fmac_f32_e32 v185, s25, v131
	s_waitcnt vmcnt(18)
	v_readlane_b32 s25, v247, 45
	v_cvt_f32_ubyte0_e32 v132, v50
	v_cvt_f32_ubyte1_e32 v133, v50
	v_cvt_f32_ubyte2_e32 v134, v50
	v_cvt_f32_ubyte3_e32 v135, v50
	v_cvt_f32_ubyte0_e32 v136, v51
	v_cvt_f32_ubyte1_e32 v137, v51
	v_cvt_f32_ubyte2_e32 v138, v51
	v_cvt_f32_ubyte3_e32 v139, v51
	v_fmac_f32_e32 v178, s25, v132
	v_fmac_f32_e32 v179, s25, v133
	v_fmac_f32_e32 v180, s25, v134
	v_fmac_f32_e32 v181, s25, v135
	v_fmac_f32_e32 v182, s25, v136
	v_fmac_f32_e32 v183, s25, v137
	v_fmac_f32_e32 v184, s25, v138
	v_fmac_f32_e32 v185, s25, v139
	s_waitcnt vmcnt(17)
	v_readlane_b32 s25, v247, 46
	v_cvt_f32_ubyte0_e32 v124, v52
	v_cvt_f32_ubyte1_e32 v125, v52
	v_cvt_f32_ubyte2_e32 v126, v52
	v_cvt_f32_ubyte3_e32 v127, v52
	v_cvt_f32_ubyte0_e32 v128, v53
	v_cvt_f32_ubyte1_e32 v129, v53
	v_cvt_f32_ubyte2_e32 v130, v53
	v_cvt_f32_ubyte3_e32 v131, v53
	v_fmac_f32_e32 v178, s25, v124
	v_fmac_f32_e32 v179, s25, v125
	v_fmac_f32_e32 v180, s25, v126
	v_fmac_f32_e32 v181, s25, v127
	v_fmac_f32_e32 v182, s25, v128
	v_fmac_f32_e32 v183, s25, v129
	v_fmac_f32_e32 v184, s25, v130
	v_fmac_f32_e32 v185, s25, v131
	s_waitcnt vmcnt(16)
	v_readlane_b32 s25, v247, 47
	v_cvt_f32_ubyte0_e32 v132, v54
	v_cvt_f32_ubyte1_e32 v133, v54
	v_cvt_f32_ubyte2_e32 v134, v54
	v_cvt_f32_ubyte3_e32 v135, v54
	v_cvt_f32_ubyte0_e32 v136, v55
	v_cvt_f32_ubyte1_e32 v137, v55
	v_cvt_f32_ubyte2_e32 v138, v55
	v_cvt_f32_ubyte3_e32 v139, v55
	v_fmac_f32_e32 v178, s25, v132
	v_fmac_f32_e32 v179, s25, v133
	v_fmac_f32_e32 v180, s25, v134
	v_fmac_f32_e32 v181, s25, v135
	v_fmac_f32_e32 v182, s25, v136
	v_fmac_f32_e32 v183, s25, v137
	v_fmac_f32_e32 v184, s25, v138
	v_fmac_f32_e32 v185, s25, v139
	s_waitcnt vmcnt(15)
	v_readlane_b32 s25, v247, 48
	v_cvt_f32_ubyte0_e32 v124, v56
	v_cvt_f32_ubyte1_e32 v125, v56
	v_cvt_f32_ubyte2_e32 v126, v56
	v_cvt_f32_ubyte3_e32 v127, v56
	v_cvt_f32_ubyte0_e32 v128, v57
	v_cvt_f32_ubyte1_e32 v129, v57
	v_cvt_f32_ubyte2_e32 v130, v57
	v_cvt_f32_ubyte3_e32 v131, v57
	v_fmac_f32_e32 v178, s25, v124
	v_fmac_f32_e32 v179, s25, v125
	v_fmac_f32_e32 v180, s25, v126
	v_fmac_f32_e32 v181, s25, v127
	v_fmac_f32_e32 v182, s25, v128
	v_fmac_f32_e32 v183, s25, v129
	v_fmac_f32_e32 v184, s25, v130
	v_fmac_f32_e32 v185, s25, v131
	s_waitcnt vmcnt(14)
	v_readlane_b32 s25, v247, 49
	v_cvt_f32_ubyte0_e32 v132, v58
	v_cvt_f32_ubyte1_e32 v133, v58
	v_cvt_f32_ubyte2_e32 v134, v58
	v_cvt_f32_ubyte3_e32 v135, v58
	v_cvt_f32_ubyte0_e32 v136, v59
	v_cvt_f32_ubyte1_e32 v137, v59
	v_cvt_f32_ubyte2_e32 v138, v59
	v_cvt_f32_ubyte3_e32 v139, v59
	v_fmac_f32_e32 v178, s25, v132
	v_fmac_f32_e32 v179, s25, v133
	v_fmac_f32_e32 v180, s25, v134
	v_fmac_f32_e32 v181, s25, v135
	v_fmac_f32_e32 v182, s25, v136
	v_fmac_f32_e32 v183, s25, v137
	v_fmac_f32_e32 v184, s25, v138
	v_fmac_f32_e32 v185, s25, v139
	s_waitcnt vmcnt(13)
	v_readlane_b32 s25, v247, 50
	v_cvt_f32_ubyte0_e32 v124, v60
	v_cvt_f32_ubyte1_e32 v125, v60
	v_cvt_f32_ubyte2_e32 v126, v60
	v_cvt_f32_ubyte3_e32 v127, v60
	v_cvt_f32_ubyte0_e32 v128, v61
	v_cvt_f32_ubyte1_e32 v129, v61
	v_cvt_f32_ubyte2_e32 v130, v61
	v_cvt_f32_ubyte3_e32 v131, v61
	v_fmac_f32_e32 v178, s25, v124
	v_fmac_f32_e32 v179, s25, v125
	v_fmac_f32_e32 v180, s25, v126
	v_fmac_f32_e32 v181, s25, v127
	v_fmac_f32_e32 v182, s25, v128
	v_fmac_f32_e32 v183, s25, v129
	v_fmac_f32_e32 v184, s25, v130
	v_fmac_f32_e32 v185, s25, v131
	s_waitcnt vmcnt(12)
	v_readlane_b32 s25, v247, 51
	v_cvt_f32_ubyte0_e32 v132, v62
	v_cvt_f32_ubyte1_e32 v133, v62
	v_cvt_f32_ubyte2_e32 v134, v62
	v_cvt_f32_ubyte3_e32 v135, v62
	v_cvt_f32_ubyte0_e32 v136, v63
	v_cvt_f32_ubyte1_e32 v137, v63
	v_cvt_f32_ubyte2_e32 v138, v63
	v_cvt_f32_ubyte3_e32 v139, v63
	v_fmac_f32_e32 v178, s25, v132
	v_fmac_f32_e32 v179, s25, v133
	v_fmac_f32_e32 v180, s25, v134
	v_fmac_f32_e32 v181, s25, v135
	v_fmac_f32_e32 v182, s25, v136
	v_fmac_f32_e32 v183, s25, v137
	v_fmac_f32_e32 v184, s25, v138
	v_fmac_f32_e32 v185, s25, v139
	s_waitcnt vmcnt(11)
	v_readlane_b32 s25, v247, 52
	v_cvt_f32_ubyte0_e32 v124, v64
	v_cvt_f32_ubyte1_e32 v125, v64
	v_cvt_f32_ubyte2_e32 v126, v64
	v_cvt_f32_ubyte3_e32 v127, v64
	v_cvt_f32_ubyte0_e32 v128, v65
	v_cvt_f32_ubyte1_e32 v129, v65
	v_cvt_f32_ubyte2_e32 v130, v65
	v_cvt_f32_ubyte3_e32 v131, v65
	v_fmac_f32_e32 v178, s25, v124
	v_fmac_f32_e32 v179, s25, v125
	v_fmac_f32_e32 v180, s25, v126
	v_fmac_f32_e32 v181, s25, v127
	v_fmac_f32_e32 v182, s25, v128
	v_fmac_f32_e32 v183, s25, v129
	v_fmac_f32_e32 v184, s25, v130
	v_fmac_f32_e32 v185, s25, v131
	s_waitcnt vmcnt(10)
	v_readlane_b32 s25, v247, 53
	v_cvt_f32_ubyte0_e32 v132, v66
	v_cvt_f32_ubyte1_e32 v133, v66
	v_cvt_f32_ubyte2_e32 v134, v66
	v_cvt_f32_ubyte3_e32 v135, v66
	v_cvt_f32_ubyte0_e32 v136, v67
	v_cvt_f32_ubyte1_e32 v137, v67
	v_cvt_f32_ubyte2_e32 v138, v67
	v_cvt_f32_ubyte3_e32 v139, v67
	v_fmac_f32_e32 v178, s25, v132
	v_fmac_f32_e32 v179, s25, v133
	v_fmac_f32_e32 v180, s25, v134
	v_fmac_f32_e32 v181, s25, v135
	v_fmac_f32_e32 v182, s25, v136
	v_fmac_f32_e32 v183, s25, v137
	v_fmac_f32_e32 v184, s25, v138
	v_fmac_f32_e32 v185, s25, v139
	s_waitcnt vmcnt(9)
	v_readlane_b32 s25, v247, 54
	v_cvt_f32_ubyte0_e32 v124, v68
	v_cvt_f32_ubyte1_e32 v125, v68
	v_cvt_f32_ubyte2_e32 v126, v68
	v_cvt_f32_ubyte3_e32 v127, v68
	v_cvt_f32_ubyte0_e32 v128, v69
	v_cvt_f32_ubyte1_e32 v129, v69
	v_cvt_f32_ubyte2_e32 v130, v69
	v_cvt_f32_ubyte3_e32 v131, v69
	v_fmac_f32_e32 v178, s25, v124
	v_fmac_f32_e32 v179, s25, v125
	v_fmac_f32_e32 v180, s25, v126
	v_fmac_f32_e32 v181, s25, v127
	v_fmac_f32_e32 v182, s25, v128
	v_fmac_f32_e32 v183, s25, v129
	v_fmac_f32_e32 v184, s25, v130
	v_fmac_f32_e32 v185, s25, v131
	s_waitcnt vmcnt(8)
	v_readlane_b32 s25, v247, 55
	v_cvt_f32_ubyte0_e32 v132, v70
	v_cvt_f32_ubyte1_e32 v133, v70
	v_cvt_f32_ubyte2_e32 v134, v70
	v_cvt_f32_ubyte3_e32 v135, v70
	v_cvt_f32_ubyte0_e32 v136, v71
	v_cvt_f32_ubyte1_e32 v137, v71
	v_cvt_f32_ubyte2_e32 v138, v71
	v_cvt_f32_ubyte3_e32 v139, v71
	v_fmac_f32_e32 v178, s25, v132
	v_fmac_f32_e32 v179, s25, v133
	v_fmac_f32_e32 v180, s25, v134
	v_fmac_f32_e32 v181, s25, v135
	v_fmac_f32_e32 v182, s25, v136
	v_fmac_f32_e32 v183, s25, v137
	v_fmac_f32_e32 v184, s25, v138
	v_fmac_f32_e32 v185, s25, v139
	s_waitcnt vmcnt(7)
	v_readlane_b32 s25, v247, 56
	v_cvt_f32_ubyte0_e32 v124, v72
	v_cvt_f32_ubyte1_e32 v125, v72
	v_cvt_f32_ubyte2_e32 v126, v72
	v_cvt_f32_ubyte3_e32 v127, v72
	v_cvt_f32_ubyte0_e32 v128, v73
	v_cvt_f32_ubyte1_e32 v129, v73
	v_cvt_f32_ubyte2_e32 v130, v73
	v_cvt_f32_ubyte3_e32 v131, v73
	v_fmac_f32_e32 v178, s25, v124
	v_fmac_f32_e32 v179, s25, v125
	v_fmac_f32_e32 v180, s25, v126
	v_fmac_f32_e32 v181, s25, v127
	v_fmac_f32_e32 v182, s25, v128
	v_fmac_f32_e32 v183, s25, v129
	v_fmac_f32_e32 v184, s25, v130
	v_fmac_f32_e32 v185, s25, v131
	s_waitcnt vmcnt(6)
	v_readlane_b32 s25, v247, 57
	v_cvt_f32_ubyte0_e32 v132, v74
	v_cvt_f32_ubyte1_e32 v133, v74
	v_cvt_f32_ubyte2_e32 v134, v74
	v_cvt_f32_ubyte3_e32 v135, v74
	v_cvt_f32_ubyte0_e32 v136, v75
	v_cvt_f32_ubyte1_e32 v137, v75
	v_cvt_f32_ubyte2_e32 v138, v75
	v_cvt_f32_ubyte3_e32 v139, v75
	v_fmac_f32_e32 v178, s25, v132
	v_fmac_f32_e32 v179, s25, v133
	v_fmac_f32_e32 v180, s25, v134
	v_fmac_f32_e32 v181, s25, v135
	v_fmac_f32_e32 v182, s25, v136
	v_fmac_f32_e32 v183, s25, v137
	v_fmac_f32_e32 v184, s25, v138
	v_fmac_f32_e32 v185, s25, v139
	s_waitcnt vmcnt(5)
	v_readlane_b32 s25, v247, 58
	v_cvt_f32_ubyte0_e32 v124, v76
	v_cvt_f32_ubyte1_e32 v125, v76
	v_cvt_f32_ubyte2_e32 v126, v76
	v_cvt_f32_ubyte3_e32 v127, v76
	v_cvt_f32_ubyte0_e32 v128, v77
	v_cvt_f32_ubyte1_e32 v129, v77
	v_cvt_f32_ubyte2_e32 v130, v77
	v_cvt_f32_ubyte3_e32 v131, v77
	v_fmac_f32_e32 v178, s25, v124
	v_fmac_f32_e32 v179, s25, v125
	v_fmac_f32_e32 v180, s25, v126
	v_fmac_f32_e32 v181, s25, v127
	v_fmac_f32_e32 v182, s25, v128
	v_fmac_f32_e32 v183, s25, v129
	v_fmac_f32_e32 v184, s25, v130
	v_fmac_f32_e32 v185, s25, v131
	s_waitcnt vmcnt(4)
	v_readlane_b32 s25, v247, 59
	v_cvt_f32_ubyte0_e32 v132, v78
	v_cvt_f32_ubyte1_e32 v133, v78
	v_cvt_f32_ubyte2_e32 v134, v78
	v_cvt_f32_ubyte3_e32 v135, v78
	v_cvt_f32_ubyte0_e32 v136, v79
	v_cvt_f32_ubyte1_e32 v137, v79
	v_cvt_f32_ubyte2_e32 v138, v79
	v_cvt_f32_ubyte3_e32 v139, v79
	v_fmac_f32_e32 v178, s25, v132
	v_fmac_f32_e32 v179, s25, v133
	v_fmac_f32_e32 v180, s25, v134
	v_fmac_f32_e32 v181, s25, v135
	v_fmac_f32_e32 v182, s25, v136
	v_fmac_f32_e32 v183, s25, v137
	v_fmac_f32_e32 v184, s25, v138
	v_fmac_f32_e32 v185, s25, v139
	s_waitcnt vmcnt(3)
	v_readlane_b32 s25, v247, 60
	v_cvt_f32_ubyte0_e32 v124, v80
	v_cvt_f32_ubyte1_e32 v125, v80
	v_cvt_f32_ubyte2_e32 v126, v80
	v_cvt_f32_ubyte3_e32 v127, v80
	v_cvt_f32_ubyte0_e32 v128, v81
	v_cvt_f32_ubyte1_e32 v129, v81
	v_cvt_f32_ubyte2_e32 v130, v81
	v_cvt_f32_ubyte3_e32 v131, v81
	v_fmac_f32_e32 v178, s25, v124
	v_fmac_f32_e32 v179, s25, v125
	v_fmac_f32_e32 v180, s25, v126
	v_fmac_f32_e32 v181, s25, v127
	v_fmac_f32_e32 v182, s25, v128
	v_fmac_f32_e32 v183, s25, v129
	v_fmac_f32_e32 v184, s25, v130
	v_fmac_f32_e32 v185, s25, v131
	s_waitcnt vmcnt(2)
	v_readlane_b32 s25, v247, 61
	v_cvt_f32_ubyte0_e32 v132, v82
	v_cvt_f32_ubyte1_e32 v133, v82
	v_cvt_f32_ubyte2_e32 v134, v82
	v_cvt_f32_ubyte3_e32 v135, v82
	v_cvt_f32_ubyte0_e32 v136, v83
	v_cvt_f32_ubyte1_e32 v137, v83
	v_cvt_f32_ubyte2_e32 v138, v83
	v_cvt_f32_ubyte3_e32 v139, v83
	v_fmac_f32_e32 v178, s25, v132
	v_fmac_f32_e32 v179, s25, v133
	v_fmac_f32_e32 v180, s25, v134
	v_fmac_f32_e32 v181, s25, v135
	v_fmac_f32_e32 v182, s25, v136
	v_fmac_f32_e32 v183, s25, v137
	v_fmac_f32_e32 v184, s25, v138
	v_fmac_f32_e32 v185, s25, v139
	s_waitcnt vmcnt(1)
	v_readlane_b32 s25, v247, 62
	v_cvt_f32_ubyte0_e32 v124, v84
	v_cvt_f32_ubyte1_e32 v125, v84
	v_cvt_f32_ubyte2_e32 v126, v84
	v_cvt_f32_ubyte3_e32 v127, v84
	v_cvt_f32_ubyte0_e32 v128, v85
	v_cvt_f32_ubyte1_e32 v129, v85
	v_cvt_f32_ubyte2_e32 v130, v85
	v_cvt_f32_ubyte3_e32 v131, v85
	v_fmac_f32_e32 v178, s25, v124
	v_fmac_f32_e32 v179, s25, v125
	v_fmac_f32_e32 v180, s25, v126
	v_fmac_f32_e32 v181, s25, v127
	v_fmac_f32_e32 v182, s25, v128
	v_fmac_f32_e32 v183, s25, v129
	v_fmac_f32_e32 v184, s25, v130
	v_fmac_f32_e32 v185, s25, v131
	s_waitcnt vmcnt(0)
	v_readlane_b32 s25, v247, 63
	v_cvt_f32_ubyte0_e32 v132, v86
	v_cvt_f32_ubyte1_e32 v133, v86
	v_cvt_f32_ubyte2_e32 v134, v86
	v_cvt_f32_ubyte3_e32 v135, v86
	v_cvt_f32_ubyte0_e32 v136, v87
	v_cvt_f32_ubyte1_e32 v137, v87
	v_cvt_f32_ubyte2_e32 v138, v87
	v_cvt_f32_ubyte3_e32 v139, v87
	v_fmac_f32_e32 v178, s25, v132
	v_fmac_f32_e32 v179, s25, v133
	v_fmac_f32_e32 v180, s25, v134
	v_fmac_f32_e32 v181, s25, v135
	v_fmac_f32_e32 v182, s25, v136
	v_fmac_f32_e32 v183, s25, v137
	v_fmac_f32_e32 v184, s25, v138
	v_fmac_f32_e32 v185, s25, v139
	v_lshlrev_b32_e32 v132, 16, v242
	v_and_b32_e32 v133, 0xffff0000, v242
	v_lshlrev_b32_e32 v134, 16, v243
	v_and_b32_e32 v135, 0xffff0000, v243
	v_lshlrev_b32_e32 v136, 16, v244
	v_and_b32_e32 v137, 0xffff0000, v244
	v_lshlrev_b32_e32 v138, 16, v245
	v_and_b32_e32 v139, 0xffff0000, v245
	v_add_f32_e32 v178, v178, v248
	v_add_f32_e32 v179, v179, v248
	v_add_f32_e32 v180, v180, v248
	v_add_f32_e32 v181, v181, v248
	v_add_f32_e32 v182, v182, v248
	v_add_f32_e32 v183, v183, v248
	v_add_f32_e32 v184, v184, v248
	v_add_f32_e32 v185, v185, v248
	v_add_f32_e32 v124, v132, v178
	v_add_f32_e32 v125, v133, v179
	v_add_f32_e32 v126, v134, v180
	v_add_f32_e32 v127, v135, v181
	v_add_f32_e32 v128, v136, v182
	v_add_f32_e32 v129, v137, v183
	v_add_f32_e32 v130, v138, v184
	v_add_f32_e32 v131, v139, v185
	v_mul_f32_e32 v16, v124, v124
	v_fmac_f32_e32 v16, v125, v125
	v_fmac_f32_e32 v16, v126, v126
	v_fmac_f32_e32 v16, v127, v127
	v_fmac_f32_e32 v16, v128, v128
	v_fmac_f32_e32 v16, v129, v129
	v_fmac_f32_e32 v16, v130, v130
	v_fmac_f32_e32 v16, v131, v131
	s_nop 1
	v_add_f32_dpp v17, v16, v16 quad_perm:[1,0,3,2] row_mask:0xf bank_mask:0xf
	s_nop 1
	v_add_f32_dpp v16, v17, v17 quad_perm:[2,3,0,1] row_mask:0xf bank_mask:0xf
	s_nop 1
	v_add_f32_dpp v17, v16, v16 row_half_mirror row_mask:0xf bank_mask:0xf
	s_nop 1
	v_add_f32_dpp v16, v17, v17 row_ror:8 row_mask:0xf bank_mask:0xf
	v_mov_b32_e32 v17, v16
	s_nop 1
	v_permlane16_swap_b32_e32 v16, v17
	v_add_f32_e32 v16, v16, v17
	v_mov_b32_e32 v17, v16
	s_nop 1
	v_permlane32_swap_b32_e32 v16, v17
	v_add_f32_e32 v16, v16, v17
	global_store_dwordx4 v[20:21], v[124:127], off
	global_store_dwordx4 v[20:21], v[128:131], off offset:16
	s_lshl_b32 s30, s16, 7
	s_add_u32 s28, s62, s30
	s_addc_u32 s29, s63, 0
	v_lshlrev_b32_e32 v18, 1, v1
	s_mov_b64 exec, s[2:3]
	global_store_dword v18, v16, s[28:29]
	s_mov_b64 exec, -1
	s_waitcnt lgkmcnt(0)
	s_load_dwordx16 s[84:99], s[38:39], 0x40
	s_lshl_b32 s30, s68, 12
	s_add_u32 s28, s26, s30
	s_addc_u32 s29, s27, 0
	global_load_dwordx2 v[24:25], v162, s[28:29]
	s_lshl_b32 s30, s69, 12
	s_add_u32 s28, s26, s30
	s_addc_u32 s29, s27, 0
	global_load_dwordx2 v[26:27], v162, s[28:29]
	s_lshl_b32 s30, s70, 12
	s_add_u32 s28, s26, s30
	s_addc_u32 s29, s27, 0
	global_load_dwordx2 v[28:29], v162, s[28:29]
	s_lshl_b32 s30, s71, 12
	s_add_u32 s28, s26, s30
	s_addc_u32 s29, s27, 0
	global_load_dwordx2 v[30:31], v162, s[28:29]
	s_lshl_b32 s30, s72, 12
	s_add_u32 s28, s26, s30
	s_addc_u32 s29, s27, 0
	global_load_dwordx2 v[32:33], v162, s[28:29]
	s_lshl_b32 s30, s73, 12
	s_add_u32 s28, s26, s30
	s_addc_u32 s29, s27, 0
	global_load_dwordx2 v[34:35], v162, s[28:29]
	s_lshl_b32 s30, s74, 12
	s_add_u32 s28, s26, s30
	s_addc_u32 s29, s27, 0
	global_load_dwordx2 v[36:37], v162, s[28:29]
	s_lshl_b32 s30, s75, 12
	s_add_u32 s28, s26, s30
	s_addc_u32 s29, s27, 0
	global_load_dwordx2 v[38:39], v162, s[28:29]
	s_lshl_b32 s30, s76, 12
	s_add_u32 s28, s26, s30
	s_addc_u32 s29, s27, 0
	global_load_dwordx2 v[40:41], v162, s[28:29]
	s_lshl_b32 s30, s77, 12
	s_add_u32 s28, s26, s30
	s_addc_u32 s29, s27, 0
	global_load_dwordx2 v[42:43], v162, s[28:29]
	s_lshl_b32 s30, s78, 12
	s_add_u32 s28, s26, s30
	s_addc_u32 s29, s27, 0
	global_load_dwordx2 v[44:45], v162, s[28:29]
	s_lshl_b32 s30, s79, 12
	s_add_u32 s28, s26, s30
	s_addc_u32 s29, s27, 0
	global_load_dwordx2 v[46:47], v162, s[28:29]
	s_lshl_b32 s30, s80, 12
	s_add_u32 s28, s26, s30
	s_addc_u32 s29, s27, 0
	global_load_dwordx2 v[48:49], v162, s[28:29]
	s_lshl_b32 s30, s81, 12
	s_add_u32 s28, s26, s30
	s_addc_u32 s29, s27, 0
	global_load_dwordx2 v[50:51], v162, s[28:29]
	s_lshl_b32 s30, s82, 12
	s_add_u32 s28, s26, s30
	s_addc_u32 s29, s27, 0
	global_load_dwordx2 v[52:53], v162, s[28:29]
	s_lshl_b32 s30, s83, 12
	s_add_u32 s28, s26, s30
	s_addc_u32 s29, s27, 0
	global_load_dwordx2 v[54:55], v162, s[28:29]
	s_waitcnt lgkmcnt(0)
	s_load_dwordx16 s[68:83], s[38:39], 0x80
	s_lshl_b32 s30, s84, 12
	s_add_u32 s28, s26, s30
	s_addc_u32 s29, s27, 0
	global_load_dwordx2 v[56:57], v162, s[28:29]
	s_lshl_b32 s30, s85, 12
	s_add_u32 s28, s26, s30
	s_addc_u32 s29, s27, 0
	global_load_dwordx2 v[58:59], v162, s[28:29]
	s_lshl_b32 s30, s86, 12
	s_add_u32 s28, s26, s30
	s_addc_u32 s29, s27, 0
	global_load_dwordx2 v[60:61], v162, s[28:29]
	s_lshl_b32 s30, s87, 12
	s_add_u32 s28, s26, s30
	s_addc_u32 s29, s27, 0
	global_load_dwordx2 v[62:63], v162, s[28:29]
	s_lshl_b32 s30, s88, 12
	s_add_u32 s28, s26, s30
	s_addc_u32 s29, s27, 0
	global_load_dwordx2 v[64:65], v162, s[28:29]
	s_lshl_b32 s30, s89, 12
	s_add_u32 s28, s26, s30
	s_addc_u32 s29, s27, 0
	global_load_dwordx2 v[66:67], v162, s[28:29]
	s_lshl_b32 s30, s90, 12
	s_add_u32 s28, s26, s30
	s_addc_u32 s29, s27, 0
	global_load_dwordx2 v[68:69], v162, s[28:29]
	s_lshl_b32 s30, s91, 12
	s_add_u32 s28, s26, s30
	s_addc_u32 s29, s27, 0
	global_load_dwordx2 v[70:71], v162, s[28:29]
	s_lshl_b32 s30, s92, 12
	s_add_u32 s28, s26, s30
	s_addc_u32 s29, s27, 0
	global_load_dwordx2 v[72:73], v162, s[28:29]
	s_lshl_b32 s30, s93, 12
	s_add_u32 s28, s26, s30
	s_addc_u32 s29, s27, 0
	global_load_dwordx2 v[74:75], v162, s[28:29]
	s_lshl_b32 s30, s94, 12
	s_add_u32 s28, s26, s30
	s_addc_u32 s29, s27, 0
	global_load_dwordx2 v[76:77], v162, s[28:29]
	s_lshl_b32 s30, s95, 12
	s_add_u32 s28, s26, s30
	s_addc_u32 s29, s27, 0
	global_load_dwordx2 v[78:79], v162, s[28:29]
	s_lshl_b32 s30, s96, 12
	s_add_u32 s28, s26, s30
	s_addc_u32 s29, s27, 0
	global_load_dwordx2 v[80:81], v162, s[28:29]
	s_lshl_b32 s30, s97, 12
	s_add_u32 s28, s26, s30
	s_addc_u32 s29, s27, 0
	global_load_dwordx2 v[82:83], v162, s[28:29]
	s_lshl_b32 s30, s98, 12
	s_add_u32 s28, s26, s30
	s_addc_u32 s29, s27, 0
	global_load_dwordx2 v[84:85], v162, s[28:29]
	s_lshl_b32 s30, s99, 12
	s_add_u32 s28, s26, s30
	s_addc_u32 s29, s27, 0
	global_load_dwordx2 v[86:87], v162, s[28:29]
	s_add_i32 s16, s16, 1
	s_cmp_lt_i32 s16, s17
	s_cbranch_scc1 .Lpb_tok
	s_waitcnt vmcnt(0)
	s_waitcnt vmcnt(0)
	v_cmp_eq_u32_e32 vcc, 0, v0
	s_waitcnt vmcnt(0) lgkmcnt(0)
	s_barrier
	s_and_saveexec_b64 s[2:3], vcc
	s_cbranch_execz .Lgbc_1444
	v_readlane_b32 s4, v237, 5
	s_waitcnt vmcnt(0) expcnt(0) lgkmcnt(0)
	s_nop 0
	v_mov_b32_e32 v1, s4
	ds_read_b32 v3, v1
	ds_read_b32 v1, v1 offset:4
	s_waitcnt lgkmcnt(1)
	v_cmp_ne_u32_e32 vcc, 0, v3
	s_branch .Lgbc_1412
	v_readlane_b32 s4, v237, 2
	v_readlane_b32 s5, v237, 3
	s_load_dwordx2 s[8:9], s[6:7], 0x4
	s_lshl_b64 s[4:5], s[4:5], 2
	v_readlane_b32 s6, v237, 0
	s_add_u32 s4, s6, s4
	v_readlane_b32 s6, v237, 1
	s_addc_u32 s5, s6, s5
	s_add_u32 s6, s4, 0x1000
	s_addc_u32 s7, s5, 0
	s_waitcnt lgkmcnt(0)
	s_mul_i32 s20, s8, s38
	s_add_u32 s8, s4, 0x1100
	s_mul_i32 s20, s20, s9
	s_addc_u32 s9, s5, 0
	s_add_u32 s10, s4, 0x1200
	s_addc_u32 s11, s5, 0
	s_add_u32 s12, s4, 0x1300
	s_addc_u32 s13, s5, 0
	s_mov_b32 s21, 1
	v_mov_b32_e32 v17, 0
	s_branch .Lgbc_1400
